# redundant setprio pairs and post-barrier lgkmcnt(0) removed; all s_setprio dropped from GEMM K-loops
# speedup vs baseline: 1.0098x; 1.0032x over previous
; #define PG8_STAGE(bufoff, gbase, voff) do { _Pragma("unroll") for (int _i = 0; _i < 2; ++_i) \
;         __builtin_amdgcn_global_load_lds((const unsigned*)((const char*)(gbase) + (voff)[_i]), (PG8_LAS unsigned*)(lds + (bufoff) + ldsw + _i * 8192), 16, 0, 0); } while (0)
; #define PG8_LDA(dst, b, h) do { _Pragma("unroll") for (int m = 0; m < 4; ++m) _Pragma("unroll") for (int k = 0; k < 2; ++k) dst[m][k] = *(const PG8_LAS bf16x8*)(lds + PG8_SA(b, h) + aoff + m * 2048 + k * 1024); } while (0)
; #define PG8_LDB(dst, b, h) do { _Pragma("unroll") for (int n = 0; n < 2; ++n) _Pragma("unroll") for (int k = 0; k < 2; ++k) dst[n][k] = *(const PG8_LAS bf16x8*)(lds + PG8_SB(b, h) + boff + n * 2048 + k * 1024); } while (0)
; #define PG8_MMA(ai, bj, At, Bt) do { __builtin_amdgcn_s_setprio(1); _Pragma("unroll") for (int m = 0; m < 4; ++m) _Pragma("unroll") for (int n = 0; n < 2; ++n) _Pragma("unroll") for (int k = 0; k < 2; ++k) \
;         acc[ai][bj][m][n] = __builtin_amdgcn_mfma_f32_16x16x32_bf16(Bt[n][k], At[m][k], acc[ai][bj][m][n], 0, 0, 0); __builtin_amdgcn_s_setprio(0); } while (0)
; #define PG8_WAIT_V(n) asm volatile("s_waitcnt vmcnt(" #n ")" ::: "memory")
; #define PG8_BAR __builtin_amdgcn_s_barrier()
; template <class Epi, class Sched, bool ALIGN_EPI = false>
; __device__ __forceinline__ void gemm_phase(PG8_LAS unsigned char* lds, const Gemm g, const Sched& S, const Epi& E) {
;     ...
;         for (int t = 0; t < nt; t += 2) {
;             const bool last = (t == nt - 2);
;             const char* a1 = cA + (size_t)(t + 1) * kstep;
;             const char* a2 = last ? nA : cA + (size_t)(t + 2) * kstep; const char* b2 = last ? nB : cB + (size_t)(t + 2) * kstep;
;             const char* a3 = a2 + kstep; const char* b3 = b2 + kstep;
;             unsigned w0[2], w1[2];
; #pragma unroll
;             for (int i = 0; i < 2; ++i) { w0[i] = (Sched::GATHER && last) ? vn0[i] : vc0[i]; w1[i] = (Sched::GATHER && last) ? vn1[i] : vc1[i]; }
;             if (last && has_next) S.a_ready(nxt);
;             PG8_LDB(B0, 0, 0); PG8_LDB(B1, 0, 1); PG8_SCHED; PG8_LDA(At, 0, 0); PG8_STAGE(PG8_SA(1, 1), a1 + hstepA, vc1);
;             PG8_WAIT_V(8); PG8_WAIT_L(0); PG8_BAR; PG8_MMA(0, 0, At, B0); PG8_MMA(0, 1, At, B1); PG8_BAR; PG8_SCHED;
;             PG8_LDA(At, 0, 1); PG8_STAGE(PG8_SB(0, 0), b2, voffB); PG8_STAGE(PG8_SB(0, 1), b2 + hstep, voffB); PG8_STAGE(PG8_SA(0, 0), a2, w0);
.LBB0_247:
	ds_read_b128 v[132:135], v191
	ds_read_b128 v[136:139], v191 offset:1024
	ds_read_b128 v[140:143], v191 offset:2048
	ds_read_b128 v[144:147], v191 offset:3072
	ds_read_b128 v[148:151], v193
	ds_read_b128 v[152:155], v193 offset:1024
	ds_read_b128 v[156:159], v193 offset:2048
	ds_read_b128 v[196:199], v193 offset:3072
	s_add_u32 s52, s50, 0xfff80080
	s_addc_u32 s53, s51, -1
	s_cmp_eq_u32 s80, 28
	s_cselect_b32 s55, s9, s53
	s_cselect_b32 s54, s76, s52
	s_cselect_b32 s53, s45, s79
	s_cselect_b32 s52, s77, s78
	v_lshl_add_u64 v[160:161], s[50:51], 0, v[172:173]
	s_add_i32 m0, s59, 0xc000
	ds_read_b128 v[204:207], v195
	ds_read_b128 v[210:213], v195 offset:1024
	ds_read_b128 v[214:217], v195 offset:2048
	ds_read_b128 v[218:221], v195 offset:3072
	ds_read_b128 v[222:225], v195 offset:4096
	ds_read_b128 v[226:229], v195 offset:5120
	ds_read_b128 v[230:233], v195 offset:6144
	ds_read_b128 v[234:237], v195 offset:7168
	global_load_lds_dwordx4 v[160:161], off
	v_lshl_add_u64 v[160:161], s[50:51], 0, v[174:175]
	s_add_i32 m0, s59, 0xe000
	s_nop 0
	global_load_lds_dwordx4 v[160:161], off
	s_waitcnt vmcnt(8)
	s_waitcnt lgkmcnt(0)
	s_barrier
	v_mfma_f32_16x16x32_bf16 v[126:129], v[132:135], v[204:207], v[126:129]
	v_mfma_f32_16x16x32_bf16 v[122:125], v[140:143], v[204:207], v[122:125]
	v_mfma_f32_16x16x32_bf16 v[110:113], v[132:135], v[214:217], v[110:113]
	v_mfma_f32_16x16x32_bf16 v[106:109], v[140:143], v[214:217], v[106:109]
	v_mfma_f32_16x16x32_bf16 v[94:97], v[132:135], v[222:225], v[94:97]
	v_mfma_f32_16x16x32_bf16 v[90:93], v[140:143], v[222:225], v[90:93]
	v_mfma_f32_16x16x32_bf16 v[78:81], v[132:135], v[230:233], v[78:81]
	v_mfma_f32_16x16x32_bf16 v[74:77], v[140:143], v[230:233], v[74:77]
	v_mfma_f32_16x16x32_bf16 v[126:129], v[136:139], v[210:213], v[126:129]
	v_mfma_f32_16x16x32_bf16 v[122:125], v[144:147], v[210:213], v[122:125]
	v_mfma_f32_16x16x32_bf16 v[110:113], v[136:139], v[218:221], v[110:113]
	v_mfma_f32_16x16x32_bf16 v[106:109], v[144:147], v[218:221], v[106:109]
	v_mfma_f32_16x16x32_bf16 v[94:97], v[136:139], v[226:229], v[94:97]
	v_mfma_f32_16x16x32_bf16 v[90:93], v[144:147], v[226:229], v[90:93]
	v_mfma_f32_16x16x32_bf16 v[78:81], v[136:139], v[234:237], v[78:81]
	v_mfma_f32_16x16x32_bf16 v[74:77], v[144:147], v[234:237], v[74:77]
	v_mfma_f32_16x16x32_bf16 v[118:121], v[148:151], v[204:207], v[118:121]
	v_mfma_f32_16x16x32_bf16 v[114:117], v[156:159], v[204:207], v[114:117]
	v_mfma_f32_16x16x32_bf16 v[102:105], v[148:151], v[214:217], v[102:105]
	v_mfma_f32_16x16x32_bf16 v[98:101], v[156:159], v[214:217], v[98:101]
	v_mfma_f32_16x16x32_bf16 v[86:89], v[148:151], v[222:225], v[86:89]
	v_mfma_f32_16x16x32_bf16 v[82:85], v[156:159], v[222:225], v[82:85]
	v_mfma_f32_16x16x32_bf16 v[70:73], v[148:151], v[230:233], v[70:73]
	v_mfma_f32_16x16x32_bf16 v[66:69], v[156:159], v[230:233], v[66:69]
	v_mfma_f32_16x16x32_bf16 v[118:121], v[152:155], v[210:213], v[118:121]
	v_mfma_f32_16x16x32_bf16 v[114:117], v[196:199], v[210:213], v[114:117]
	v_mfma_f32_16x16x32_bf16 v[102:105], v[152:155], v[218:221], v[102:105]
	v_mfma_f32_16x16x32_bf16 v[98:101], v[196:199], v[218:221], v[98:101]
	v_mfma_f32_16x16x32_bf16 v[86:89], v[152:155], v[226:229], v[86:89]
	v_mfma_f32_16x16x32_bf16 v[82:85], v[196:199], v[226:229], v[82:85]
	v_mfma_f32_16x16x32_bf16 v[70:73], v[152:155], v[234:237], v[70:73]
	v_mfma_f32_16x16x32_bf16 v[66:69], v[196:199], v[234:237], v[66:69]
	s_barrier
	s_add_i32 s81, s67, s57
	v_lshl_add_u64 v[160:161], s[52:53], 0, v[164:165]
	s_mov_b32 m0, s81
	ds_read_b128 v[204:207], v195 offset:16384
	ds_read_b128 v[210:213], v195 offset:17408
	ds_read_b128 v[214:217], v195 offset:18432
	ds_read_b128 v[218:221], v195 offset:19456
	ds_read_b128 v[222:225], v195 offset:20480
	ds_read_b128 v[226:229], v195 offset:21504
	ds_read_b128 v[230:233], v195 offset:22528
	ds_read_b128 v[234:237], v195 offset:23552
	global_load_lds_dwordx4 v[160:161], off
	s_add_i32 m0, s81, 0x2000
	s_add_u32 s82, s52, 0x80000
	v_lshl_add_u64 v[200:201], s[52:53], 0, v[168:169]
	s_addc_u32 s83, s53, 0
	s_add_i32 s81, s68, s57
	global_load_lds_dwordx4 v[200:201], off
	v_lshl_add_u64 v[238:239], s[82:83], 0, v[164:165]
	s_mov_b32 m0, s81
	v_lshl_add_u64 v[240:241], s[54:55], 0, v[166:167]
	global_load_lds_dwordx4 v[238:239], off
	v_lshl_add_u64 v[238:239], s[82:83], 0, v[168:169]
	s_add_i32 m0, s81, 0x2000
	s_nop 0
	global_load_lds_dwordx4 v[238:239], off
	v_lshl_add_u64 v[238:239], s[54:55], 0, v[162:163]
	s_mov_b32 m0, s59
	s_nop 0
	global_load_lds_dwordx4 v[238:239], off
	s_mov_b32 m0, s60
	s_nop 0
	global_load_lds_dwordx4 v[240:241], off
	s_waitcnt vmcnt(8)
	s_waitcnt lgkmcnt(0)
	s_barrier
; #define PG8_STAGE(bufoff, gbase, voff) do { _Pragma("unroll") for (int _i = 0; _i < 2; ++_i) \
;         __builtin_amdgcn_global_load_lds((const unsigned*)((const char*)(gbase) + (voff)[_i]), (PG8_LAS unsigned*)(lds + (bufoff) + ldsw + _i * 8192), 16, 0, 0); } while (0)
; #define PG8_LDA(dst, b, h) do { _Pragma("unroll") for (int m = 0; m < 4; ++m) _Pragma("unroll") for (int k = 0; k < 2; ++k) dst[m][k] = *(const PG8_LAS bf16x8*)(lds + PG8_SA(b, h) + aoff + m * 2048 + k * 1024); } while (0)
; #define PG8_LDB(dst, b, h) do { _Pragma("unroll") for (int n = 0; n < 2; ++n) _Pragma("unroll") for (int k = 0; k < 2; ++k) dst[n][k] = *(const PG8_LAS bf16x8*)(lds + PG8_SB(b, h) + boff + n * 2048 + k * 1024); } while (0)
; #define PG8_MMA(ai, bj, At, Bt) do { __builtin_amdgcn_s_setprio(1); _Pragma("unroll") for (int m = 0; m < 4; ++m) _Pragma("unroll") for (int n = 0; n < 2; ++n) _Pragma("unroll") for (int k = 0; k < 2; ++k) \
;         acc[ai][bj][m][n] = __builtin_amdgcn_mfma_f32_16x16x32_bf16(Bt[n][k], At[m][k], acc[ai][bj][m][n], 0, 0, 0); __builtin_amdgcn_s_setprio(0); } while (0)
; #define PG8_WAIT_V(n) asm volatile("s_waitcnt vmcnt(" #n ")" ::: "memory")
; #define PG8_WAIT_L(n) asm volatile("s_waitcnt lgkmcnt(" #n ")" ::: "memory")
; #define PG8_BAR __builtin_amdgcn_s_barrier()
; #define PG8_SCHED __builtin_amdgcn_sched_barrier(0)
; template <class Epi, class Sched, bool ALIGN_EPI = false>
; __device__ __forceinline__ void gemm_phase(PG8_LAS unsigned char* lds, const Gemm g, const Sched& S, const Epi& E) {
;     ...
;             PG8_WAIT_V(8); PG8_WAIT_L(0); PG8_BAR; PG8_MMA(1, 0, At, B0); PG8_MMA(1, 1, At, B1); PG8_BAR; PG8_SCHED;
;             PG8_LDB(B0, 1, 0); PG8_LDB(B1, 1, 1); PG8_SCHED; PG8_LDA(At, 1, 0); PG8_STAGE(PG8_SA(0, 1), a2 + hstepA, w1);
;             PG8_WAIT_V(8); PG8_WAIT_L(0); PG8_BAR; PG8_MMA(0, 0, At, B0); PG8_MMA(0, 1, At, B1); PG8_BAR; PG8_SCHED;
	v_mfma_f32_16x16x32_bf16 v[54:57], v[132:135], v[204:207], v[54:57]
	v_mfma_f32_16x16x32_bf16 v[50:53], v[140:143], v[204:207], v[50:53]
	v_mfma_f32_16x16x32_bf16 v[38:41], v[132:135], v[214:217], v[38:41]
	v_mfma_f32_16x16x32_bf16 v[34:37], v[140:143], v[214:217], v[34:37]
	v_mfma_f32_16x16x32_bf16 v[22:25], v[132:135], v[222:225], v[22:25]
	v_mfma_f32_16x16x32_bf16 v[18:21], v[140:143], v[222:225], v[18:21]
	v_mfma_f32_16x16x32_bf16 v[6:9], v[132:135], v[230:233], v[6:9]
	v_mfma_f32_16x16x32_bf16 v[2:5], v[140:143], v[230:233], v[2:5]
	v_mfma_f32_16x16x32_bf16 v[54:57], v[136:139], v[210:213], v[54:57]
	v_mfma_f32_16x16x32_bf16 v[50:53], v[144:147], v[210:213], v[50:53]
	v_mfma_f32_16x16x32_bf16 v[38:41], v[136:139], v[218:221], v[38:41]
	v_mfma_f32_16x16x32_bf16 v[34:37], v[144:147], v[218:221], v[34:37]
	v_mfma_f32_16x16x32_bf16 v[22:25], v[136:139], v[226:229], v[22:25]
	v_mfma_f32_16x16x32_bf16 v[18:21], v[144:147], v[226:229], v[18:21]
	v_mfma_f32_16x16x32_bf16 v[6:9], v[136:139], v[234:237], v[6:9]
	v_mfma_f32_16x16x32_bf16 v[2:5], v[144:147], v[234:237], v[2:5]
	v_mfma_f32_16x16x32_bf16 v[58:61], v[148:151], v[204:207], v[58:61]
	v_mfma_f32_16x16x32_bf16 v[62:65], v[156:159], v[204:207], v[62:65]
	v_mfma_f32_16x16x32_bf16 v[42:45], v[148:151], v[214:217], v[42:45]
	v_mfma_f32_16x16x32_bf16 v[46:49], v[156:159], v[214:217], v[46:49]
	v_mfma_f32_16x16x32_bf16 v[26:29], v[148:151], v[222:225], v[26:29]
	v_mfma_f32_16x16x32_bf16 v[30:33], v[156:159], v[222:225], v[30:33]
	v_mfma_f32_16x16x32_bf16 v[10:13], v[148:151], v[230:233], v[10:13]
	v_mfma_f32_16x16x32_bf16 v[14:17], v[156:159], v[230:233], v[14:17]
	v_mfma_f32_16x16x32_bf16 v[58:61], v[152:155], v[210:213], v[58:61]
	v_mfma_f32_16x16x32_bf16 v[62:65], v[196:199], v[210:213], v[62:65]
	v_mfma_f32_16x16x32_bf16 v[42:45], v[152:155], v[218:221], v[42:45]
	v_mfma_f32_16x16x32_bf16 v[46:49], v[196:199], v[218:221], v[46:49]
	v_mfma_f32_16x16x32_bf16 v[26:29], v[152:155], v[226:229], v[26:29]
	v_mfma_f32_16x16x32_bf16 v[30:33], v[196:199], v[226:229], v[30:33]
	v_mfma_f32_16x16x32_bf16 v[10:13], v[152:155], v[234:237], v[10:13]
	v_mfma_f32_16x16x32_bf16 v[14:17], v[196:199], v[234:237], v[14:17]
	s_barrier
	s_add_i32 s81, 0, 0x18000
	v_add_u32_e32 v131, s81, v181
	s_add_i32 s82, 0, 0x1c000
	ds_read_b128 v[132:135], v131
	ds_read_b128 v[136:139], v131 offset:1024
	ds_read_b128 v[140:143], v131 offset:2048
	ds_read_b128 v[144:147], v131 offset:3072
	v_add_u32_e32 v131, s82, v181
	ds_read_b128 v[148:151], v131
	ds_read_b128 v[152:155], v131 offset:1024
	ds_read_b128 v[156:159], v131 offset:2048
	ds_read_b128 v[196:199], v131 offset:3072
	s_add_u32 s54, s54, 0x80000
	s_addc_u32 s55, s55, 0
	s_mov_b32 m0, s61
	v_lshl_add_u64 v[242:243], s[54:55], 0, v[162:163]
	ds_read_b128 v[204:207], v195 offset:32768
	ds_read_b128 v[210:213], v195 offset:33792
	ds_read_b128 v[214:217], v195 offset:34816
	ds_read_b128 v[218:221], v195 offset:35840
	ds_read_b128 v[222:225], v195 offset:36864
	ds_read_b128 v[226:229], v195 offset:37888
	ds_read_b128 v[230:233], v195 offset:38912
	ds_read_b128 v[234:237], v195 offset:39936
	global_load_lds_dwordx4 v[242:243], off
	v_lshl_add_u64 v[242:243], s[54:55], 0, v[166:167]
	s_mov_b32 m0, s62
	s_nop 0
	global_load_lds_dwordx4 v[242:243], off
	s_waitcnt vmcnt(8)
	s_waitcnt lgkmcnt(0)
	s_barrier
	v_mfma_f32_16x16x32_bf16 v[126:129], v[132:135], v[204:207], v[126:129]
	v_mfma_f32_16x16x32_bf16 v[122:125], v[140:143], v[204:207], v[122:125]
	v_mfma_f32_16x16x32_bf16 v[110:113], v[132:135], v[214:217], v[110:113]
	v_mfma_f32_16x16x32_bf16 v[106:109], v[140:143], v[214:217], v[106:109]
	v_mfma_f32_16x16x32_bf16 v[94:97], v[132:135], v[222:225], v[94:97]
	v_mfma_f32_16x16x32_bf16 v[90:93], v[140:143], v[222:225], v[90:93]
	v_mfma_f32_16x16x32_bf16 v[78:81], v[132:135], v[230:233], v[78:81]
	v_mfma_f32_16x16x32_bf16 v[74:77], v[140:143], v[230:233], v[74:77]
	v_mfma_f32_16x16x32_bf16 v[126:129], v[136:139], v[210:213], v[126:129]
	v_mfma_f32_16x16x32_bf16 v[122:125], v[144:147], v[210:213], v[122:125]
	v_mfma_f32_16x16x32_bf16 v[110:113], v[136:139], v[218:221], v[110:113]
	v_mfma_f32_16x16x32_bf16 v[106:109], v[144:147], v[218:221], v[106:109]
	v_mfma_f32_16x16x32_bf16 v[94:97], v[136:139], v[226:229], v[94:97]
	v_mfma_f32_16x16x32_bf16 v[90:93], v[144:147], v[226:229], v[90:93]
	v_mfma_f32_16x16x32_bf16 v[78:81], v[136:139], v[234:237], v[78:81]
	v_mfma_f32_16x16x32_bf16 v[74:77], v[144:147], v[234:237], v[74:77]
	v_mfma_f32_16x16x32_bf16 v[118:121], v[148:151], v[204:207], v[118:121]
	v_mfma_f32_16x16x32_bf16 v[114:117], v[156:159], v[204:207], v[114:117]
	v_mfma_f32_16x16x32_bf16 v[102:105], v[148:151], v[214:217], v[102:105]
	v_mfma_f32_16x16x32_bf16 v[98:101], v[156:159], v[214:217], v[98:101]
	v_mfma_f32_16x16x32_bf16 v[86:89], v[148:151], v[222:225], v[86:89]
	v_mfma_f32_16x16x32_bf16 v[82:85], v[156:159], v[222:225], v[82:85]
	v_mfma_f32_16x16x32_bf16 v[70:73], v[148:151], v[230:233], v[70:73]
	v_mfma_f32_16x16x32_bf16 v[66:69], v[156:159], v[230:233], v[66:69]
	v_mfma_f32_16x16x32_bf16 v[118:121], v[152:155], v[210:213], v[118:121]
	v_mfma_f32_16x16x32_bf16 v[114:117], v[196:199], v[210:213], v[114:117]
	v_mfma_f32_16x16x32_bf16 v[102:105], v[152:155], v[218:221], v[102:105]
	v_mfma_f32_16x16x32_bf16 v[98:101], v[196:199], v[218:221], v[98:101]
	v_mfma_f32_16x16x32_bf16 v[86:89], v[152:155], v[226:229], v[86:89]
	v_mfma_f32_16x16x32_bf16 v[82:85], v[196:199], v[226:229], v[82:85]
	v_mfma_f32_16x16x32_bf16 v[70:73], v[152:155], v[234:237], v[70:73]
	v_mfma_f32_16x16x32_bf16 v[66:69], v[196:199], v[234:237], v[66:69]
	s_barrier
; #define PG8_STAGE(bufoff, gbase, voff) do { _Pragma("unroll") for (int _i = 0; _i < 2; ++_i) \
;         __builtin_amdgcn_global_load_lds((const unsigned*)((const char*)(gbase) + (voff)[_i]), (PG8_LAS unsigned*)(lds + (bufoff) + ldsw + _i * 8192), 16, 0, 0); } while (0)
; #define PG8_LDA(dst, b, h) do { _Pragma("unroll") for (int m = 0; m < 4; ++m) _Pragma("unroll") for (int k = 0; k < 2; ++k) dst[m][k] = *(const PG8_LAS bf16x8*)(lds + PG8_SA(b, h) + aoff + m * 2048 + k * 1024); } while (0)
; #define PG8_MMA(ai, bj, At, Bt) do { __builtin_amdgcn_s_setprio(1); _Pragma("unroll") for (int m = 0; m < 4; ++m) _Pragma("unroll") for (int n = 0; n < 2; ++n) _Pragma("unroll") for (int k = 0; k < 2; ++k) \
;         acc[ai][bj][m][n] = __builtin_amdgcn_mfma_f32_16x16x32_bf16(Bt[n][k], At[m][k], acc[ai][bj][m][n], 0, 0, 0); __builtin_amdgcn_s_setprio(0); } while (0)
; #define PG8_WAIT_V(n) asm volatile("s_waitcnt vmcnt(" #n ")" ::: "memory")
; #define PG8_WAIT_L(n) asm volatile("s_waitcnt lgkmcnt(" #n ")" ::: "memory")
; #define PG8_BAR __builtin_amdgcn_s_barrier()
; #define PG8_SCHED __builtin_amdgcn_sched_barrier(0)
; template <class Epi, class Sched, bool ALIGN_EPI = false>
; __device__ __forceinline__ void gemm_phase(PG8_LAS unsigned char* lds, const Gemm g, const Sched& S, const Epi& E) {
;     ...
;             PG8_LDA(At, 1, 1); PG8_STAGE(PG8_SB(1, 0), b3, voffB); PG8_STAGE(PG8_SB(1, 1), b3 + hstep, voffB); PG8_STAGE(PG8_SA(1, 0), a3, w0);
;             PG8_WAIT_V(8); PG8_WAIT_L(0); PG8_BAR; PG8_MMA(1, 0, At, B0); PG8_MMA(1, 1, At, B1); PG8_BAR; PG8_SCHED;
;             if constexpr (Epi::KSCALE) { if (((t + 2) & 7) == 0 && t + 2 < nt) { E.kscale(acc, pf, ((t + 2) >> 3) - 1, wr, fr); PG8_SCHED; } }
;         }
	s_add_i32 s54, s81, s57
	v_lshl_add_u64 v[160:161], v[160:161], 0, s[20:21]
	s_mov_b32 m0, s54
	ds_read_b128 v[204:207], v195 offset:49152
	ds_read_b128 v[210:213], v195 offset:50176
	ds_read_b128 v[214:217], v195 offset:51200
	ds_read_b128 v[218:221], v195 offset:52224
	ds_read_b128 v[222:225], v195 offset:53248
	ds_read_b128 v[226:229], v195 offset:54272
	ds_read_b128 v[230:233], v195 offset:55296
	ds_read_b128 v[234:237], v195 offset:56320
	global_load_lds_dwordx4 v[160:161], off
	s_add_i32 m0, s54, 0x2000
	s_add_u32 s52, s52, 0x80080
	v_lshl_add_u64 v[160:161], v[200:201], 0, s[20:21]
	s_addc_u32 s53, s53, 0
	s_add_i32 s54, s82, s57
	global_load_lds_dwordx4 v[160:161], off
	v_lshl_add_u64 v[160:161], s[52:53], 0, v[164:165]
	s_mov_b32 m0, s54
	s_nop 0
	global_load_lds_dwordx4 v[160:161], off
	v_lshl_add_u64 v[160:161], s[52:53], 0, v[168:169]
	s_add_i32 m0, s54, 0x2000
	s_nop 0
	global_load_lds_dwordx4 v[160:161], off
	v_lshl_add_u64 v[160:161], v[238:239], 0, s[20:21]
	s_mov_b32 m0, s65
	s_nop 0
	global_load_lds_dwordx4 v[160:161], off
	v_lshl_add_u64 v[160:161], v[240:241], 0, s[20:21]
	s_mov_b32 m0, s66
	s_nop 0
	global_load_lds_dwordx4 v[160:161], off
	s_waitcnt vmcnt(8)
	s_waitcnt lgkmcnt(0)
	s_barrier
	v_mfma_f32_16x16x32_bf16 v[54:57], v[132:135], v[204:207], v[54:57]
	v_mfma_f32_16x16x32_bf16 v[50:53], v[140:143], v[204:207], v[50:53]
	v_mfma_f32_16x16x32_bf16 v[38:41], v[132:135], v[214:217], v[38:41]
	v_mfma_f32_16x16x32_bf16 v[34:37], v[140:143], v[214:217], v[34:37]
	v_mfma_f32_16x16x32_bf16 v[22:25], v[132:135], v[222:225], v[22:25]
	v_mfma_f32_16x16x32_bf16 v[18:21], v[140:143], v[222:225], v[18:21]
	v_mfma_f32_16x16x32_bf16 v[6:9], v[132:135], v[230:233], v[6:9]
	v_mfma_f32_16x16x32_bf16 v[2:5], v[140:143], v[230:233], v[2:5]
	v_mfma_f32_16x16x32_bf16 v[54:57], v[136:139], v[210:213], v[54:57]
	v_mfma_f32_16x16x32_bf16 v[50:53], v[144:147], v[210:213], v[50:53]
	v_mfma_f32_16x16x32_bf16 v[38:41], v[136:139], v[218:221], v[38:41]
	v_mfma_f32_16x16x32_bf16 v[34:37], v[144:147], v[218:221], v[34:37]
	v_mfma_f32_16x16x32_bf16 v[22:25], v[136:139], v[226:229], v[22:25]
	v_mfma_f32_16x16x32_bf16 v[18:21], v[144:147], v[226:229], v[18:21]
	v_mfma_f32_16x16x32_bf16 v[6:9], v[136:139], v[234:237], v[6:9]
	v_mfma_f32_16x16x32_bf16 v[2:5], v[144:147], v[234:237], v[2:5]
	v_mfma_f32_16x16x32_bf16 v[58:61], v[148:151], v[204:207], v[58:61]
	v_mfma_f32_16x16x32_bf16 v[62:65], v[156:159], v[204:207], v[62:65]
	v_mfma_f32_16x16x32_bf16 v[42:45], v[148:151], v[214:217], v[42:45]
	v_mfma_f32_16x16x32_bf16 v[46:49], v[156:159], v[214:217], v[46:49]
	v_mfma_f32_16x16x32_bf16 v[26:29], v[148:151], v[222:225], v[26:29]
	v_mfma_f32_16x16x32_bf16 v[30:33], v[156:159], v[222:225], v[30:33]
	v_mfma_f32_16x16x32_bf16 v[10:13], v[148:151], v[230:233], v[10:13]
	v_mfma_f32_16x16x32_bf16 v[14:17], v[156:159], v[230:233], v[14:17]
	v_mfma_f32_16x16x32_bf16 v[58:61], v[152:155], v[210:213], v[58:61]
	v_mfma_f32_16x16x32_bf16 v[62:65], v[196:199], v[210:213], v[62:65]
	v_mfma_f32_16x16x32_bf16 v[42:45], v[152:155], v[218:221], v[42:45]
	v_mfma_f32_16x16x32_bf16 v[46:49], v[196:199], v[218:221], v[46:49]
	v_mfma_f32_16x16x32_bf16 v[26:29], v[152:155], v[226:229], v[26:29]
	v_mfma_f32_16x16x32_bf16 v[30:33], v[196:199], v[226:229], v[30:33]
	v_mfma_f32_16x16x32_bf16 v[10:13], v[152:155], v[234:237], v[10:13]
	v_mfma_f32_16x16x32_bf16 v[14:17], v[196:199], v[234:237], v[14:17]
	s_barrier
	s_add_i32 s80, s80, 2
	s_add_u32 s50, s50, 0x100
	s_addc_u32 s51, s51, 0
	s_add_u32 s78, s78, 0x100
	s_addc_u32 s79, s79, 0
	s_cmp_gt_u32 s80, 29
	s_cbranch_scc0 .LBB0_247
	s_and_b64 vcc, exec, s[22:23]
	s_cbranch_vccz .LBB0_250
	s_barrier

; #define PG8_STAGE(bufoff, gbase, voff) do { _Pragma("unroll") for (int _i = 0; _i < 2; ++_i) \
;         __builtin_amdgcn_global_load_lds((const unsigned*)((const char*)(gbase) + (voff)[_i]), (PG8_LAS unsigned*)(lds + (bufoff) + ldsw + _i * 8192), 16, 0, 0); } while (0)
; #define PG8_LDA(dst, b, h) do { _Pragma("unroll") for (int m = 0; m < 4; ++m) _Pragma("unroll") for (int k = 0; k < 2; ++k) dst[m][k] = *(const PG8_LAS bf16x8*)(lds + PG8_SA(b, h) + aoff + m * 2048 + k * 1024); } while (0)
; #define PG8_LDB(dst, b, h) do { _Pragma("unroll") for (int n = 0; n < 2; ++n) _Pragma("unroll") for (int k = 0; k < 2; ++k) dst[n][k] = *(const PG8_LAS bf16x8*)(lds + PG8_SB(b, h) + boff + n * 2048 + k * 1024); } while (0)
; #define PG8_MMA(ai, bj, At, Bt) do { __builtin_amdgcn_s_setprio(1); _Pragma("unroll") for (int m = 0; m < 4; ++m) _Pragma("unroll") for (int n = 0; n < 2; ++n) _Pragma("unroll") for (int k = 0; k < 2; ++k) \
;         acc[ai][bj][m][n] = __builtin_amdgcn_mfma_f32_16x16x32_bf16(Bt[n][k], At[m][k], acc[ai][bj][m][n], 0, 0, 0); __builtin_amdgcn_s_setprio(0); } while (0)
; #define PG8_WAIT_V(n) asm volatile("s_waitcnt vmcnt(" #n ")" ::: "memory")
; #define PG8_BAR __builtin_amdgcn_s_barrier()
; template <class Epi, class Sched, bool ALIGN_EPI = false>
; __device__ __forceinline__ void gemm_phase(PG8_LAS unsigned char* lds, const Gemm g, const Sched& S, const Epi& E) {
;     ...
;         for (int t = 0; t < nt; t += 2) {
;             const bool last = (t == nt - 2);
;             const char* a1 = cA + (size_t)(t + 1) * kstep;
;             const char* a2 = last ? nA : cA + (size_t)(t + 2) * kstep; const char* b2 = last ? nB : cB + (size_t)(t + 2) * kstep;
;             const char* a3 = a2 + kstep; const char* b3 = b2 + kstep;
;             unsigned w0[2], w1[2];
; #pragma unroll
;             for (int i = 0; i < 2; ++i) { w0[i] = (Sched::GATHER && last) ? vn0[i] : vc0[i]; w1[i] = (Sched::GATHER && last) ? vn1[i] : vc1[i]; }
;             if (last && has_next) S.a_ready(nxt);
;             PG8_LDB(B0, 0, 0); PG8_LDB(B1, 0, 1); PG8_SCHED; PG8_LDA(At, 0, 0); PG8_STAGE(PG8_SA(1, 1), a1 + hstepA, vc1);
;             PG8_WAIT_V(8); PG8_WAIT_L(0); PG8_BAR; PG8_MMA(0, 0, At, B0); PG8_MMA(0, 1, At, B1); PG8_BAR; PG8_SCHED;
;             PG8_LDA(At, 0, 1); PG8_STAGE(PG8_SB(0, 0), b2, voffB); PG8_STAGE(PG8_SB(0, 1), b2 + hstep, voffB); PG8_STAGE(PG8_SA(0, 0), a2, w0);
.LBB0_504:
	v_add_u32_e32 v3, s74, v178
	s_add_u32 s54, s50, s52
	ds_read_b128 v[138:141], v3
	ds_read_b128 v[162:165], v3 offset:1024
	ds_read_b128 v[166:169], v3 offset:2048
	ds_read_b128 v[170:173], v3 offset:3072
	v_add_u32_e32 v3, s75, v178
	s_addc_u32 s55, s51, s53
	ds_read_b128 v[186:189], v3
	s_waitcnt lgkmcnt(0)
	ds_read_b128 v[190:193], v3 offset:1024
	ds_read_b128 v[194:197], v3 offset:2048
	ds_read_b128 v[198:201], v3 offset:3072
	s_add_u32 s54, s54, 0x100
	s_addc_u32 s55, s55, 0
	s_add_u32 s82, s79, s52
	s_addc_u32 s83, s80, s53
	s_cmpk_eq_i32 s52, 0xf00
	s_cselect_b32 s57, s47, s55
	s_cselect_b32 s56, s49, s54
	s_cselect_b32 s55, s45, s83
	s_cselect_b32 s54, s78, s82
	v_lshl_add_u64 v[142:143], v[132:133], 0, s[52:53]
	s_add_i32 m0, s62, 0xc000
	ds_read_b128 v[202:205], v184
	ds_read_b128 v[206:209], v184 offset:1024
	ds_read_b128 v[210:213], v184 offset:2048
	ds_read_b128 v[214:217], v184 offset:3072
	ds_read_b128 v[218:221], v184 offset:4096
	ds_read_b128 v[222:225], v184 offset:5120
	ds_read_b128 v[226:229], v184 offset:6144
	ds_read_b128 v[230:233], v184 offset:7168
	global_load_lds_dwordx4 v[142:143], off
	v_lshl_add_u64 v[142:143], v[134:135], 0, s[52:53]
	s_add_i32 m0, s62, 0xe000
	s_nop 0
	global_load_lds_dwordx4 v[142:143], off
	s_waitcnt vmcnt(8)
	s_waitcnt lgkmcnt(0)
	s_barrier
	v_mfma_f32_16x16x32_bf16 v[128:131], v[138:141], v[202:205], v[128:131]
	v_mfma_f32_16x16x32_bf16 v[124:127], v[166:169], v[202:205], v[124:127]
	v_mfma_f32_16x16x32_bf16 v[120:123], v[138:141], v[210:213], v[120:123]
	v_mfma_f32_16x16x32_bf16 v[112:115], v[166:169], v[210:213], v[112:115]
	v_mfma_f32_16x16x32_bf16 v[96:99], v[138:141], v[218:221], v[96:99]
	v_mfma_f32_16x16x32_bf16 v[92:95], v[166:169], v[218:221], v[92:95]
	v_mfma_f32_16x16x32_bf16 v[80:83], v[138:141], v[226:229], v[80:83]
	v_mfma_f32_16x16x32_bf16 v[76:79], v[166:169], v[226:229], v[76:79]
	v_mfma_f32_16x16x32_bf16 v[128:131], v[162:165], v[206:209], v[128:131]
	v_mfma_f32_16x16x32_bf16 v[124:127], v[170:173], v[206:209], v[124:127]
	v_mfma_f32_16x16x32_bf16 v[120:123], v[162:165], v[214:217], v[120:123]
	v_mfma_f32_16x16x32_bf16 v[112:115], v[170:173], v[214:217], v[112:115]
	v_mfma_f32_16x16x32_bf16 v[96:99], v[162:165], v[222:225], v[96:99]
	v_mfma_f32_16x16x32_bf16 v[92:95], v[170:173], v[222:225], v[92:95]
	v_mfma_f32_16x16x32_bf16 v[80:83], v[162:165], v[230:233], v[80:83]
	v_mfma_f32_16x16x32_bf16 v[76:79], v[170:173], v[230:233], v[76:79]
	v_mfma_f32_16x16x32_bf16 v[116:119], v[186:189], v[202:205], v[116:119]
	v_mfma_f32_16x16x32_bf16 v[108:111], v[194:197], v[202:205], v[108:111]
	v_mfma_f32_16x16x32_bf16 v[104:107], v[186:189], v[210:213], v[104:107]
	v_mfma_f32_16x16x32_bf16 v[100:103], v[194:197], v[210:213], v[100:103]
	v_mfma_f32_16x16x32_bf16 v[88:91], v[186:189], v[218:221], v[88:91]
	v_mfma_f32_16x16x32_bf16 v[84:87], v[194:197], v[218:221], v[84:87]
	v_mfma_f32_16x16x32_bf16 v[72:75], v[186:189], v[226:229], v[72:75]
	v_mfma_f32_16x16x32_bf16 v[68:71], v[194:197], v[226:229], v[68:71]
	v_mfma_f32_16x16x32_bf16 v[116:119], v[190:193], v[206:209], v[116:119]
	v_mfma_f32_16x16x32_bf16 v[108:111], v[198:201], v[206:209], v[108:111]
	v_mfma_f32_16x16x32_bf16 v[104:107], v[190:193], v[214:217], v[104:107]
	v_mfma_f32_16x16x32_bf16 v[100:103], v[198:201], v[214:217], v[100:103]
	v_mfma_f32_16x16x32_bf16 v[88:91], v[190:193], v[222:225], v[88:91]
	v_mfma_f32_16x16x32_bf16 v[84:87], v[198:201], v[222:225], v[84:87]
	v_mfma_f32_16x16x32_bf16 v[72:75], v[190:193], v[230:233], v[72:75]
	v_mfma_f32_16x16x32_bf16 v[68:71], v[198:201], v[230:233], v[68:71]
	s_barrier
	s_add_i32 s82, s74, s61
	v_lshl_add_u64 v[142:143], s[54:55], 0, v[146:147]
	s_mov_b32 m0, s82
	ds_read_b128 v[202:205], v184 offset:16384
	ds_read_b128 v[206:209], v184 offset:17408
	ds_read_b128 v[210:213], v184 offset:18432
	ds_read_b128 v[214:217], v184 offset:19456
	ds_read_b128 v[218:221], v184 offset:20480
	ds_read_b128 v[222:225], v184 offset:21504
	ds_read_b128 v[226:229], v184 offset:22528
	ds_read_b128 v[230:233], v184 offset:23552
	global_load_lds_dwordx4 v[142:143], off
	s_add_i32 m0, s82, 0x2000
	s_add_u32 s82, s54, 0x80000
	v_lshl_add_u64 v[174:175], s[54:55], 0, v[150:151]
	s_addc_u32 s83, s55, 0
	s_add_i32 s84, s75, s61
	global_load_lds_dwordx4 v[174:175], off
	v_lshl_add_u64 v[234:235], s[82:83], 0, v[146:147]
	s_mov_b32 m0, s84
	v_lshl_add_u64 v[236:237], s[56:57], 0, v[148:149]
	global_load_lds_dwordx4 v[234:235], off
	v_lshl_add_u64 v[234:235], s[82:83], 0, v[150:151]
	s_add_i32 m0, s84, 0x2000
	s_nop 0
	global_load_lds_dwordx4 v[234:235], off
	v_lshl_add_u64 v[234:235], s[56:57], 0, v[144:145]
	s_mov_b32 m0, s62
	s_nop 0
	global_load_lds_dwordx4 v[234:235], off
	s_mov_b32 m0, s63
	s_nop 0
	global_load_lds_dwordx4 v[236:237], off
	s_waitcnt vmcnt(8)
	s_waitcnt lgkmcnt(0)
	s_barrier
; #define PG8_STAGE(bufoff, gbase, voff) do { _Pragma("unroll") for (int _i = 0; _i < 2; ++_i) \
;         __builtin_amdgcn_global_load_lds((const unsigned*)((const char*)(gbase) + (voff)[_i]), (PG8_LAS unsigned*)(lds + (bufoff) + ldsw + _i * 8192), 16, 0, 0); } while (0)
; #define PG8_LDA(dst, b, h) do { _Pragma("unroll") for (int m = 0; m < 4; ++m) _Pragma("unroll") for (int k = 0; k < 2; ++k) dst[m][k] = *(const PG8_LAS bf16x8*)(lds + PG8_SA(b, h) + aoff + m * 2048 + k * 1024); } while (0)
; #define PG8_LDB(dst, b, h) do { _Pragma("unroll") for (int n = 0; n < 2; ++n) _Pragma("unroll") for (int k = 0; k < 2; ++k) dst[n][k] = *(const PG8_LAS bf16x8*)(lds + PG8_SB(b, h) + boff + n * 2048 + k * 1024); } while (0)
; #define PG8_MMA(ai, bj, At, Bt) do { __builtin_amdgcn_s_setprio(1); _Pragma("unroll") for (int m = 0; m < 4; ++m) _Pragma("unroll") for (int n = 0; n < 2; ++n) _Pragma("unroll") for (int k = 0; k < 2; ++k) \
;         acc[ai][bj][m][n] = __builtin_amdgcn_mfma_f32_16x16x32_bf16(Bt[n][k], At[m][k], acc[ai][bj][m][n], 0, 0, 0); __builtin_amdgcn_s_setprio(0); } while (0)
; #define PG8_WAIT_V(n) asm volatile("s_waitcnt vmcnt(" #n ")" ::: "memory")
; #define PG8_WAIT_L(n) asm volatile("s_waitcnt lgkmcnt(" #n ")" ::: "memory")
; #define PG8_BAR __builtin_amdgcn_s_barrier()
; #define PG8_SCHED __builtin_amdgcn_sched_barrier(0)
; template <class Epi, class Sched, bool ALIGN_EPI = false>
; __device__ __forceinline__ void gemm_phase(PG8_LAS unsigned char* lds, const Gemm g, const Sched& S, const Epi& E) {
;     ...
;             PG8_WAIT_V(8); PG8_WAIT_L(0); PG8_BAR; PG8_MMA(1, 0, At, B0); PG8_MMA(1, 1, At, B1); PG8_BAR; PG8_SCHED;
;             PG8_LDB(B0, 1, 0); PG8_LDB(B1, 1, 1); PG8_SCHED; PG8_LDA(At, 1, 0); PG8_STAGE(PG8_SA(0, 1), a2 + hstepA, w1);
;             PG8_WAIT_V(8); PG8_WAIT_L(0); PG8_BAR; PG8_MMA(0, 0, At, B0); PG8_MMA(0, 1, At, B1); PG8_BAR; PG8_SCHED;
	v_mfma_f32_16x16x32_bf16 v[64:67], v[138:141], v[202:205], v[64:67]
	v_mfma_f32_16x16x32_bf16 v[60:63], v[166:169], v[202:205], v[60:63]
	v_mfma_f32_16x16x32_bf16 v[48:51], v[138:141], v[210:213], v[48:51]
	v_mfma_f32_16x16x32_bf16 v[44:47], v[166:169], v[210:213], v[44:47]
	v_mfma_f32_16x16x32_bf16 v[32:35], v[138:141], v[218:221], v[32:35]
	v_mfma_f32_16x16x32_bf16 v[28:31], v[166:169], v[218:221], v[28:31]
	v_mfma_f32_16x16x32_bf16 v[16:19], v[138:141], v[226:229], v[16:19]
	v_mfma_f32_16x16x32_bf16 v[12:15], v[166:169], v[226:229], v[12:15]
	v_mfma_f32_16x16x32_bf16 v[64:67], v[162:165], v[206:209], v[64:67]
	v_mfma_f32_16x16x32_bf16 v[60:63], v[170:173], v[206:209], v[60:63]
	v_mfma_f32_16x16x32_bf16 v[48:51], v[162:165], v[214:217], v[48:51]
	v_mfma_f32_16x16x32_bf16 v[44:47], v[170:173], v[214:217], v[44:47]
	v_mfma_f32_16x16x32_bf16 v[32:35], v[162:165], v[222:225], v[32:35]
	v_mfma_f32_16x16x32_bf16 v[28:31], v[170:173], v[222:225], v[28:31]
	v_mfma_f32_16x16x32_bf16 v[16:19], v[162:165], v[230:233], v[16:19]
	v_mfma_f32_16x16x32_bf16 v[12:15], v[170:173], v[230:233], v[12:15]
	v_mfma_f32_16x16x32_bf16 v[56:59], v[186:189], v[202:205], v[56:59]
	v_mfma_f32_16x16x32_bf16 v[52:55], v[194:197], v[202:205], v[52:55]
	v_mfma_f32_16x16x32_bf16 v[40:43], v[186:189], v[210:213], v[40:43]
	v_mfma_f32_16x16x32_bf16 v[36:39], v[194:197], v[210:213], v[36:39]
	v_mfma_f32_16x16x32_bf16 v[24:27], v[186:189], v[218:221], v[24:27]
	v_mfma_f32_16x16x32_bf16 v[20:23], v[194:197], v[218:221], v[20:23]
	v_mfma_f32_16x16x32_bf16 v[8:11], v[186:189], v[226:229], v[8:11]
	v_mfma_f32_16x16x32_bf16 v[4:7], v[194:197], v[226:229], v[4:7]
	v_mfma_f32_16x16x32_bf16 v[56:59], v[190:193], v[206:209], v[56:59]
	v_mfma_f32_16x16x32_bf16 v[52:55], v[198:201], v[206:209], v[52:55]
	v_mfma_f32_16x16x32_bf16 v[40:43], v[190:193], v[214:217], v[40:43]
	v_mfma_f32_16x16x32_bf16 v[36:39], v[198:201], v[214:217], v[36:39]
	v_mfma_f32_16x16x32_bf16 v[24:27], v[190:193], v[222:225], v[24:27]
	v_mfma_f32_16x16x32_bf16 v[20:23], v[198:201], v[222:225], v[20:23]
	v_mfma_f32_16x16x32_bf16 v[8:11], v[190:193], v[230:233], v[8:11]
	v_mfma_f32_16x16x32_bf16 v[4:7], v[198:201], v[230:233], v[4:7]
	s_barrier
	s_add_i32 s82, 0, 0x18000
	v_add_u32_e32 v3, s82, v178
	s_add_i32 s83, 0, 0x1c000
	ds_read_b128 v[138:141], v3
	ds_read_b128 v[162:165], v3 offset:1024
	ds_read_b128 v[166:169], v3 offset:2048
	ds_read_b128 v[170:173], v3 offset:3072
	v_add_u32_e32 v3, s83, v178
	ds_read_b128 v[186:189], v3
	ds_read_b128 v[190:193], v3 offset:1024
	ds_read_b128 v[194:197], v3 offset:2048
	ds_read_b128 v[198:201], v3 offset:3072
	s_add_u32 s56, s56, 0x80000
	s_addc_u32 s57, s57, 0
	s_mov_b32 m0, s64
	v_lshl_add_u64 v[238:239], s[56:57], 0, v[144:145]
	ds_read_b128 v[202:205], v184 offset:32768
	ds_read_b128 v[206:209], v184 offset:33792
	ds_read_b128 v[210:213], v184 offset:34816
	ds_read_b128 v[214:217], v184 offset:35840
	ds_read_b128 v[218:221], v184 offset:36864
	ds_read_b128 v[222:225], v184 offset:37888
	ds_read_b128 v[226:229], v184 offset:38912
	ds_read_b128 v[230:233], v184 offset:39936
	global_load_lds_dwordx4 v[238:239], off
	v_lshl_add_u64 v[238:239], s[56:57], 0, v[148:149]
	s_mov_b32 m0, s65
	s_nop 0
	global_load_lds_dwordx4 v[238:239], off
	s_waitcnt vmcnt(8)
	s_waitcnt lgkmcnt(0)
	s_barrier
	v_mfma_f32_16x16x32_bf16 v[128:131], v[138:141], v[202:205], v[128:131]
	v_mfma_f32_16x16x32_bf16 v[124:127], v[166:169], v[202:205], v[124:127]
	v_mfma_f32_16x16x32_bf16 v[120:123], v[138:141], v[210:213], v[120:123]
	v_mfma_f32_16x16x32_bf16 v[112:115], v[166:169], v[210:213], v[112:115]
	v_mfma_f32_16x16x32_bf16 v[96:99], v[138:141], v[218:221], v[96:99]
	v_mfma_f32_16x16x32_bf16 v[92:95], v[166:169], v[218:221], v[92:95]
	v_mfma_f32_16x16x32_bf16 v[80:83], v[138:141], v[226:229], v[80:83]
	v_mfma_f32_16x16x32_bf16 v[76:79], v[166:169], v[226:229], v[76:79]
	v_mfma_f32_16x16x32_bf16 v[128:131], v[162:165], v[206:209], v[128:131]
	v_mfma_f32_16x16x32_bf16 v[124:127], v[170:173], v[206:209], v[124:127]
	v_mfma_f32_16x16x32_bf16 v[120:123], v[162:165], v[214:217], v[120:123]
	v_mfma_f32_16x16x32_bf16 v[112:115], v[170:173], v[214:217], v[112:115]
	v_mfma_f32_16x16x32_bf16 v[96:99], v[162:165], v[222:225], v[96:99]
	v_mfma_f32_16x16x32_bf16 v[92:95], v[170:173], v[222:225], v[92:95]
	v_mfma_f32_16x16x32_bf16 v[80:83], v[162:165], v[230:233], v[80:83]
	v_mfma_f32_16x16x32_bf16 v[76:79], v[170:173], v[230:233], v[76:79]
	v_mfma_f32_16x16x32_bf16 v[116:119], v[186:189], v[202:205], v[116:119]
	v_mfma_f32_16x16x32_bf16 v[108:111], v[194:197], v[202:205], v[108:111]
	v_mfma_f32_16x16x32_bf16 v[104:107], v[186:189], v[210:213], v[104:107]
	v_mfma_f32_16x16x32_bf16 v[100:103], v[194:197], v[210:213], v[100:103]
	v_mfma_f32_16x16x32_bf16 v[88:91], v[186:189], v[218:221], v[88:91]
	v_mfma_f32_16x16x32_bf16 v[84:87], v[194:197], v[218:221], v[84:87]
	v_mfma_f32_16x16x32_bf16 v[72:75], v[186:189], v[226:229], v[72:75]
	v_mfma_f32_16x16x32_bf16 v[68:71], v[194:197], v[226:229], v[68:71]
	v_mfma_f32_16x16x32_bf16 v[116:119], v[190:193], v[206:209], v[116:119]
	v_mfma_f32_16x16x32_bf16 v[108:111], v[198:201], v[206:209], v[108:111]
	v_mfma_f32_16x16x32_bf16 v[104:107], v[190:193], v[214:217], v[104:107]
	v_mfma_f32_16x16x32_bf16 v[100:103], v[198:201], v[214:217], v[100:103]
	v_mfma_f32_16x16x32_bf16 v[88:91], v[190:193], v[222:225], v[88:91]
	v_mfma_f32_16x16x32_bf16 v[84:87], v[198:201], v[222:225], v[84:87]
	v_mfma_f32_16x16x32_bf16 v[72:75], v[190:193], v[230:233], v[72:75]
	v_mfma_f32_16x16x32_bf16 v[68:71], v[198:201], v[230:233], v[68:71]
	s_barrier
; #define PG8_STAGE(bufoff, gbase, voff) do { _Pragma("unroll") for (int _i = 0; _i < 2; ++_i) \
;         __builtin_amdgcn_global_load_lds((const unsigned*)((const char*)(gbase) + (voff)[_i]), (PG8_LAS unsigned*)(lds + (bufoff) + ldsw + _i * 8192), 16, 0, 0); } while (0)
; #define PG8_LDA(dst, b, h) do { _Pragma("unroll") for (int m = 0; m < 4; ++m) _Pragma("unroll") for (int k = 0; k < 2; ++k) dst[m][k] = *(const PG8_LAS bf16x8*)(lds + PG8_SA(b, h) + aoff + m * 2048 + k * 1024); } while (0)
; #define PG8_MMA(ai, bj, At, Bt) do { __builtin_amdgcn_s_setprio(1); _Pragma("unroll") for (int m = 0; m < 4; ++m) _Pragma("unroll") for (int n = 0; n < 2; ++n) _Pragma("unroll") for (int k = 0; k < 2; ++k) \
;         acc[ai][bj][m][n] = __builtin_amdgcn_mfma_f32_16x16x32_bf16(Bt[n][k], At[m][k], acc[ai][bj][m][n], 0, 0, 0); __builtin_amdgcn_s_setprio(0); } while (0)
; #define PG8_WAIT_V(n) asm volatile("s_waitcnt vmcnt(" #n ")" ::: "memory")
; #define PG8_WAIT_L(n) asm volatile("s_waitcnt lgkmcnt(" #n ")" ::: "memory")
; #define PG8_BAR __builtin_amdgcn_s_barrier()
; #define PG8_SCHED __builtin_amdgcn_sched_barrier(0)
; template <class Epi, class Sched, bool ALIGN_EPI = false>
; __device__ __forceinline__ void gemm_phase(PG8_LAS unsigned char* lds, const Gemm g, const Sched& S, const Epi& E) {
;     ...
;             PG8_LDA(At, 1, 1); PG8_STAGE(PG8_SB(1, 0), b3, voffB); PG8_STAGE(PG8_SB(1, 1), b3 + hstep, voffB); PG8_STAGE(PG8_SA(1, 0), a3, w0);
;             PG8_WAIT_V(8); PG8_WAIT_L(0); PG8_BAR; PG8_MMA(1, 0, At, B0); PG8_MMA(1, 1, At, B1); PG8_BAR; PG8_SCHED;
;             if constexpr (Epi::KSCALE) { if (((t + 2) & 7) == 0 && t + 2 < nt) { E.kscale(acc, pf, ((t + 2) >> 3) - 1, wr, fr); PG8_SCHED; } }
	s_add_i32 s56, s82, s61
	v_lshl_add_u64 v[142:143], v[142:143], 0, s[18:19]
	s_mov_b32 m0, s56
	ds_read_b128 v[202:205], v184 offset:49152
	ds_read_b128 v[206:209], v184 offset:50176
	ds_read_b128 v[210:213], v184 offset:51200
	ds_read_b128 v[214:217], v184 offset:52224
	ds_read_b128 v[218:221], v184 offset:53248
	ds_read_b128 v[222:225], v184 offset:54272
	ds_read_b128 v[226:229], v184 offset:55296
	ds_read_b128 v[230:233], v184 offset:56320
	global_load_lds_dwordx4 v[142:143], off
	s_add_i32 m0, s56, 0x2000
	s_add_u32 s54, s54, 0x80080
	v_lshl_add_u64 v[142:143], v[174:175], 0, s[18:19]
	s_addc_u32 s55, s55, 0
	s_add_i32 s56, s83, s61
	global_load_lds_dwordx4 v[142:143], off
	v_lshl_add_u64 v[142:143], s[54:55], 0, v[146:147]
	s_mov_b32 m0, s56
	s_nop 0
	global_load_lds_dwordx4 v[142:143], off
	v_lshl_add_u64 v[142:143], s[54:55], 0, v[150:151]
	s_add_i32 m0, s56, 0x2000
	s_nop 0
	global_load_lds_dwordx4 v[142:143], off
	v_lshl_add_u64 v[142:143], v[234:235], 0, s[18:19]
	s_mov_b32 m0, s68
	s_nop 0
	global_load_lds_dwordx4 v[142:143], off
	v_lshl_add_u64 v[142:143], v[236:237], 0, s[18:19]
	s_mov_b32 m0, s69
	s_nop 0
	global_load_lds_dwordx4 v[142:143], off
	s_waitcnt vmcnt(8)
	s_waitcnt lgkmcnt(0)
	s_barrier
	v_mfma_f32_16x16x32_bf16 v[64:67], v[138:141], v[202:205], v[64:67]
	v_mfma_f32_16x16x32_bf16 v[60:63], v[166:169], v[202:205], v[60:63]
	v_mfma_f32_16x16x32_bf16 v[48:51], v[138:141], v[210:213], v[48:51]
	v_mfma_f32_16x16x32_bf16 v[44:47], v[166:169], v[210:213], v[44:47]
	v_mfma_f32_16x16x32_bf16 v[32:35], v[138:141], v[218:221], v[32:35]
	v_mfma_f32_16x16x32_bf16 v[28:31], v[166:169], v[218:221], v[28:31]
	v_mfma_f32_16x16x32_bf16 v[16:19], v[138:141], v[226:229], v[16:19]
	v_mfma_f32_16x16x32_bf16 v[12:15], v[166:169], v[226:229], v[12:15]
	v_mfma_f32_16x16x32_bf16 v[64:67], v[162:165], v[206:209], v[64:67]
	v_mfma_f32_16x16x32_bf16 v[60:63], v[170:173], v[206:209], v[60:63]
	v_mfma_f32_16x16x32_bf16 v[48:51], v[162:165], v[214:217], v[48:51]
	v_mfma_f32_16x16x32_bf16 v[44:47], v[170:173], v[214:217], v[44:47]
	v_mfma_f32_16x16x32_bf16 v[32:35], v[162:165], v[222:225], v[32:35]
	v_mfma_f32_16x16x32_bf16 v[28:31], v[170:173], v[222:225], v[28:31]
	v_mfma_f32_16x16x32_bf16 v[16:19], v[162:165], v[230:233], v[16:19]
	v_mfma_f32_16x16x32_bf16 v[12:15], v[170:173], v[230:233], v[12:15]
	v_mfma_f32_16x16x32_bf16 v[56:59], v[186:189], v[202:205], v[56:59]
	v_mfma_f32_16x16x32_bf16 v[52:55], v[194:197], v[202:205], v[52:55]
	v_mfma_f32_16x16x32_bf16 v[40:43], v[186:189], v[210:213], v[40:43]
	v_mfma_f32_16x16x32_bf16 v[36:39], v[194:197], v[210:213], v[36:39]
	v_mfma_f32_16x16x32_bf16 v[24:27], v[186:189], v[218:221], v[24:27]
	v_mfma_f32_16x16x32_bf16 v[20:23], v[194:197], v[218:221], v[20:23]
	v_mfma_f32_16x16x32_bf16 v[8:11], v[186:189], v[226:229], v[8:11]
	v_mfma_f32_16x16x32_bf16 v[4:7], v[194:197], v[226:229], v[4:7]
	v_mfma_f32_16x16x32_bf16 v[56:59], v[190:193], v[206:209], v[56:59]
	v_mfma_f32_16x16x32_bf16 v[52:55], v[198:201], v[206:209], v[52:55]
	v_mfma_f32_16x16x32_bf16 v[40:43], v[190:193], v[214:217], v[40:43]
	v_mfma_f32_16x16x32_bf16 v[36:39], v[198:201], v[214:217], v[36:39]
	v_mfma_f32_16x16x32_bf16 v[24:27], v[190:193], v[222:225], v[24:27]
	v_mfma_f32_16x16x32_bf16 v[20:23], v[198:201], v[222:225], v[20:23]
	v_mfma_f32_16x16x32_bf16 v[8:11], v[190:193], v[230:233], v[8:11]
	v_mfma_f32_16x16x32_bf16 v[4:7], v[198:201], v[230:233], v[4:7]
	s_barrier
	s_mov_b32 s82, s81
	s_add_i32 s81, s81, 2
	s_and_b32 s54, s81, 6
	s_cmp_eq_u32 s54, 0
	s_cselect_b64 s[56:57], -1, 0
	s_cmp_gt_u32 s82, 29
	s_cselect_b64 s[54:55], -1, 0
	s_cmp_lt_u32 s82, 30
	s_cselect_b64 s[82:83], -1, 0
	s_and_b64 s[56:57], s[56:57], s[82:83]
	s_andn2_b64 vcc, exec, s[56:57]
	s_cbranch_vccnz .LBB0_503
; #define PG8_SCHED __builtin_amdgcn_sched_barrier(0)
;     __device__ __forceinline__ void kscale(f32x4 (&acc)[2][2][4][2], const Pre& pf, int b, int wr, int fr) const {
; #pragma unroll
;         for (int ai = 0; ai < 2; ++ai)
; #pragma unroll
;             for (int m = 0; m < 4; ++m) { const float f = pf.tab[(ai * HALF + wr * 64 + m * 16 + fr) * 4 + b];
; #pragma unroll
;                 for (int bj = 0; bj < 2; ++bj)
; #pragma unroll
;                     for (int n = 0; n < 2; ++n) acc[ai][bj][m][n] = acc[ai][bj][m][n] * f; }
;     }
; template <class Epi, class Sched, bool ALIGN_EPI = false>
; __device__ __forceinline__ void gemm_phase(PG8_LAS unsigned char* lds, const Gemm g, const Sched& S, const Epi& E) {
;     ...
;             if constexpr (Epi::KSCALE) { if (((t + 2) & 7) == 0 && t + 2 < nt) { E.kscale(acc, pf, ((t + 2) >> 3) - 1, wr, fr); PG8_SCHED; } }
	s_lshr_b32 s56, s81, 1
	v_add_u32_e32 v3, s56, v137
	v_add_u32_e32 v136, -4, v3
	ds_read_b32 v136, v136
	ds_read_b32 v138, v3 offset:2812
	ds_read2_b32 v[140:141], v3 offset0:63 offset1:127
	v_add_u32_e32 v3, 0xfc, v3
	s_waitcnt lgkmcnt(0)
	v_pk_mul_f32 v[130:131], v[130:131], v[136:137] op_sel_hi:[1,0]
	v_pk_mul_f32 v[128:129], v[128:129], v[136:137] op_sel_hi:[1,0]
	v_pk_mul_f32 v[126:127], v[126:127], v[136:137] op_sel_hi:[1,0]
	v_pk_mul_f32 v[124:125], v[124:125], v[136:137] op_sel_hi:[1,0]
	v_pk_mul_f32 v[118:119], v[118:119], v[136:137] op_sel_hi:[1,0]
	v_pk_mul_f32 v[116:117], v[116:117], v[136:137] op_sel_hi:[1,0]
	v_pk_mul_f32 v[110:111], v[110:111], v[136:137] op_sel_hi:[1,0]
	v_pk_mul_f32 v[108:109], v[108:109], v[136:137] op_sel_hi:[1,0]
	v_pk_mul_f32 v[122:123], v[122:123], v[140:141] op_sel_hi:[1,0]
	v_pk_mul_f32 v[120:121], v[120:121], v[140:141] op_sel_hi:[1,0]
	v_pk_mul_f32 v[114:115], v[114:115], v[140:141] op_sel_hi:[1,0]
	v_pk_mul_f32 v[112:113], v[112:113], v[140:141] op_sel_hi:[1,0]
	v_pk_mul_f32 v[106:107], v[106:107], v[140:141] op_sel_hi:[1,0]
	v_pk_mul_f32 v[104:105], v[104:105], v[140:141] op_sel_hi:[1,0]
	v_pk_mul_f32 v[102:103], v[102:103], v[140:141] op_sel_hi:[1,0]
	v_pk_mul_f32 v[100:101], v[100:101], v[140:141] op_sel_hi:[1,0]
	v_mov_b32_e32 v136, v141
	ds_read2st64_b32 v[140:141], v3 offset0:2 offset1:7
	v_pk_mul_f32 v[98:99], v[98:99], v[136:137] op_sel_hi:[1,0]
	v_pk_mul_f32 v[96:97], v[96:97], v[136:137] op_sel_hi:[1,0]
	v_pk_mul_f32 v[94:95], v[94:95], v[136:137] op_sel_hi:[1,0]
	v_pk_mul_f32 v[92:93], v[92:93], v[136:137] op_sel_hi:[1,0]
	v_pk_mul_f32 v[90:91], v[90:91], v[136:137] op_sel_hi:[1,0]
	v_pk_mul_f32 v[88:89], v[88:89], v[136:137] op_sel_hi:[1,0]
	v_pk_mul_f32 v[86:87], v[86:87], v[136:137] op_sel_hi:[1,0]
	v_pk_mul_f32 v[84:85], v[84:85], v[136:137] op_sel_hi:[1,0]
	s_waitcnt lgkmcnt(0)
	v_pk_mul_f32 v[82:83], v[82:83], v[140:141] op_sel_hi:[1,0]
	v_pk_mul_f32 v[80:81], v[80:81], v[140:141] op_sel_hi:[1,0]
	v_pk_mul_f32 v[78:79], v[78:79], v[140:141] op_sel_hi:[1,0]
	v_pk_mul_f32 v[76:77], v[76:77], v[140:141] op_sel_hi:[1,0]
	v_pk_mul_f32 v[74:75], v[74:75], v[140:141] op_sel_hi:[1,0]
	v_pk_mul_f32 v[72:73], v[72:73], v[140:141] op_sel_hi:[1,0]
	v_pk_mul_f32 v[70:71], v[70:71], v[140:141] op_sel_hi:[1,0]
	v_pk_mul_f32 v[68:69], v[68:69], v[140:141] op_sel_hi:[1,0]
	v_mov_b32_e32 v136, v141
	ds_read2st64_b32 v[140:141], v3 offset0:8 offset1:9
	v_pk_mul_f32 v[66:67], v[66:67], v[136:137] op_sel_hi:[1,0]
	v_pk_mul_f32 v[64:65], v[64:65], v[136:137] op_sel_hi:[1,0]
	v_pk_mul_f32 v[62:63], v[62:63], v[136:137] op_sel_hi:[1,0]
	v_pk_mul_f32 v[60:61], v[60:61], v[136:137] op_sel_hi:[1,0]
	v_pk_mul_f32 v[58:59], v[58:59], v[136:137] op_sel_hi:[1,0]
	v_pk_mul_f32 v[56:57], v[56:57], v[136:137] op_sel_hi:[1,0]
	v_pk_mul_f32 v[54:55], v[54:55], v[136:137] op_sel_hi:[1,0]
	v_pk_mul_f32 v[52:53], v[52:53], v[136:137] op_sel_hi:[1,0]
	s_waitcnt lgkmcnt(0)
	v_mov_b32_e32 v136, v141
	v_pk_mul_f32 v[50:51], v[50:51], v[140:141] op_sel_hi:[1,0]
	v_pk_mul_f32 v[48:49], v[48:49], v[140:141] op_sel_hi:[1,0]
	v_pk_mul_f32 v[46:47], v[46:47], v[140:141] op_sel_hi:[1,0]
	v_pk_mul_f32 v[44:45], v[44:45], v[140:141] op_sel_hi:[1,0]
	v_pk_mul_f32 v[42:43], v[42:43], v[140:141] op_sel_hi:[1,0]
	v_pk_mul_f32 v[40:41], v[40:41], v[140:141] op_sel_hi:[1,0]
	v_pk_mul_f32 v[38:39], v[38:39], v[140:141] op_sel_hi:[1,0]
	v_pk_mul_f32 v[36:37], v[36:37], v[140:141] op_sel_hi:[1,0]
	v_pk_mul_f32 v[34:35], v[34:35], v[136:137] op_sel_hi:[1,0]
	v_pk_mul_f32 v[32:33], v[32:33], v[136:137] op_sel_hi:[1,0]
	v_pk_mul_f32 v[30:31], v[30:31], v[136:137] op_sel_hi:[1,0]
	v_pk_mul_f32 v[28:29], v[28:29], v[136:137] op_sel_hi:[1,0]
	v_pk_mul_f32 v[26:27], v[26:27], v[136:137] op_sel_hi:[1,0]
	v_pk_mul_f32 v[24:25], v[24:25], v[136:137] op_sel_hi:[1,0]
	v_pk_mul_f32 v[22:23], v[22:23], v[136:137] op_sel_hi:[1,0]
	v_pk_mul_f32 v[20:21], v[20:21], v[136:137] op_sel_hi:[1,0]
	v_pk_mul_f32 v[18:19], v[18:19], v[138:139] op_sel_hi:[1,0]
	v_pk_mul_f32 v[16:17], v[16:17], v[138:139] op_sel_hi:[1,0]
	v_pk_mul_f32 v[14:15], v[14:15], v[138:139] op_sel_hi:[1,0]
	v_pk_mul_f32 v[12:13], v[12:13], v[138:139] op_sel_hi:[1,0]
	v_pk_mul_f32 v[10:11], v[10:11], v[138:139] op_sel_hi:[1,0]
	v_pk_mul_f32 v[8:9], v[8:9], v[138:139] op_sel_hi:[1,0]
	v_pk_mul_f32 v[6:7], v[6:7], v[138:139] op_sel_hi:[1,0]
	v_pk_mul_f32 v[4:5], v[4:5], v[138:139] op_sel_hi:[1,0]
	s_branch .LBB0_503

; #define PG8_STAGE(bufoff, gbase, voff) do { _Pragma("unroll") for (int _i = 0; _i < 2; ++_i) \
;         __builtin_amdgcn_global_load_lds((const unsigned*)((const char*)(gbase) + (voff)[_i]), (PG8_LAS unsigned*)(lds + (bufoff) + ldsw + _i * 8192), 16, 0, 0); } while (0)
; #define PG8_LDA(dst, b, h) do { _Pragma("unroll") for (int m = 0; m < 4; ++m) _Pragma("unroll") for (int k = 0; k < 2; ++k) dst[m][k] = *(const PG8_LAS bf16x8*)(lds + PG8_SA(b, h) + aoff + m * 2048 + k * 1024); } while (0)
; #define PG8_LDB(dst, b, h) do { _Pragma("unroll") for (int n = 0; n < 2; ++n) _Pragma("unroll") for (int k = 0; k < 2; ++k) dst[n][k] = *(const PG8_LAS bf16x8*)(lds + PG8_SB(b, h) + boff + n * 2048 + k * 1024); } while (0)
; #define PG8_MMA(ai, bj, At, Bt) do { __builtin_amdgcn_s_setprio(1); _Pragma("unroll") for (int m = 0; m < 4; ++m) _Pragma("unroll") for (int n = 0; n < 2; ++n) _Pragma("unroll") for (int k = 0; k < 2; ++k) \
;         acc[ai][bj][m][n] = __builtin_amdgcn_mfma_f32_16x16x32_bf16(Bt[n][k], At[m][k], acc[ai][bj][m][n], 0, 0, 0); __builtin_amdgcn_s_setprio(0); } while (0)
; #define PG8_WAIT_V(n) asm volatile("s_waitcnt vmcnt(" #n ")" ::: "memory")
; #define PG8_BAR __builtin_amdgcn_s_barrier()
; template <class Epi, class Sched, bool ALIGN_EPI = false>
; __device__ __forceinline__ void gemm_phase(PG8_LAS unsigned char* lds, const Gemm g, const Sched& S, const Epi& E) {
;     ...
;         for (int t = 0; t < nt; t += 2) {
;             const bool last = (t == nt - 2);
;             const char* a1 = cA + (size_t)(t + 1) * kstep;
;             const char* a2 = last ? nA : cA + (size_t)(t + 2) * kstep; const char* b2 = last ? nB : cB + (size_t)(t + 2) * kstep;
;             const char* a3 = a2 + kstep; const char* b3 = b2 + kstep;
;             unsigned w0[2], w1[2];
; #pragma unroll
;             for (int i = 0; i < 2; ++i) { w0[i] = (Sched::GATHER && last) ? vn0[i] : vc0[i]; w1[i] = (Sched::GATHER && last) ? vn1[i] : vc1[i]; }
;             if (last && has_next) S.a_ready(nxt);
;             PG8_LDB(B0, 0, 0); PG8_LDB(B1, 0, 1); PG8_SCHED; PG8_LDA(At, 0, 0); PG8_STAGE(PG8_SA(1, 1), a1 + hstepA, vc1);
;             PG8_WAIT_V(8); PG8_WAIT_L(0); PG8_BAR; PG8_MMA(0, 0, At, B0); PG8_MMA(0, 1, At, B1); PG8_BAR; PG8_SCHED;
;             PG8_LDA(At, 0, 1); PG8_STAGE(PG8_SB(0, 0), b2, voffB); PG8_STAGE(PG8_SB(0, 1), b2 + hstep, voffB); PG8_STAGE(PG8_SA(0, 0), a2, w0);
.LBB0_721:
	s_add_u32 s58, s36, s56
	v_add_u32_e32 v155, s82, v143
	s_addc_u32 s59, s37, s57
	ds_read_b128 v[164:167], v155
	ds_read_b128 v[168:171], v155 offset:1024
	ds_read_b128 v[172:175], v155 offset:2048
	ds_read_b128 v[176:179], v155 offset:3072
	v_add_u32_e32 v155, s83, v143
	s_add_u32 s60, s58, 0x3c800100
	ds_read_b128 v[180:183], v155
	ds_read_b128 v[184:187], v155 offset:1024
	ds_read_b128 v[188:191], v155 offset:2048
	ds_read_b128 v[192:195], v155 offset:3072
	s_addc_u32 s61, s59, 0
	s_add_u32 s91, s49, s56
	s_addc_u32 s92, s89, s57
	s_cmpk_eq_i32 s56, 0xf00
	s_cselect_b64 vcc, -1, 0
	s_and_b64 s[58:59], vcc, exec
	v_cndmask_b32_e32 v134, v151, v149, vcc
	s_cselect_b32 s61, s21, s61
	s_cselect_b32 s60, s20, s60
	v_cndmask_b32_e32 v153, v152, v157, vcc
	v_cndmask_b32_e32 v228, v150, v162, vcc
	v_cndmask_b32_e32 v155, v154, v163, vcc
	s_cselect_b32 s59, s53, s92
	s_cselect_b32 s58, s52, s91
	v_lshl_add_u64 v[230:231], v[160:161], 0, s[56:57]
	s_add_i32 m0, s55, 0xc000
	ds_read_b128 v[196:199], v147
	ds_read_b128 v[200:203], v147 offset:1024
	ds_read_b128 v[204:207], v147 offset:2048
	ds_read_b128 v[208:211], v147 offset:3072
	ds_read_b128 v[212:215], v147 offset:4096
	ds_read_b128 v[216:219], v147 offset:5120
	ds_read_b128 v[220:223], v147 offset:6144
	ds_read_b128 v[224:227], v147 offset:7168
	global_load_lds_dwordx4 v[230:231], off
	v_lshl_add_u64 v[230:231], v[158:159], 0, s[56:57]
	s_add_i32 m0, s55, 0xe000
	s_nop 0
	global_load_lds_dwordx4 v[230:231], off
	s_waitcnt vmcnt(8)
	s_waitcnt lgkmcnt(0)
	s_barrier
	v_mfma_f32_16x16x32_bf16 v[126:129], v[164:167], v[196:199], v[126:129]
	v_mfma_f32_16x16x32_bf16 v[122:125], v[172:175], v[196:199], v[122:125]
	v_mfma_f32_16x16x32_bf16 v[110:113], v[164:167], v[204:207], v[110:113]
	v_mfma_f32_16x16x32_bf16 v[106:109], v[172:175], v[204:207], v[106:109]
	v_mfma_f32_16x16x32_bf16 v[94:97], v[164:167], v[212:215], v[94:97]
	v_mfma_f32_16x16x32_bf16 v[90:93], v[172:175], v[212:215], v[90:93]
	v_mfma_f32_16x16x32_bf16 v[78:81], v[164:167], v[220:223], v[78:81]
	v_mfma_f32_16x16x32_bf16 v[74:77], v[172:175], v[220:223], v[74:77]
	v_mfma_f32_16x16x32_bf16 v[126:129], v[168:171], v[200:203], v[126:129]
	v_mfma_f32_16x16x32_bf16 v[122:125], v[176:179], v[200:203], v[122:125]
	v_mfma_f32_16x16x32_bf16 v[110:113], v[168:171], v[208:211], v[110:113]
	v_mfma_f32_16x16x32_bf16 v[106:109], v[176:179], v[208:211], v[106:109]
	v_mfma_f32_16x16x32_bf16 v[94:97], v[168:171], v[216:219], v[94:97]
	v_mfma_f32_16x16x32_bf16 v[90:93], v[176:179], v[216:219], v[90:93]
	v_mfma_f32_16x16x32_bf16 v[78:81], v[168:171], v[224:227], v[78:81]
	v_mfma_f32_16x16x32_bf16 v[74:77], v[176:179], v[224:227], v[74:77]
	v_mfma_f32_16x16x32_bf16 v[118:121], v[180:183], v[196:199], v[118:121]
	v_mfma_f32_16x16x32_bf16 v[114:117], v[188:191], v[196:199], v[114:117]
	v_mfma_f32_16x16x32_bf16 v[102:105], v[180:183], v[204:207], v[102:105]
	v_mfma_f32_16x16x32_bf16 v[98:101], v[188:191], v[204:207], v[98:101]
	v_mfma_f32_16x16x32_bf16 v[86:89], v[180:183], v[212:215], v[86:89]
	v_mfma_f32_16x16x32_bf16 v[82:85], v[188:191], v[212:215], v[82:85]
	v_mfma_f32_16x16x32_bf16 v[70:73], v[180:183], v[220:223], v[70:73]
	v_mfma_f32_16x16x32_bf16 v[66:69], v[188:191], v[220:223], v[66:69]
	v_mfma_f32_16x16x32_bf16 v[118:121], v[184:187], v[200:203], v[118:121]
	v_mfma_f32_16x16x32_bf16 v[114:117], v[192:195], v[200:203], v[114:117]
	v_mfma_f32_16x16x32_bf16 v[102:105], v[184:187], v[208:211], v[102:105]
	v_mfma_f32_16x16x32_bf16 v[98:101], v[192:195], v[208:211], v[98:101]
	v_mfma_f32_16x16x32_bf16 v[86:89], v[184:187], v[216:219], v[86:89]
	v_mfma_f32_16x16x32_bf16 v[82:85], v[192:195], v[216:219], v[82:85]
	v_mfma_f32_16x16x32_bf16 v[70:73], v[184:187], v[224:227], v[70:73]
	v_mfma_f32_16x16x32_bf16 v[66:69], v[192:195], v[224:227], v[66:69]
	s_barrier
	s_add_i32 s91, s82, s74
	v_lshl_add_u64 v[230:231], s[58:59], 0, v[130:131]
	s_mov_b32 m0, s91
	ds_read_b128 v[196:199], v147 offset:16384
	ds_read_b128 v[200:203], v147 offset:17408
	ds_read_b128 v[204:207], v147 offset:18432
	ds_read_b128 v[208:211], v147 offset:19456
	ds_read_b128 v[212:215], v147 offset:20480
	ds_read_b128 v[216:219], v147 offset:21504
	ds_read_b128 v[220:223], v147 offset:22528
	ds_read_b128 v[224:227], v147 offset:23552
	global_load_lds_dwordx4 v[230:231], off
	s_add_i32 m0, s91, 0x2000
	s_add_u32 s92, s58, 0x80000
	v_lshl_add_u64 v[232:233], s[58:59], 0, v[132:133]
	s_addc_u32 s93, s59, 0
	s_add_i32 s91, s83, s74
	global_load_lds_dwordx4 v[232:233], off
	v_lshl_add_u64 v[234:235], s[92:93], 0, v[130:131]
	s_mov_b32 m0, s91
	v_mov_b32_e32 v229, v135
	global_load_lds_dwordx4 v[234:235], off
	v_lshl_add_u64 v[234:235], s[92:93], 0, v[132:133]
	s_add_i32 m0, s91, 0x2000
	s_nop 0
	global_load_lds_dwordx4 v[234:235], off
	s_mov_b32 m0, s55
	v_lshl_add_u64 v[234:235], s[60:61], 0, v[134:135]
	global_load_lds_dwordx4 v134, s[60:61]
	s_mov_b32 m0, s75
	s_nop 0
	global_load_lds_dwordx4 v228, s[60:61]
	s_waitcnt vmcnt(8)
	s_waitcnt lgkmcnt(0)
	v_lshl_add_u64 v[228:229], s[60:61], 0, v[228:229]
	s_barrier
; #define PG8_STAGE(bufoff, gbase, voff) do { _Pragma("unroll") for (int _i = 0; _i < 2; ++_i) \
;         __builtin_amdgcn_global_load_lds((const unsigned*)((const char*)(gbase) + (voff)[_i]), (PG8_LAS unsigned*)(lds + (bufoff) + ldsw + _i * 8192), 16, 0, 0); } while (0)
; #define PG8_LDA(dst, b, h) do { _Pragma("unroll") for (int m = 0; m < 4; ++m) _Pragma("unroll") for (int k = 0; k < 2; ++k) dst[m][k] = *(const PG8_LAS bf16x8*)(lds + PG8_SA(b, h) + aoff + m * 2048 + k * 1024); } while (0)
; #define PG8_LDB(dst, b, h) do { _Pragma("unroll") for (int n = 0; n < 2; ++n) _Pragma("unroll") for (int k = 0; k < 2; ++k) dst[n][k] = *(const PG8_LAS bf16x8*)(lds + PG8_SB(b, h) + boff + n * 2048 + k * 1024); } while (0)
; #define PG8_MMA(ai, bj, At, Bt) do { __builtin_amdgcn_s_setprio(1); _Pragma("unroll") for (int m = 0; m < 4; ++m) _Pragma("unroll") for (int n = 0; n < 2; ++n) _Pragma("unroll") for (int k = 0; k < 2; ++k) \
;         acc[ai][bj][m][n] = __builtin_amdgcn_mfma_f32_16x16x32_bf16(Bt[n][k], At[m][k], acc[ai][bj][m][n], 0, 0, 0); __builtin_amdgcn_s_setprio(0); } while (0)
; #define PG8_WAIT_V(n) asm volatile("s_waitcnt vmcnt(" #n ")" ::: "memory")
; #define PG8_WAIT_L(n) asm volatile("s_waitcnt lgkmcnt(" #n ")" ::: "memory")
; #define PG8_BAR __builtin_amdgcn_s_barrier()
; #define PG8_SCHED __builtin_amdgcn_sched_barrier(0)
; template <class Epi, class Sched, bool ALIGN_EPI = false>
; __device__ __forceinline__ void gemm_phase(PG8_LAS unsigned char* lds, const Gemm g, const Sched& S, const Epi& E) {
;     ...
;             PG8_WAIT_V(8); PG8_WAIT_L(0); PG8_BAR; PG8_MMA(1, 0, At, B0); PG8_MMA(1, 1, At, B1); PG8_BAR; PG8_SCHED;
;             PG8_LDB(B0, 1, 0); PG8_LDB(B1, 1, 1); PG8_SCHED; PG8_LDA(At, 1, 0); PG8_STAGE(PG8_SA(0, 1), a2 + hstepA, w1);
;             PG8_WAIT_V(8); PG8_WAIT_L(0); PG8_BAR; PG8_MMA(0, 0, At, B0); PG8_MMA(0, 1, At, B1); PG8_BAR; PG8_SCHED;
	v_mfma_f32_16x16x32_bf16 v[62:65], v[164:167], v[196:199], v[62:65]
	v_mfma_f32_16x16x32_bf16 v[58:61], v[172:175], v[196:199], v[58:61]
	v_mfma_f32_16x16x32_bf16 v[50:53], v[164:167], v[204:207], v[50:53]
	v_mfma_f32_16x16x32_bf16 v[42:45], v[172:175], v[204:207], v[42:45]
	v_mfma_f32_16x16x32_bf16 v[34:37], v[164:167], v[212:215], v[34:37]
	v_mfma_f32_16x16x32_bf16 v[30:33], v[172:175], v[212:215], v[30:33]
	v_mfma_f32_16x16x32_bf16 v[14:17], v[164:167], v[220:223], v[14:17]
	v_mfma_f32_16x16x32_bf16 v[2:5], v[172:175], v[220:223], v[2:5]
	v_mfma_f32_16x16x32_bf16 v[62:65], v[168:171], v[200:203], v[62:65]
	v_mfma_f32_16x16x32_bf16 v[58:61], v[176:179], v[200:203], v[58:61]
	v_mfma_f32_16x16x32_bf16 v[50:53], v[168:171], v[208:211], v[50:53]
	v_mfma_f32_16x16x32_bf16 v[42:45], v[176:179], v[208:211], v[42:45]
	v_mfma_f32_16x16x32_bf16 v[34:37], v[168:171], v[216:219], v[34:37]
	v_mfma_f32_16x16x32_bf16 v[30:33], v[176:179], v[216:219], v[30:33]
	v_mfma_f32_16x16x32_bf16 v[14:17], v[168:171], v[224:227], v[14:17]
	v_mfma_f32_16x16x32_bf16 v[2:5], v[176:179], v[224:227], v[2:5]
	v_mfma_f32_16x16x32_bf16 v[54:57], v[180:183], v[196:199], v[54:57]
	v_mfma_f32_16x16x32_bf16 v[46:49], v[188:191], v[196:199], v[46:49]
	v_mfma_f32_16x16x32_bf16 v[38:41], v[180:183], v[204:207], v[38:41]
	v_mfma_f32_16x16x32_bf16 v[26:29], v[188:191], v[204:207], v[26:29]
	v_mfma_f32_16x16x32_bf16 v[22:25], v[180:183], v[212:215], v[22:25]
	v_mfma_f32_16x16x32_bf16 v[18:21], v[188:191], v[212:215], v[18:21]
	v_mfma_f32_16x16x32_bf16 v[10:13], v[180:183], v[220:223], v[10:13]
	v_mfma_f32_16x16x32_bf16 v[6:9], v[188:191], v[220:223], v[6:9]
	v_mfma_f32_16x16x32_bf16 v[54:57], v[184:187], v[200:203], v[54:57]
	v_mfma_f32_16x16x32_bf16 v[46:49], v[192:195], v[200:203], v[46:49]
	v_mfma_f32_16x16x32_bf16 v[38:41], v[184:187], v[208:211], v[38:41]
	v_mfma_f32_16x16x32_bf16 v[26:29], v[192:195], v[208:211], v[26:29]
	v_mfma_f32_16x16x32_bf16 v[22:25], v[184:187], v[216:219], v[22:25]
	v_mfma_f32_16x16x32_bf16 v[18:21], v[192:195], v[216:219], v[18:21]
	v_mfma_f32_16x16x32_bf16 v[10:13], v[184:187], v[224:227], v[10:13]
	v_mfma_f32_16x16x32_bf16 v[6:9], v[192:195], v[224:227], v[6:9]
	s_barrier
	s_add_i32 s91, 0, 0x18000
	v_add_u32_e32 v134, s91, v143
	s_add_i32 s92, 0, 0x1c000
	ds_read_b128 v[164:167], v134
	ds_read_b128 v[168:171], v134 offset:1024
	ds_read_b128 v[172:175], v134 offset:2048
	ds_read_b128 v[176:179], v134 offset:3072
	v_add_u32_e32 v134, s92, v143
	ds_read_b128 v[180:183], v134
	ds_read_b128 v[184:187], v134 offset:1024
	ds_read_b128 v[188:191], v134 offset:2048
	ds_read_b128 v[192:195], v134 offset:3072
	s_mov_b32 m0, s76
	ds_read_b128 v[196:199], v147 offset:32768
	ds_read_b128 v[200:203], v147 offset:33792
	ds_read_b128 v[204:207], v147 offset:34816
	ds_read_b128 v[208:211], v147 offset:35840
	ds_read_b128 v[212:215], v147 offset:36864
	ds_read_b128 v[216:219], v147 offset:37888
	ds_read_b128 v[220:223], v147 offset:38912
	ds_read_b128 v[224:227], v147 offset:39936
	global_load_lds_dwordx4 v153, s[60:61]
	s_mov_b32 m0, s77
	s_nop 0
	global_load_lds_dwordx4 v155, s[60:61]
	s_waitcnt vmcnt(8)
	s_waitcnt lgkmcnt(0)
	s_barrier
	v_mfma_f32_16x16x32_bf16 v[126:129], v[164:167], v[196:199], v[126:129]
	v_mfma_f32_16x16x32_bf16 v[122:125], v[172:175], v[196:199], v[122:125]
	v_mfma_f32_16x16x32_bf16 v[110:113], v[164:167], v[204:207], v[110:113]
	v_mfma_f32_16x16x32_bf16 v[106:109], v[172:175], v[204:207], v[106:109]
	v_mfma_f32_16x16x32_bf16 v[94:97], v[164:167], v[212:215], v[94:97]
	v_mfma_f32_16x16x32_bf16 v[90:93], v[172:175], v[212:215], v[90:93]
	v_mfma_f32_16x16x32_bf16 v[78:81], v[164:167], v[220:223], v[78:81]
	v_mfma_f32_16x16x32_bf16 v[74:77], v[172:175], v[220:223], v[74:77]
	v_mfma_f32_16x16x32_bf16 v[126:129], v[168:171], v[200:203], v[126:129]
	v_mfma_f32_16x16x32_bf16 v[122:125], v[176:179], v[200:203], v[122:125]
	v_mfma_f32_16x16x32_bf16 v[110:113], v[168:171], v[208:211], v[110:113]
	v_mfma_f32_16x16x32_bf16 v[106:109], v[176:179], v[208:211], v[106:109]
	v_mfma_f32_16x16x32_bf16 v[94:97], v[168:171], v[216:219], v[94:97]
	v_mfma_f32_16x16x32_bf16 v[90:93], v[176:179], v[216:219], v[90:93]
	v_mfma_f32_16x16x32_bf16 v[78:81], v[168:171], v[224:227], v[78:81]
	v_mfma_f32_16x16x32_bf16 v[74:77], v[176:179], v[224:227], v[74:77]
	v_mfma_f32_16x16x32_bf16 v[118:121], v[180:183], v[196:199], v[118:121]
	v_mfma_f32_16x16x32_bf16 v[114:117], v[188:191], v[196:199], v[114:117]
	v_mfma_f32_16x16x32_bf16 v[102:105], v[180:183], v[204:207], v[102:105]
	v_mfma_f32_16x16x32_bf16 v[98:101], v[188:191], v[204:207], v[98:101]
	v_mfma_f32_16x16x32_bf16 v[86:89], v[180:183], v[212:215], v[86:89]
	v_mfma_f32_16x16x32_bf16 v[82:85], v[188:191], v[212:215], v[82:85]
	v_mfma_f32_16x16x32_bf16 v[70:73], v[180:183], v[220:223], v[70:73]
	v_mfma_f32_16x16x32_bf16 v[66:69], v[188:191], v[220:223], v[66:69]
	v_mfma_f32_16x16x32_bf16 v[118:121], v[184:187], v[200:203], v[118:121]
	v_mfma_f32_16x16x32_bf16 v[114:117], v[192:195], v[200:203], v[114:117]
	v_mfma_f32_16x16x32_bf16 v[102:105], v[184:187], v[208:211], v[102:105]
	v_mfma_f32_16x16x32_bf16 v[98:101], v[192:195], v[208:211], v[98:101]
	v_mfma_f32_16x16x32_bf16 v[86:89], v[184:187], v[216:219], v[86:89]
	v_mfma_f32_16x16x32_bf16 v[82:85], v[192:195], v[216:219], v[82:85]
	v_mfma_f32_16x16x32_bf16 v[70:73], v[184:187], v[224:227], v[70:73]
	v_mfma_f32_16x16x32_bf16 v[66:69], v[192:195], v[224:227], v[66:69]
	s_barrier
; #define PG8_STAGE(bufoff, gbase, voff) do { _Pragma("unroll") for (int _i = 0; _i < 2; ++_i) \
;         __builtin_amdgcn_global_load_lds((const unsigned*)((const char*)(gbase) + (voff)[_i]), (PG8_LAS unsigned*)(lds + (bufoff) + ldsw + _i * 8192), 16, 0, 0); } while (0)
; #define PG8_LDA(dst, b, h) do { _Pragma("unroll") for (int m = 0; m < 4; ++m) _Pragma("unroll") for (int k = 0; k < 2; ++k) dst[m][k] = *(const PG8_LAS bf16x8*)(lds + PG8_SA(b, h) + aoff + m * 2048 + k * 1024); } while (0)
; #define PG8_MMA(ai, bj, At, Bt) do { __builtin_amdgcn_s_setprio(1); _Pragma("unroll") for (int m = 0; m < 4; ++m) _Pragma("unroll") for (int n = 0; n < 2; ++n) _Pragma("unroll") for (int k = 0; k < 2; ++k) \
;         acc[ai][bj][m][n] = __builtin_amdgcn_mfma_f32_16x16x32_bf16(Bt[n][k], At[m][k], acc[ai][bj][m][n], 0, 0, 0); __builtin_amdgcn_s_setprio(0); } while (0)
; #define PG8_WAIT_V(n) asm volatile("s_waitcnt vmcnt(" #n ")" ::: "memory")
; #define PG8_WAIT_L(n) asm volatile("s_waitcnt lgkmcnt(" #n ")" ::: "memory")
; #define PG8_BAR __builtin_amdgcn_s_barrier()
; #define PG8_SCHED __builtin_amdgcn_sched_barrier(0)
; template <class Epi, class Sched, bool ALIGN_EPI = false>
; __device__ __forceinline__ void gemm_phase(PG8_LAS unsigned char* lds, const Gemm g, const Sched& S, const Epi& E) {
;     ...
;             PG8_LDA(At, 1, 1); PG8_STAGE(PG8_SB(1, 0), b3, voffB); PG8_STAGE(PG8_SB(1, 1), b3 + hstep, voffB); PG8_STAGE(PG8_SA(1, 0), a3, w0);
;             PG8_WAIT_V(8); PG8_WAIT_L(0); PG8_BAR; PG8_MMA(1, 0, At, B0); PG8_MMA(1, 1, At, B1); PG8_BAR; PG8_SCHED;
;             if constexpr (Epi::KSCALE) { if (((t + 2) & 7) == 0 && t + 2 < nt) { E.kscale(acc, pf, ((t + 2) >> 3) - 1, wr, fr); PG8_SCHED; } }
;         }
	s_add_i32 s60, s91, s74
	v_lshl_add_u64 v[230:231], v[230:231], 0, s[44:45]
	s_mov_b32 m0, s60
	ds_read_b128 v[196:199], v147 offset:49152
	ds_read_b128 v[200:203], v147 offset:50176
	ds_read_b128 v[204:207], v147 offset:51200
	ds_read_b128 v[208:211], v147 offset:52224
	ds_read_b128 v[212:215], v147 offset:53248
	ds_read_b128 v[216:219], v147 offset:54272
	ds_read_b128 v[220:223], v147 offset:55296
	ds_read_b128 v[224:227], v147 offset:56320
	global_load_lds_dwordx4 v[230:231], off
	s_add_i32 m0, s60, 0x2000
	s_add_u32 s58, s58, 0x80080
	v_lshl_add_u64 v[230:231], v[232:233], 0, s[44:45]
	s_addc_u32 s59, s59, 0
	s_add_i32 s60, s92, s74
	global_load_lds_dwordx4 v[230:231], off
	v_lshl_add_u64 v[230:231], s[58:59], 0, v[130:131]
	s_mov_b32 m0, s60
	v_lshl_add_u64 v[228:229], v[228:229], 0, s[44:45]
	global_load_lds_dwordx4 v[230:231], off
	v_lshl_add_u64 v[230:231], s[58:59], 0, v[132:133]
	s_add_i32 m0, s60, 0x2000
	s_nop 0
	global_load_lds_dwordx4 v[230:231], off
	v_lshl_add_u64 v[230:231], v[234:235], 0, s[44:45]
	s_mov_b32 m0, s80
	s_nop 0
	global_load_lds_dwordx4 v[230:231], off
	s_mov_b32 m0, s81
	s_nop 0
	global_load_lds_dwordx4 v[228:229], off
	s_waitcnt vmcnt(8)
	s_waitcnt lgkmcnt(0)
	s_barrier
	v_mfma_f32_16x16x32_bf16 v[62:65], v[164:167], v[196:199], v[62:65]
	v_mfma_f32_16x16x32_bf16 v[58:61], v[172:175], v[196:199], v[58:61]
	v_mfma_f32_16x16x32_bf16 v[50:53], v[164:167], v[204:207], v[50:53]
	v_mfma_f32_16x16x32_bf16 v[42:45], v[172:175], v[204:207], v[42:45]
	v_mfma_f32_16x16x32_bf16 v[34:37], v[164:167], v[212:215], v[34:37]
	v_mfma_f32_16x16x32_bf16 v[30:33], v[172:175], v[212:215], v[30:33]
	v_mfma_f32_16x16x32_bf16 v[14:17], v[164:167], v[220:223], v[14:17]
	v_mfma_f32_16x16x32_bf16 v[2:5], v[172:175], v[220:223], v[2:5]
	v_mfma_f32_16x16x32_bf16 v[62:65], v[168:171], v[200:203], v[62:65]
	v_mfma_f32_16x16x32_bf16 v[58:61], v[176:179], v[200:203], v[58:61]
	v_mfma_f32_16x16x32_bf16 v[50:53], v[168:171], v[208:211], v[50:53]
	v_mfma_f32_16x16x32_bf16 v[42:45], v[176:179], v[208:211], v[42:45]
	v_mfma_f32_16x16x32_bf16 v[34:37], v[168:171], v[216:219], v[34:37]
	v_mfma_f32_16x16x32_bf16 v[30:33], v[176:179], v[216:219], v[30:33]
	v_mfma_f32_16x16x32_bf16 v[14:17], v[168:171], v[224:227], v[14:17]
	v_mfma_f32_16x16x32_bf16 v[2:5], v[176:179], v[224:227], v[2:5]
	v_mfma_f32_16x16x32_bf16 v[54:57], v[180:183], v[196:199], v[54:57]
	v_mfma_f32_16x16x32_bf16 v[46:49], v[188:191], v[196:199], v[46:49]
	v_mfma_f32_16x16x32_bf16 v[38:41], v[180:183], v[204:207], v[38:41]
	v_mfma_f32_16x16x32_bf16 v[26:29], v[188:191], v[204:207], v[26:29]
	v_mfma_f32_16x16x32_bf16 v[22:25], v[180:183], v[212:215], v[22:25]
	v_mfma_f32_16x16x32_bf16 v[18:21], v[188:191], v[212:215], v[18:21]
	v_mfma_f32_16x16x32_bf16 v[10:13], v[180:183], v[220:223], v[10:13]
	v_mfma_f32_16x16x32_bf16 v[6:9], v[188:191], v[220:223], v[6:9]
	v_mfma_f32_16x16x32_bf16 v[54:57], v[184:187], v[200:203], v[54:57]
	v_mfma_f32_16x16x32_bf16 v[46:49], v[192:195], v[200:203], v[46:49]
	v_mfma_f32_16x16x32_bf16 v[38:41], v[184:187], v[208:211], v[38:41]
	v_mfma_f32_16x16x32_bf16 v[26:29], v[192:195], v[208:211], v[26:29]
	v_mfma_f32_16x16x32_bf16 v[22:25], v[184:187], v[216:219], v[22:25]
	v_mfma_f32_16x16x32_bf16 v[18:21], v[192:195], v[216:219], v[18:21]
	v_mfma_f32_16x16x32_bf16 v[10:13], v[184:187], v[224:227], v[10:13]
	v_mfma_f32_16x16x32_bf16 v[6:9], v[192:195], v[224:227], v[6:9]
	s_barrier
	s_add_i32 s90, s90, 2
	s_add_u32 s56, s56, 0x100
	s_addc_u32 s57, s57, 0
	s_cmp_gt_u32 s90, 29
	s_cbranch_scc0 .LBB0_721
	s_and_b64 vcc, exec, s[46:47]
	s_cbranch_vccz .LBB0_724
	s_barrier

; #define PG8_STAGE(bufoff, gbase, voff) do { _Pragma("unroll") for (int _i = 0; _i < 2; ++_i) \
;         __builtin_amdgcn_global_load_lds((const unsigned*)((const char*)(gbase) + (voff)[_i]), (PG8_LAS unsigned*)(lds + (bufoff) + ldsw + _i * 8192), 16, 0, 0); } while (0)
; #define PG8_LDA(dst, b, h) do { _Pragma("unroll") for (int m = 0; m < 4; ++m) _Pragma("unroll") for (int k = 0; k < 2; ++k) dst[m][k] = *(const PG8_LAS bf16x8*)(lds + PG8_SA(b, h) + aoff + m * 2048 + k * 1024); } while (0)
; #define PG8_LDB(dst, b, h) do { _Pragma("unroll") for (int n = 0; n < 2; ++n) _Pragma("unroll") for (int k = 0; k < 2; ++k) dst[n][k] = *(const PG8_LAS bf16x8*)(lds + PG8_SB(b, h) + boff + n * 2048 + k * 1024); } while (0)
; #define PG8_MMA(ai, bj, At, Bt) do { __builtin_amdgcn_s_setprio(1); _Pragma("unroll") for (int m = 0; m < 4; ++m) _Pragma("unroll") for (int n = 0; n < 2; ++n) _Pragma("unroll") for (int k = 0; k < 2; ++k) \
;         acc[ai][bj][m][n] = __builtin_amdgcn_mfma_f32_16x16x32_bf16(Bt[n][k], At[m][k], acc[ai][bj][m][n], 0, 0, 0); __builtin_amdgcn_s_setprio(0); } while (0)
; #define PG8_WAIT_V(n) asm volatile("s_waitcnt vmcnt(" #n ")" ::: "memory")
; #define PG8_BAR __builtin_amdgcn_s_barrier()
; template <class Epi, class Sched, bool ALIGN_EPI = false>
; __device__ __forceinline__ void gemm_phase(PG8_LAS unsigned char* lds, const Gemm g, const Sched& S, const Epi& E) {
;     ...
;         for (int t = 0; t < nt; t += 2) {
;             const bool last = (t == nt - 2);
;             const char* a1 = cA + (size_t)(t + 1) * kstep;
;             const char* a2 = last ? nA : cA + (size_t)(t + 2) * kstep; const char* b2 = last ? nB : cB + (size_t)(t + 2) * kstep;
;             const char* a3 = a2 + kstep; const char* b3 = b2 + kstep;
;             unsigned w0[2], w1[2];
; #pragma unroll
;             for (int i = 0; i < 2; ++i) { w0[i] = (Sched::GATHER && last) ? vn0[i] : vc0[i]; w1[i] = (Sched::GATHER && last) ? vn1[i] : vc1[i]; }
;             if (last && has_next) S.a_ready(nxt);
;             PG8_LDB(B0, 0, 0); PG8_LDB(B1, 0, 1); PG8_SCHED; PG8_LDA(At, 0, 0); PG8_STAGE(PG8_SA(1, 1), a1 + hstepA, vc1);
;             PG8_WAIT_V(8); PG8_WAIT_L(0); PG8_BAR; PG8_MMA(0, 0, At, B0); PG8_MMA(0, 1, At, B1); PG8_BAR; PG8_SCHED;
;             PG8_LDA(At, 0, 1); PG8_STAGE(PG8_SB(0, 0), b2, voffB); PG8_STAGE(PG8_SB(0, 1), b2 + hstep, voffB); PG8_STAGE(PG8_SA(0, 0), a2, w0);
.LBB0_787:
	ds_read_b128 v[172:175], v167
	ds_read_b128 v[176:179], v167 offset:1024
	ds_read_b128 v[180:183], v167 offset:2048
	ds_read_b128 v[184:187], v167 offset:3072
	ds_read_b128 v[188:191], v168
	ds_read_b128 v[192:195], v168 offset:1024
	ds_read_b128 v[196:199], v168 offset:2048
	ds_read_b128 v[200:203], v168 offset:3072
	s_add_u32 s18, s16, 0x3c800100
	s_addc_u32 s19, s17, 0
	s_add_u32 s58, s16, s45
	s_addc_u32 s59, s17, s46
	s_cmp_eq_u32 s47, 28
	s_cselect_b32 s23, s21, s19
	s_cselect_b32 s22, s20, s18
	s_cselect_b32 s19, s13, s59
	s_cselect_b32 s18, s12, s58
	s_mov_b32 m0, s48
	v_lshl_add_u64 v[236:237], s[16:17], 0, v[160:161]
	ds_read_b128 v[204:207], v169
	ds_read_b128 v[208:211], v169 offset:1024
	ds_read_b128 v[212:215], v169 offset:2048
	ds_read_b128 v[216:219], v169 offset:3072
	ds_read_b128 v[220:223], v169 offset:4096
	ds_read_b128 v[224:227], v169 offset:5120
	ds_read_b128 v[228:231], v169 offset:6144
	ds_read_b128 v[232:235], v169 offset:7168
	global_load_lds_dwordx4 v[236:237], off
	v_lshl_add_u64 v[236:237], s[16:17], 0, v[158:159]
	s_mov_b32 m0, s49
	s_nop 0
	global_load_lds_dwordx4 v[236:237], off
	s_waitcnt vmcnt(8)
	s_waitcnt lgkmcnt(0)
	s_barrier
	v_mfma_f32_16x16x32_bf16 v[126:129], v[172:175], v[204:207], v[126:129]
	v_mfma_f32_16x16x32_bf16 v[122:125], v[180:183], v[204:207], v[122:125]
	v_mfma_f32_16x16x32_bf16 v[110:113], v[172:175], v[212:215], v[110:113]
	v_mfma_f32_16x16x32_bf16 v[106:109], v[180:183], v[212:215], v[106:109]
	v_mfma_f32_16x16x32_bf16 v[94:97], v[172:175], v[220:223], v[94:97]
	v_mfma_f32_16x16x32_bf16 v[90:93], v[180:183], v[220:223], v[90:93]
	v_mfma_f32_16x16x32_bf16 v[78:81], v[172:175], v[228:231], v[78:81]
	v_mfma_f32_16x16x32_bf16 v[74:77], v[180:183], v[228:231], v[74:77]
	v_mfma_f32_16x16x32_bf16 v[126:129], v[176:179], v[208:211], v[126:129]
	v_mfma_f32_16x16x32_bf16 v[122:125], v[184:187], v[208:211], v[122:125]
	v_mfma_f32_16x16x32_bf16 v[110:113], v[176:179], v[216:219], v[110:113]
	v_mfma_f32_16x16x32_bf16 v[106:109], v[184:187], v[216:219], v[106:109]
	v_mfma_f32_16x16x32_bf16 v[94:97], v[176:179], v[224:227], v[94:97]
	v_mfma_f32_16x16x32_bf16 v[90:93], v[184:187], v[224:227], v[90:93]
	v_mfma_f32_16x16x32_bf16 v[78:81], v[176:179], v[232:235], v[78:81]
	v_mfma_f32_16x16x32_bf16 v[74:77], v[184:187], v[232:235], v[74:77]
	v_mfma_f32_16x16x32_bf16 v[118:121], v[188:191], v[204:207], v[118:121]
	v_mfma_f32_16x16x32_bf16 v[114:117], v[196:199], v[204:207], v[114:117]
	v_mfma_f32_16x16x32_bf16 v[102:105], v[188:191], v[212:215], v[102:105]
	v_mfma_f32_16x16x32_bf16 v[98:101], v[196:199], v[212:215], v[98:101]
	v_mfma_f32_16x16x32_bf16 v[86:89], v[188:191], v[220:223], v[86:89]
	v_mfma_f32_16x16x32_bf16 v[82:85], v[196:199], v[220:223], v[82:85]
	v_mfma_f32_16x16x32_bf16 v[70:73], v[188:191], v[228:231], v[70:73]
	v_mfma_f32_16x16x32_bf16 v[66:69], v[196:199], v[228:231], v[66:69]
	v_mfma_f32_16x16x32_bf16 v[118:121], v[192:195], v[208:211], v[118:121]
	v_mfma_f32_16x16x32_bf16 v[114:117], v[200:203], v[208:211], v[114:117]
	v_mfma_f32_16x16x32_bf16 v[102:105], v[192:195], v[216:219], v[102:105]
	v_mfma_f32_16x16x32_bf16 v[98:101], v[200:203], v[216:219], v[98:101]
	v_mfma_f32_16x16x32_bf16 v[86:89], v[192:195], v[224:227], v[86:89]
	v_mfma_f32_16x16x32_bf16 v[82:85], v[200:203], v[224:227], v[82:85]
	v_mfma_f32_16x16x32_bf16 v[70:73], v[192:195], v[232:235], v[70:73]
	v_mfma_f32_16x16x32_bf16 v[66:69], v[200:203], v[232:235], v[66:69]
	s_barrier
	s_mov_b32 m0, s50
	v_lshl_add_u64 v[236:237], s[18:19], 0, v[146:147]
	s_add_u32 s58, s18, 0x80000
	ds_read_b128 v[204:207], v169 offset:16384
	ds_read_b128 v[208:211], v169 offset:17408
	ds_read_b128 v[212:215], v169 offset:18432
	ds_read_b128 v[216:219], v169 offset:19456
	ds_read_b128 v[220:223], v169 offset:20480
	ds_read_b128 v[224:227], v169 offset:21504
	ds_read_b128 v[228:231], v169 offset:22528
	ds_read_b128 v[232:235], v169 offset:23552
	global_load_lds_dwordx4 v[236:237], off
	v_lshl_add_u64 v[238:239], s[18:19], 0, v[144:145]
	s_mov_b32 m0, s51
	s_addc_u32 s59, s19, 0
	global_load_lds_dwordx4 v[238:239], off
	v_lshl_add_u64 v[240:241], s[58:59], 0, v[146:147]
	s_mov_b32 m0, s52
	v_lshl_add_u64 v[242:243], s[22:23], 0, v[150:151]
	global_load_lds_dwordx4 v[240:241], off
	v_lshl_add_u64 v[240:241], s[58:59], 0, v[144:145]
	s_mov_b32 m0, s53
	s_nop 0
	global_load_lds_dwordx4 v[240:241], off
	v_lshl_add_u64 v[240:241], s[22:23], 0, v[148:149]
	s_mov_b32 m0, s27
	s_nop 0
	global_load_lds_dwordx4 v[240:241], off
	s_mov_b32 m0, s35
	s_nop 0
	global_load_lds_dwordx4 v[242:243], off
	s_waitcnt vmcnt(8)
	s_waitcnt lgkmcnt(0)
	s_barrier
; #define PG8_STAGE(bufoff, gbase, voff) do { _Pragma("unroll") for (int _i = 0; _i < 2; ++_i) \
;         __builtin_amdgcn_global_load_lds((const unsigned*)((const char*)(gbase) + (voff)[_i]), (PG8_LAS unsigned*)(lds + (bufoff) + ldsw + _i * 8192), 16, 0, 0); } while (0)
; #define PG8_LDA(dst, b, h) do { _Pragma("unroll") for (int m = 0; m < 4; ++m) _Pragma("unroll") for (int k = 0; k < 2; ++k) dst[m][k] = *(const PG8_LAS bf16x8*)(lds + PG8_SA(b, h) + aoff + m * 2048 + k * 1024); } while (0)
; #define PG8_LDB(dst, b, h) do { _Pragma("unroll") for (int n = 0; n < 2; ++n) _Pragma("unroll") for (int k = 0; k < 2; ++k) dst[n][k] = *(const PG8_LAS bf16x8*)(lds + PG8_SB(b, h) + boff + n * 2048 + k * 1024); } while (0)
; #define PG8_MMA(ai, bj, At, Bt) do { __builtin_amdgcn_s_setprio(1); _Pragma("unroll") for (int m = 0; m < 4; ++m) _Pragma("unroll") for (int n = 0; n < 2; ++n) _Pragma("unroll") for (int k = 0; k < 2; ++k) \
;         acc[ai][bj][m][n] = __builtin_amdgcn_mfma_f32_16x16x32_bf16(Bt[n][k], At[m][k], acc[ai][bj][m][n], 0, 0, 0); __builtin_amdgcn_s_setprio(0); } while (0)
; #define PG8_WAIT_V(n) asm volatile("s_waitcnt vmcnt(" #n ")" ::: "memory")
; #define PG8_WAIT_L(n) asm volatile("s_waitcnt lgkmcnt(" #n ")" ::: "memory")
; #define PG8_BAR __builtin_amdgcn_s_barrier()
; #define PG8_SCHED __builtin_amdgcn_sched_barrier(0)
; template <class Epi, class Sched, bool ALIGN_EPI = false>
; __device__ __forceinline__ void gemm_phase(PG8_LAS unsigned char* lds, const Gemm g, const Sched& S, const Epi& E) {
;     ...
;             PG8_WAIT_V(8); PG8_WAIT_L(0); PG8_BAR; PG8_MMA(1, 0, At, B0); PG8_MMA(1, 1, At, B1); PG8_BAR; PG8_SCHED;
;             PG8_LDB(B0, 1, 0); PG8_LDB(B1, 1, 1); PG8_SCHED; PG8_LDA(At, 1, 0); PG8_STAGE(PG8_SA(0, 1), a2 + hstepA, w1);
;             PG8_WAIT_V(8); PG8_WAIT_L(0); PG8_BAR; PG8_MMA(0, 0, At, B0); PG8_MMA(0, 1, At, B1); PG8_BAR; PG8_SCHED;
	v_mfma_f32_16x16x32_bf16 v[62:65], v[172:175], v[204:207], v[62:65]
	v_mfma_f32_16x16x32_bf16 v[58:61], v[180:183], v[204:207], v[58:61]
	v_mfma_f32_16x16x32_bf16 v[50:53], v[172:175], v[212:215], v[50:53]
	v_mfma_f32_16x16x32_bf16 v[42:45], v[180:183], v[212:215], v[42:45]
	v_mfma_f32_16x16x32_bf16 v[34:37], v[172:175], v[220:223], v[34:37]
	v_mfma_f32_16x16x32_bf16 v[26:29], v[180:183], v[220:223], v[26:29]
	v_mfma_f32_16x16x32_bf16 v[14:17], v[172:175], v[228:231], v[14:17]
	v_mfma_f32_16x16x32_bf16 v[2:5], v[180:183], v[228:231], v[2:5]
	v_mfma_f32_16x16x32_bf16 v[62:65], v[176:179], v[208:211], v[62:65]
	v_mfma_f32_16x16x32_bf16 v[58:61], v[184:187], v[208:211], v[58:61]
	v_mfma_f32_16x16x32_bf16 v[50:53], v[176:179], v[216:219], v[50:53]
	v_mfma_f32_16x16x32_bf16 v[42:45], v[184:187], v[216:219], v[42:45]
	v_mfma_f32_16x16x32_bf16 v[34:37], v[176:179], v[224:227], v[34:37]
	v_mfma_f32_16x16x32_bf16 v[26:29], v[184:187], v[224:227], v[26:29]
	v_mfma_f32_16x16x32_bf16 v[14:17], v[176:179], v[232:235], v[14:17]
	v_mfma_f32_16x16x32_bf16 v[2:5], v[184:187], v[232:235], v[2:5]
	v_mfma_f32_16x16x32_bf16 v[54:57], v[188:191], v[204:207], v[54:57]
	v_mfma_f32_16x16x32_bf16 v[46:49], v[196:199], v[204:207], v[46:49]
	v_mfma_f32_16x16x32_bf16 v[38:41], v[188:191], v[212:215], v[38:41]
	v_mfma_f32_16x16x32_bf16 v[30:33], v[196:199], v[212:215], v[30:33]
	v_mfma_f32_16x16x32_bf16 v[22:25], v[188:191], v[220:223], v[22:25]
	v_mfma_f32_16x16x32_bf16 v[18:21], v[196:199], v[220:223], v[18:21]
	v_mfma_f32_16x16x32_bf16 v[10:13], v[188:191], v[228:231], v[10:13]
	v_mfma_f32_16x16x32_bf16 v[6:9], v[196:199], v[228:231], v[6:9]
	v_mfma_f32_16x16x32_bf16 v[54:57], v[192:195], v[208:211], v[54:57]
	v_mfma_f32_16x16x32_bf16 v[46:49], v[200:203], v[208:211], v[46:49]
	v_mfma_f32_16x16x32_bf16 v[38:41], v[192:195], v[216:219], v[38:41]
	v_mfma_f32_16x16x32_bf16 v[30:33], v[200:203], v[216:219], v[30:33]
	v_mfma_f32_16x16x32_bf16 v[22:25], v[192:195], v[224:227], v[22:25]
	v_mfma_f32_16x16x32_bf16 v[18:21], v[200:203], v[224:227], v[18:21]
	v_mfma_f32_16x16x32_bf16 v[10:13], v[192:195], v[232:235], v[10:13]
	v_mfma_f32_16x16x32_bf16 v[6:9], v[200:203], v[232:235], v[6:9]
	s_barrier
	ds_read_b128 v[172:175], v170
	ds_read_b128 v[176:179], v170 offset:1024
	ds_read_b128 v[180:183], v170 offset:2048
	ds_read_b128 v[184:187], v170 offset:3072
	ds_read_b128 v[188:191], v171
	ds_read_b128 v[192:195], v171 offset:1024
	ds_read_b128 v[196:199], v171 offset:2048
	ds_read_b128 v[200:203], v171 offset:3072
	s_mov_b32 m0, s40
	v_lshl_add_u64 v[244:245], s[22:23], 0, v[152:153]
	ds_read_b128 v[204:207], v169 offset:32768
	ds_read_b128 v[208:211], v169 offset:33792
	ds_read_b128 v[212:215], v169 offset:34816
	ds_read_b128 v[216:219], v169 offset:35840
	ds_read_b128 v[220:223], v169 offset:36864
	ds_read_b128 v[224:227], v169 offset:37888
	ds_read_b128 v[228:231], v169 offset:38912
	ds_read_b128 v[232:235], v169 offset:39936
	global_load_lds_dwordx4 v[244:245], off
	v_lshl_add_u64 v[244:245], s[22:23], 0, v[154:155]
	s_mov_b32 m0, s41
	s_nop 0
	global_load_lds_dwordx4 v[244:245], off
	s_waitcnt vmcnt(8)
	s_waitcnt lgkmcnt(0)
	s_barrier
	v_mfma_f32_16x16x32_bf16 v[126:129], v[172:175], v[204:207], v[126:129]
	v_mfma_f32_16x16x32_bf16 v[122:125], v[180:183], v[204:207], v[122:125]
	v_mfma_f32_16x16x32_bf16 v[110:113], v[172:175], v[212:215], v[110:113]
	v_mfma_f32_16x16x32_bf16 v[106:109], v[180:183], v[212:215], v[106:109]
	v_mfma_f32_16x16x32_bf16 v[94:97], v[172:175], v[220:223], v[94:97]
	v_mfma_f32_16x16x32_bf16 v[90:93], v[180:183], v[220:223], v[90:93]
	v_mfma_f32_16x16x32_bf16 v[78:81], v[172:175], v[228:231], v[78:81]
	v_mfma_f32_16x16x32_bf16 v[74:77], v[180:183], v[228:231], v[74:77]
	v_mfma_f32_16x16x32_bf16 v[126:129], v[176:179], v[208:211], v[126:129]
	v_mfma_f32_16x16x32_bf16 v[122:125], v[184:187], v[208:211], v[122:125]
	v_mfma_f32_16x16x32_bf16 v[110:113], v[176:179], v[216:219], v[110:113]
	v_mfma_f32_16x16x32_bf16 v[106:109], v[184:187], v[216:219], v[106:109]
	v_mfma_f32_16x16x32_bf16 v[94:97], v[176:179], v[224:227], v[94:97]
	v_mfma_f32_16x16x32_bf16 v[90:93], v[184:187], v[224:227], v[90:93]
	v_mfma_f32_16x16x32_bf16 v[78:81], v[176:179], v[232:235], v[78:81]
	v_mfma_f32_16x16x32_bf16 v[74:77], v[184:187], v[232:235], v[74:77]
	v_mfma_f32_16x16x32_bf16 v[118:121], v[188:191], v[204:207], v[118:121]
	v_mfma_f32_16x16x32_bf16 v[114:117], v[196:199], v[204:207], v[114:117]
	v_mfma_f32_16x16x32_bf16 v[102:105], v[188:191], v[212:215], v[102:105]
	v_mfma_f32_16x16x32_bf16 v[98:101], v[196:199], v[212:215], v[98:101]
	v_mfma_f32_16x16x32_bf16 v[86:89], v[188:191], v[220:223], v[86:89]
	v_mfma_f32_16x16x32_bf16 v[82:85], v[196:199], v[220:223], v[82:85]
	v_mfma_f32_16x16x32_bf16 v[70:73], v[188:191], v[228:231], v[70:73]
	v_mfma_f32_16x16x32_bf16 v[66:69], v[196:199], v[228:231], v[66:69]
	v_mfma_f32_16x16x32_bf16 v[118:121], v[192:195], v[208:211], v[118:121]
	v_mfma_f32_16x16x32_bf16 v[114:117], v[200:203], v[208:211], v[114:117]
	v_mfma_f32_16x16x32_bf16 v[102:105], v[192:195], v[216:219], v[102:105]
	v_mfma_f32_16x16x32_bf16 v[98:101], v[200:203], v[216:219], v[98:101]
	v_mfma_f32_16x16x32_bf16 v[86:89], v[192:195], v[224:227], v[86:89]
	v_mfma_f32_16x16x32_bf16 v[82:85], v[200:203], v[224:227], v[82:85]
	v_mfma_f32_16x16x32_bf16 v[70:73], v[192:195], v[232:235], v[70:73]
	v_mfma_f32_16x16x32_bf16 v[66:69], v[200:203], v[232:235], v[66:69]
	s_barrier
; #define PG8_STAGE(bufoff, gbase, voff) do { _Pragma("unroll") for (int _i = 0; _i < 2; ++_i) \
;         __builtin_amdgcn_global_load_lds((const unsigned*)((const char*)(gbase) + (voff)[_i]), (PG8_LAS unsigned*)(lds + (bufoff) + ldsw + _i * 8192), 16, 0, 0); } while (0)
; #define PG8_LDA(dst, b, h) do { _Pragma("unroll") for (int m = 0; m < 4; ++m) _Pragma("unroll") for (int k = 0; k < 2; ++k) dst[m][k] = *(const PG8_LAS bf16x8*)(lds + PG8_SA(b, h) + aoff + m * 2048 + k * 1024); } while (0)
; #define PG8_MMA(ai, bj, At, Bt) do { __builtin_amdgcn_s_setprio(1); _Pragma("unroll") for (int m = 0; m < 4; ++m) _Pragma("unroll") for (int n = 0; n < 2; ++n) _Pragma("unroll") for (int k = 0; k < 2; ++k) \
;         acc[ai][bj][m][n] = __builtin_amdgcn_mfma_f32_16x16x32_bf16(Bt[n][k], At[m][k], acc[ai][bj][m][n], 0, 0, 0); __builtin_amdgcn_s_setprio(0); } while (0)
; #define PG8_WAIT_V(n) asm volatile("s_waitcnt vmcnt(" #n ")" ::: "memory")
; #define PG8_WAIT_L(n) asm volatile("s_waitcnt lgkmcnt(" #n ")" ::: "memory")
; #define PG8_BAR __builtin_amdgcn_s_barrier()
; #define PG8_SCHED __builtin_amdgcn_sched_barrier(0)
; template <class Epi, class Sched, bool ALIGN_EPI = false>
; __device__ __forceinline__ void gemm_phase(PG8_LAS unsigned char* lds, const Gemm g, const Sched& S, const Epi& E) {
;     ...
;             PG8_LDA(At, 1, 1); PG8_STAGE(PG8_SB(1, 0), b3, voffB); PG8_STAGE(PG8_SB(1, 1), b3 + hstep, voffB); PG8_STAGE(PG8_SA(1, 0), a3, w0);
;             PG8_WAIT_V(8); PG8_WAIT_L(0); PG8_BAR; PG8_MMA(1, 0, At, B0); PG8_MMA(1, 1, At, B1); PG8_BAR; PG8_SCHED;
;             if constexpr (Epi::KSCALE) { if (((t + 2) & 7) == 0 && t + 2 < nt) { E.kscale(acc, pf, ((t + 2) >> 3) - 1, wr, fr); PG8_SCHED; } }
;         }
	s_mov_b32 m0, s54
	v_lshl_add_u64 v[236:237], v[236:237], 0, s[14:15]
	s_add_u32 s18, s18, 0x80080
	ds_read_b128 v[204:207], v169 offset:49152
	ds_read_b128 v[208:211], v169 offset:50176
	ds_read_b128 v[212:215], v169 offset:51200
	ds_read_b128 v[216:219], v169 offset:52224
	ds_read_b128 v[220:223], v169 offset:53248
	ds_read_b128 v[224:227], v169 offset:54272
	ds_read_b128 v[228:231], v169 offset:55296
	ds_read_b128 v[232:235], v169 offset:56320
	global_load_lds_dwordx4 v[236:237], off
	v_lshl_add_u64 v[236:237], v[238:239], 0, s[14:15]
	s_mov_b32 m0, s55
	s_addc_u32 s19, s19, 0
	global_load_lds_dwordx4 v[236:237], off
	v_lshl_add_u64 v[236:237], s[18:19], 0, v[146:147]
	s_mov_b32 m0, s56
	s_nop 0
	global_load_lds_dwordx4 v[236:237], off
	v_lshl_add_u64 v[236:237], s[18:19], 0, v[144:145]
	s_mov_b32 m0, s57
	s_nop 0
	global_load_lds_dwordx4 v[236:237], off
	v_lshl_add_u64 v[236:237], v[240:241], 0, s[14:15]
	s_mov_b32 m0, s43
	s_nop 0
	global_load_lds_dwordx4 v[236:237], off
	v_lshl_add_u64 v[236:237], v[242:243], 0, s[14:15]
	s_mov_b32 m0, s44
	s_nop 0
	global_load_lds_dwordx4 v[236:237], off
	s_waitcnt vmcnt(8)
	s_waitcnt lgkmcnt(0)
	s_barrier
	v_mfma_f32_16x16x32_bf16 v[62:65], v[172:175], v[204:207], v[62:65]
	v_mfma_f32_16x16x32_bf16 v[58:61], v[180:183], v[204:207], v[58:61]
	v_mfma_f32_16x16x32_bf16 v[50:53], v[172:175], v[212:215], v[50:53]
	v_mfma_f32_16x16x32_bf16 v[42:45], v[180:183], v[212:215], v[42:45]
	v_mfma_f32_16x16x32_bf16 v[34:37], v[172:175], v[220:223], v[34:37]
	v_mfma_f32_16x16x32_bf16 v[26:29], v[180:183], v[220:223], v[26:29]
	v_mfma_f32_16x16x32_bf16 v[14:17], v[172:175], v[228:231], v[14:17]
	v_mfma_f32_16x16x32_bf16 v[2:5], v[180:183], v[228:231], v[2:5]
	v_mfma_f32_16x16x32_bf16 v[62:65], v[176:179], v[208:211], v[62:65]
	v_mfma_f32_16x16x32_bf16 v[58:61], v[184:187], v[208:211], v[58:61]
	v_mfma_f32_16x16x32_bf16 v[50:53], v[176:179], v[216:219], v[50:53]
	v_mfma_f32_16x16x32_bf16 v[42:45], v[184:187], v[216:219], v[42:45]
	v_mfma_f32_16x16x32_bf16 v[34:37], v[176:179], v[224:227], v[34:37]
	v_mfma_f32_16x16x32_bf16 v[26:29], v[184:187], v[224:227], v[26:29]
	v_mfma_f32_16x16x32_bf16 v[14:17], v[176:179], v[232:235], v[14:17]
	v_mfma_f32_16x16x32_bf16 v[2:5], v[184:187], v[232:235], v[2:5]
	v_mfma_f32_16x16x32_bf16 v[54:57], v[188:191], v[204:207], v[54:57]
	v_mfma_f32_16x16x32_bf16 v[46:49], v[196:199], v[204:207], v[46:49]
	v_mfma_f32_16x16x32_bf16 v[38:41], v[188:191], v[212:215], v[38:41]
	v_mfma_f32_16x16x32_bf16 v[30:33], v[196:199], v[212:215], v[30:33]
	v_mfma_f32_16x16x32_bf16 v[22:25], v[188:191], v[220:223], v[22:25]
	v_mfma_f32_16x16x32_bf16 v[18:21], v[196:199], v[220:223], v[18:21]
	v_mfma_f32_16x16x32_bf16 v[10:13], v[188:191], v[228:231], v[10:13]
	v_mfma_f32_16x16x32_bf16 v[6:9], v[196:199], v[228:231], v[6:9]
	v_mfma_f32_16x16x32_bf16 v[54:57], v[192:195], v[208:211], v[54:57]
	v_mfma_f32_16x16x32_bf16 v[46:49], v[200:203], v[208:211], v[46:49]
	v_mfma_f32_16x16x32_bf16 v[38:41], v[192:195], v[216:219], v[38:41]
	v_mfma_f32_16x16x32_bf16 v[30:33], v[200:203], v[216:219], v[30:33]
	v_mfma_f32_16x16x32_bf16 v[22:25], v[192:195], v[224:227], v[22:25]
	v_mfma_f32_16x16x32_bf16 v[18:21], v[200:203], v[224:227], v[18:21]
	v_mfma_f32_16x16x32_bf16 v[10:13], v[192:195], v[232:235], v[10:13]
	v_mfma_f32_16x16x32_bf16 v[6:9], v[200:203], v[232:235], v[6:9]
	s_barrier
	s_add_i32 s47, s47, 2
	s_add_u32 s16, s16, 0x100
	s_addc_u32 s17, s17, 0
	s_cmp_gt_u32 s47, 29
	s_cbranch_scc0 .LBB0_787
	s_cmpk_lt_u32 s24, 0x100
	s_cbranch_scc0 .LBB0_790
	s_barrier

; #define PG8_STAGE(bufoff, gbase, voff) do { _Pragma("unroll") for (int _i = 0; _i < 2; ++_i) \
;         __builtin_amdgcn_global_load_lds((const unsigned*)((const char*)(gbase) + (voff)[_i]), (PG8_LAS unsigned*)(lds + (bufoff) + ldsw + _i * 8192), 16, 0, 0); } while (0)
; #define PG8_LDA(dst, b, h) do { _Pragma("unroll") for (int m = 0; m < 4; ++m) _Pragma("unroll") for (int k = 0; k < 2; ++k) dst[m][k] = *(const PG8_LAS bf16x8*)(lds + PG8_SA(b, h) + aoff + m * 2048 + k * 1024); } while (0)
; #define PG8_LDB(dst, b, h) do { _Pragma("unroll") for (int n = 0; n < 2; ++n) _Pragma("unroll") for (int k = 0; k < 2; ++k) dst[n][k] = *(const PG8_LAS bf16x8*)(lds + PG8_SB(b, h) + boff + n * 2048 + k * 1024); } while (0)
; #define PG8_MMA(ai, bj, At, Bt) do { __builtin_amdgcn_s_setprio(1); _Pragma("unroll") for (int m = 0; m < 4; ++m) _Pragma("unroll") for (int n = 0; n < 2; ++n) _Pragma("unroll") for (int k = 0; k < 2; ++k) \
;         acc[ai][bj][m][n] = __builtin_amdgcn_mfma_f32_16x16x32_bf16(Bt[n][k], At[m][k], acc[ai][bj][m][n], 0, 0, 0); __builtin_amdgcn_s_setprio(0); } while (0)
; #define PG8_WAIT_V(n) asm volatile("s_waitcnt vmcnt(" #n ")" ::: "memory")
; #define PG8_BAR __builtin_amdgcn_s_barrier()
; template <class Epi, class Sched, bool ALIGN_EPI = false>
; __device__ __forceinline__ void gemm_phase(PG8_LAS unsigned char* lds, const Gemm g, const Sched& S, const Epi& E) {
;     ...
;         for (int t = 0; t < nt; t += 2) {
;             const bool last = (t == nt - 2);
;             const char* a1 = cA + (size_t)(t + 1) * kstep;
;             const char* a2 = last ? nA : cA + (size_t)(t + 2) * kstep; const char* b2 = last ? nB : cB + (size_t)(t + 2) * kstep;
;             const char* a3 = a2 + kstep; const char* b3 = b2 + kstep;
;             unsigned w0[2], w1[2];
; #pragma unroll
;             for (int i = 0; i < 2; ++i) { w0[i] = (Sched::GATHER && last) ? vn0[i] : vc0[i]; w1[i] = (Sched::GATHER && last) ? vn1[i] : vc1[i]; }
;             if (last && has_next) S.a_ready(nxt);
;             PG8_LDB(B0, 0, 0); PG8_LDB(B1, 0, 1); PG8_SCHED; PG8_LDA(At, 0, 0); PG8_STAGE(PG8_SA(1, 1), a1 + hstepA, vc1);
;             PG8_WAIT_V(8); PG8_WAIT_L(0); PG8_BAR; PG8_MMA(0, 0, At, B0); PG8_MMA(0, 1, At, B1); PG8_BAR; PG8_SCHED;
;             PG8_LDA(At, 0, 1); PG8_STAGE(PG8_SB(0, 0), b2, voffB); PG8_STAGE(PG8_SB(0, 1), b2 + hstep, voffB); PG8_STAGE(PG8_SA(0, 0), a2, w0);
.LBB0_805:
	ds_read_b128 v[142:145], v1
	ds_read_b128 v[158:161], v1 offset:1024
	ds_read_b128 v[162:165], v1 offset:2048
	ds_read_b128 v[166:169], v1 offset:3072
	ds_read_b128 v[170:173], v156
	ds_read_b128 v[174:177], v156 offset:1024
	ds_read_b128 v[178:181], v156 offset:2048
	ds_read_b128 v[182:185], v156 offset:3072
	s_add_u32 s62, s60, 0xfffe0080
	s_addc_u32 s63, s61, -1
	s_cmp_eq_u32 s92, 4
	s_cselect_b32 s65, s45, s63
	s_cselect_b32 s64, s57, s62
	s_cselect_b32 s63, s47, s91
	s_cselect_b32 s62, s89, s90
	v_lshl_add_u64 v[218:219], s[60:61], 0, v[140:141]
	s_add_i32 m0, s59, 0xc000
	ds_read_b128 v[186:189], v157
	ds_read_b128 v[190:193], v157 offset:1024
	ds_read_b128 v[194:197], v157 offset:2048
	ds_read_b128 v[198:201], v157 offset:3072
	ds_read_b128 v[202:205], v157 offset:4096
	ds_read_b128 v[206:209], v157 offset:5120
	ds_read_b128 v[210:213], v157 offset:6144
	ds_read_b128 v[214:217], v157 offset:7168
	global_load_lds_dwordx4 v[218:219], off
	v_lshl_add_u64 v[218:219], s[60:61], 0, v[138:139]
	s_add_i32 m0, s59, 0xe000
	s_nop 0
	global_load_lds_dwordx4 v[218:219], off
	s_waitcnt vmcnt(8)
	s_waitcnt lgkmcnt(0)
	s_barrier
	v_mfma_f32_16x16x32_bf16 v[126:129], v[142:145], v[186:189], v[126:129]
	v_mfma_f32_16x16x32_bf16 v[122:125], v[162:165], v[186:189], v[122:125]
	v_mfma_f32_16x16x32_bf16 v[114:117], v[142:145], v[194:197], v[114:117]
	v_mfma_f32_16x16x32_bf16 v[106:109], v[162:165], v[194:197], v[106:109]
	v_mfma_f32_16x16x32_bf16 v[98:101], v[142:145], v[202:205], v[98:101]
	v_mfma_f32_16x16x32_bf16 v[90:93], v[162:165], v[202:205], v[90:93]
	v_mfma_f32_16x16x32_bf16 v[82:85], v[142:145], v[210:213], v[82:85]
	v_mfma_f32_16x16x32_bf16 v[74:77], v[162:165], v[210:213], v[74:77]
	v_mfma_f32_16x16x32_bf16 v[126:129], v[158:161], v[190:193], v[126:129]
	v_mfma_f32_16x16x32_bf16 v[122:125], v[166:169], v[190:193], v[122:125]
	v_mfma_f32_16x16x32_bf16 v[114:117], v[158:161], v[198:201], v[114:117]
	v_mfma_f32_16x16x32_bf16 v[106:109], v[166:169], v[198:201], v[106:109]
	v_mfma_f32_16x16x32_bf16 v[98:101], v[158:161], v[206:209], v[98:101]
	v_mfma_f32_16x16x32_bf16 v[90:93], v[166:169], v[206:209], v[90:93]
	v_mfma_f32_16x16x32_bf16 v[82:85], v[158:161], v[214:217], v[82:85]
	v_mfma_f32_16x16x32_bf16 v[74:77], v[166:169], v[214:217], v[74:77]
	v_mfma_f32_16x16x32_bf16 v[118:121], v[170:173], v[186:189], v[118:121]
	v_mfma_f32_16x16x32_bf16 v[110:113], v[178:181], v[186:189], v[110:113]
	v_mfma_f32_16x16x32_bf16 v[102:105], v[170:173], v[194:197], v[102:105]
	v_mfma_f32_16x16x32_bf16 v[94:97], v[178:181], v[194:197], v[94:97]
	v_mfma_f32_16x16x32_bf16 v[86:89], v[170:173], v[202:205], v[86:89]
	v_mfma_f32_16x16x32_bf16 v[78:81], v[178:181], v[202:205], v[78:81]
	v_mfma_f32_16x16x32_bf16 v[62:65], v[170:173], v[210:213], v[62:65]
	v_mfma_f32_16x16x32_bf16 v[58:61], v[178:181], v[210:213], v[58:61]
	v_mfma_f32_16x16x32_bf16 v[118:121], v[174:177], v[190:193], v[118:121]
	v_mfma_f32_16x16x32_bf16 v[110:113], v[182:185], v[190:193], v[110:113]
	v_mfma_f32_16x16x32_bf16 v[102:105], v[174:177], v[198:201], v[102:105]
	v_mfma_f32_16x16x32_bf16 v[94:97], v[182:185], v[198:201], v[94:97]
	v_mfma_f32_16x16x32_bf16 v[86:89], v[174:177], v[206:209], v[86:89]
	v_mfma_f32_16x16x32_bf16 v[78:81], v[182:185], v[206:209], v[78:81]
	v_mfma_f32_16x16x32_bf16 v[62:65], v[174:177], v[214:217], v[62:65]
	v_mfma_f32_16x16x32_bf16 v[58:61], v[182:185], v[214:217], v[58:61]
	s_barrier
	s_add_i32 s93, s79, s66
	v_lshl_add_u64 v[218:219], s[62:63], 0, v[132:133]
	s_mov_b32 m0, s93
	ds_read_b128 v[186:189], v157 offset:16384
	ds_read_b128 v[190:193], v157 offset:17408
	ds_read_b128 v[194:197], v157 offset:18432
	ds_read_b128 v[198:201], v157 offset:19456
	ds_read_b128 v[202:205], v157 offset:20480
	ds_read_b128 v[206:209], v157 offset:21504
	ds_read_b128 v[210:213], v157 offset:22528
	ds_read_b128 v[214:217], v157 offset:23552
	global_load_lds_dwordx4 v[218:219], off
	s_add_i32 m0, s93, 0x2000
	s_add_u32 s94, s62, 0x20000
	v_lshl_add_u64 v[220:221], s[62:63], 0, v[136:137]
	s_addc_u32 s95, s63, 0
	s_add_i32 s93, s80, s66
	global_load_lds_dwordx4 v[220:221], off
	v_lshl_add_u64 v[222:223], s[94:95], 0, v[132:133]
	s_mov_b32 m0, s93
	v_lshl_add_u64 v[224:225], s[64:65], 0, v[134:135]
	global_load_lds_dwordx4 v[222:223], off
	v_lshl_add_u64 v[222:223], s[94:95], 0, v[136:137]
	s_add_i32 m0, s93, 0x2000
	s_nop 0
	global_load_lds_dwordx4 v[222:223], off
	v_lshl_add_u64 v[222:223], s[64:65], 0, v[130:131]
	s_mov_b32 m0, s59
	s_nop 0
	global_load_lds_dwordx4 v[222:223], off
	s_mov_b32 m0, s67
	s_nop 0
	global_load_lds_dwordx4 v[224:225], off
	s_waitcnt vmcnt(8)
	s_waitcnt lgkmcnt(0)
	s_barrier
; #define PG8_STAGE(bufoff, gbase, voff) do { _Pragma("unroll") for (int _i = 0; _i < 2; ++_i) \
;         __builtin_amdgcn_global_load_lds((const unsigned*)((const char*)(gbase) + (voff)[_i]), (PG8_LAS unsigned*)(lds + (bufoff) + ldsw + _i * 8192), 16, 0, 0); } while (0)
; #define PG8_LDA(dst, b, h) do { _Pragma("unroll") for (int m = 0; m < 4; ++m) _Pragma("unroll") for (int k = 0; k < 2; ++k) dst[m][k] = *(const PG8_LAS bf16x8*)(lds + PG8_SA(b, h) + aoff + m * 2048 + k * 1024); } while (0)
; #define PG8_LDB(dst, b, h) do { _Pragma("unroll") for (int n = 0; n < 2; ++n) _Pragma("unroll") for (int k = 0; k < 2; ++k) dst[n][k] = *(const PG8_LAS bf16x8*)(lds + PG8_SB(b, h) + boff + n * 2048 + k * 1024); } while (0)
; #define PG8_MMA(ai, bj, At, Bt) do { __builtin_amdgcn_s_setprio(1); _Pragma("unroll") for (int m = 0; m < 4; ++m) _Pragma("unroll") for (int n = 0; n < 2; ++n) _Pragma("unroll") for (int k = 0; k < 2; ++k) \
;         acc[ai][bj][m][n] = __builtin_amdgcn_mfma_f32_16x16x32_bf16(Bt[n][k], At[m][k], acc[ai][bj][m][n], 0, 0, 0); __builtin_amdgcn_s_setprio(0); } while (0)
; #define PG8_WAIT_V(n) asm volatile("s_waitcnt vmcnt(" #n ")" ::: "memory")
; #define PG8_WAIT_L(n) asm volatile("s_waitcnt lgkmcnt(" #n ")" ::: "memory")
; #define PG8_BAR __builtin_amdgcn_s_barrier()
; #define PG8_SCHED __builtin_amdgcn_sched_barrier(0)
; template <class Epi, class Sched, bool ALIGN_EPI = false>
; __device__ __forceinline__ void gemm_phase(PG8_LAS unsigned char* lds, const Gemm g, const Sched& S, const Epi& E) {
;     ...
;             PG8_WAIT_V(8); PG8_WAIT_L(0); PG8_BAR; PG8_MMA(1, 0, At, B0); PG8_MMA(1, 1, At, B1); PG8_BAR; PG8_SCHED;
;             PG8_LDB(B0, 1, 0); PG8_LDB(B1, 1, 1); PG8_SCHED; PG8_LDA(At, 1, 0); PG8_STAGE(PG8_SA(0, 1), a2 + hstepA, w1);
;             PG8_WAIT_V(8); PG8_WAIT_L(0); PG8_BAR; PG8_MMA(0, 0, At, B0); PG8_MMA(0, 1, At, B1); PG8_BAR; PG8_SCHED;
	v_mfma_f32_16x16x32_bf16 v[54:57], v[142:145], v[186:189], v[54:57]
	v_mfma_f32_16x16x32_bf16 v[42:45], v[162:165], v[186:189], v[42:45]
	v_mfma_f32_16x16x32_bf16 v[30:33], v[142:145], v[194:197], v[30:33]
	v_mfma_f32_16x16x32_bf16 v[26:29], v[162:165], v[194:197], v[26:29]
	v_mfma_f32_16x16x32_bf16 v[14:17], v[142:145], v[202:205], v[14:17]
	v_mfma_f32_16x16x32_bf16 v[10:13], v[162:165], v[202:205], v[10:13]
	v_mfma_f32_16x16x32_bf16 v[6:9], v[142:145], v[210:213], v[6:9]
	v_mfma_f32_16x16x32_bf16 v[2:5], v[162:165], v[210:213], v[2:5]
	v_mfma_f32_16x16x32_bf16 v[54:57], v[158:161], v[190:193], v[54:57]
	v_mfma_f32_16x16x32_bf16 v[42:45], v[166:169], v[190:193], v[42:45]
	v_mfma_f32_16x16x32_bf16 v[30:33], v[158:161], v[198:201], v[30:33]
	v_mfma_f32_16x16x32_bf16 v[26:29], v[166:169], v[198:201], v[26:29]
	v_mfma_f32_16x16x32_bf16 v[14:17], v[158:161], v[206:209], v[14:17]
	v_mfma_f32_16x16x32_bf16 v[10:13], v[166:169], v[206:209], v[10:13]
	v_mfma_f32_16x16x32_bf16 v[6:9], v[158:161], v[214:217], v[6:9]
	v_mfma_f32_16x16x32_bf16 v[2:5], v[166:169], v[214:217], v[2:5]
	v_mfma_f32_16x16x32_bf16 v[70:73], v[170:173], v[186:189], v[70:73]
	v_mfma_f32_16x16x32_bf16 v[66:69], v[178:181], v[186:189], v[66:69]
	v_mfma_f32_16x16x32_bf16 v[50:53], v[170:173], v[194:197], v[50:53]
	v_mfma_f32_16x16x32_bf16 v[46:49], v[178:181], v[194:197], v[46:49]
	v_mfma_f32_16x16x32_bf16 v[38:41], v[170:173], v[202:205], v[38:41]
	v_mfma_f32_16x16x32_bf16 v[34:37], v[178:181], v[202:205], v[34:37]
	v_mfma_f32_16x16x32_bf16 v[22:25], v[170:173], v[210:213], v[22:25]
	v_mfma_f32_16x16x32_bf16 v[18:21], v[178:181], v[210:213], v[18:21]
	v_mfma_f32_16x16x32_bf16 v[70:73], v[174:177], v[190:193], v[70:73]
	v_mfma_f32_16x16x32_bf16 v[66:69], v[182:185], v[190:193], v[66:69]
	v_mfma_f32_16x16x32_bf16 v[50:53], v[174:177], v[198:201], v[50:53]
	v_mfma_f32_16x16x32_bf16 v[46:49], v[182:185], v[198:201], v[46:49]
	v_mfma_f32_16x16x32_bf16 v[38:41], v[174:177], v[206:209], v[38:41]
	v_mfma_f32_16x16x32_bf16 v[34:37], v[182:185], v[206:209], v[34:37]
	v_mfma_f32_16x16x32_bf16 v[22:25], v[174:177], v[214:217], v[22:25]
	v_mfma_f32_16x16x32_bf16 v[18:21], v[182:185], v[214:217], v[18:21]
	s_barrier
	s_add_i32 s93, 0, 0x18000
	s_add_i32 s94, 0, 0x1c000
	v_add_u32_e32 v166, s93, v147
	v_add_u32_e32 v182, s94, v147
	ds_read_b128 v[142:145], v166
	ds_read_b128 v[158:161], v166 offset:1024
	ds_read_b128 v[162:165], v166 offset:2048
	ds_read_b128 v[166:169], v166 offset:3072
	ds_read_b128 v[170:173], v182
	ds_read_b128 v[174:177], v182 offset:1024
	ds_read_b128 v[178:181], v182 offset:2048
	ds_read_b128 v[182:185], v182 offset:3072
	s_add_u32 s64, s64, 0x20000
	s_addc_u32 s65, s65, 0
	s_mov_b32 m0, s68
	v_lshl_add_u64 v[226:227], s[64:65], 0, v[130:131]
	ds_read_b128 v[186:189], v157 offset:32768
	ds_read_b128 v[190:193], v157 offset:33792
	ds_read_b128 v[194:197], v157 offset:34816
	ds_read_b128 v[198:201], v157 offset:35840
	ds_read_b128 v[202:205], v157 offset:36864
	ds_read_b128 v[206:209], v157 offset:37888
	ds_read_b128 v[210:213], v157 offset:38912
	ds_read_b128 v[214:217], v157 offset:39936
	global_load_lds_dwordx4 v[226:227], off
	v_lshl_add_u64 v[226:227], s[64:65], 0, v[134:135]
	s_mov_b32 m0, s69
	s_nop 0
	global_load_lds_dwordx4 v[226:227], off
	s_waitcnt vmcnt(8)
	s_waitcnt lgkmcnt(0)
	s_barrier
	v_mfma_f32_16x16x32_bf16 v[126:129], v[142:145], v[186:189], v[126:129]
	v_mfma_f32_16x16x32_bf16 v[122:125], v[162:165], v[186:189], v[122:125]
	v_mfma_f32_16x16x32_bf16 v[114:117], v[142:145], v[194:197], v[114:117]
	v_mfma_f32_16x16x32_bf16 v[106:109], v[162:165], v[194:197], v[106:109]
	v_mfma_f32_16x16x32_bf16 v[98:101], v[142:145], v[202:205], v[98:101]
	v_mfma_f32_16x16x32_bf16 v[90:93], v[162:165], v[202:205], v[90:93]
	v_mfma_f32_16x16x32_bf16 v[82:85], v[142:145], v[210:213], v[82:85]
	v_mfma_f32_16x16x32_bf16 v[74:77], v[162:165], v[210:213], v[74:77]
	v_mfma_f32_16x16x32_bf16 v[126:129], v[158:161], v[190:193], v[126:129]
	v_mfma_f32_16x16x32_bf16 v[122:125], v[166:169], v[190:193], v[122:125]
	v_mfma_f32_16x16x32_bf16 v[114:117], v[158:161], v[198:201], v[114:117]
	v_mfma_f32_16x16x32_bf16 v[106:109], v[166:169], v[198:201], v[106:109]
	v_mfma_f32_16x16x32_bf16 v[98:101], v[158:161], v[206:209], v[98:101]
	v_mfma_f32_16x16x32_bf16 v[90:93], v[166:169], v[206:209], v[90:93]
	v_mfma_f32_16x16x32_bf16 v[82:85], v[158:161], v[214:217], v[82:85]
	v_mfma_f32_16x16x32_bf16 v[74:77], v[166:169], v[214:217], v[74:77]
	v_mfma_f32_16x16x32_bf16 v[118:121], v[170:173], v[186:189], v[118:121]
	v_mfma_f32_16x16x32_bf16 v[110:113], v[178:181], v[186:189], v[110:113]
	v_mfma_f32_16x16x32_bf16 v[102:105], v[170:173], v[194:197], v[102:105]
	v_mfma_f32_16x16x32_bf16 v[94:97], v[178:181], v[194:197], v[94:97]
	v_mfma_f32_16x16x32_bf16 v[86:89], v[170:173], v[202:205], v[86:89]
	v_mfma_f32_16x16x32_bf16 v[78:81], v[178:181], v[202:205], v[78:81]
	v_mfma_f32_16x16x32_bf16 v[62:65], v[170:173], v[210:213], v[62:65]
	v_mfma_f32_16x16x32_bf16 v[58:61], v[178:181], v[210:213], v[58:61]
	v_mfma_f32_16x16x32_bf16 v[118:121], v[174:177], v[190:193], v[118:121]
	v_mfma_f32_16x16x32_bf16 v[110:113], v[182:185], v[190:193], v[110:113]
	v_mfma_f32_16x16x32_bf16 v[102:105], v[174:177], v[198:201], v[102:105]
	v_mfma_f32_16x16x32_bf16 v[94:97], v[182:185], v[198:201], v[94:97]
	v_mfma_f32_16x16x32_bf16 v[86:89], v[174:177], v[206:209], v[86:89]
	v_mfma_f32_16x16x32_bf16 v[78:81], v[182:185], v[206:209], v[78:81]
	v_mfma_f32_16x16x32_bf16 v[62:65], v[174:177], v[214:217], v[62:65]
	v_mfma_f32_16x16x32_bf16 v[58:61], v[182:185], v[214:217], v[58:61]
	s_barrier
; #define PG8_STAGE(bufoff, gbase, voff) do { _Pragma("unroll") for (int _i = 0; _i < 2; ++_i) \
;         __builtin_amdgcn_global_load_lds((const unsigned*)((const char*)(gbase) + (voff)[_i]), (PG8_LAS unsigned*)(lds + (bufoff) + ldsw + _i * 8192), 16, 0, 0); } while (0)
; #define PG8_LDA(dst, b, h) do { _Pragma("unroll") for (int m = 0; m < 4; ++m) _Pragma("unroll") for (int k = 0; k < 2; ++k) dst[m][k] = *(const PG8_LAS bf16x8*)(lds + PG8_SA(b, h) + aoff + m * 2048 + k * 1024); } while (0)
; #define PG8_MMA(ai, bj, At, Bt) do { __builtin_amdgcn_s_setprio(1); _Pragma("unroll") for (int m = 0; m < 4; ++m) _Pragma("unroll") for (int n = 0; n < 2; ++n) _Pragma("unroll") for (int k = 0; k < 2; ++k) \
;         acc[ai][bj][m][n] = __builtin_amdgcn_mfma_f32_16x16x32_bf16(Bt[n][k], At[m][k], acc[ai][bj][m][n], 0, 0, 0); __builtin_amdgcn_s_setprio(0); } while (0)
; #define PG8_WAIT_V(n) asm volatile("s_waitcnt vmcnt(" #n ")" ::: "memory")
; #define PG8_WAIT_L(n) asm volatile("s_waitcnt lgkmcnt(" #n ")" ::: "memory")
; #define PG8_BAR __builtin_amdgcn_s_barrier()
; #define PG8_SCHED __builtin_amdgcn_sched_barrier(0)
; template <class Epi, class Sched, bool ALIGN_EPI = false>
; __device__ __forceinline__ void gemm_phase(PG8_LAS unsigned char* lds, const Gemm g, const Sched& S, const Epi& E) {
;     ...
;             PG8_LDA(At, 1, 1); PG8_STAGE(PG8_SB(1, 0), b3, voffB); PG8_STAGE(PG8_SB(1, 1), b3 + hstep, voffB); PG8_STAGE(PG8_SA(1, 0), a3, w0);
;             PG8_WAIT_V(8); PG8_WAIT_L(0); PG8_BAR; PG8_MMA(1, 0, At, B0); PG8_MMA(1, 1, At, B1); PG8_BAR; PG8_SCHED;
;             if constexpr (Epi::KSCALE) { if (((t + 2) & 7) == 0 && t + 2 < nt) { E.kscale(acc, pf, ((t + 2) >> 3) - 1, wr, fr); PG8_SCHED; } }
;         }
;         if constexpr (ALIGN_EPI) { if (wr == 0) PG8_BAR; }
	s_add_i32 s64, s93, s66
	v_lshl_add_u64 v[218:219], v[218:219], 0, s[18:19]
	s_mov_b32 m0, s64
	ds_read_b128 v[186:189], v157 offset:49152
	ds_read_b128 v[190:193], v157 offset:50176
	ds_read_b128 v[194:197], v157 offset:51200
	ds_read_b128 v[198:201], v157 offset:52224
	ds_read_b128 v[202:205], v157 offset:53248
	ds_read_b128 v[206:209], v157 offset:54272
	ds_read_b128 v[210:213], v157 offset:55296
	ds_read_b128 v[214:217], v157 offset:56320
	global_load_lds_dwordx4 v[218:219], off
	s_add_i32 m0, s64, 0x2000
	s_add_u32 s62, s62, 0x20080
	v_lshl_add_u64 v[218:219], v[220:221], 0, s[18:19]
	s_addc_u32 s63, s63, 0
	s_add_i32 s64, s94, s66
	global_load_lds_dwordx4 v[218:219], off
	v_lshl_add_u64 v[218:219], s[62:63], 0, v[132:133]
	s_mov_b32 m0, s64
	s_nop 0
	global_load_lds_dwordx4 v[218:219], off
	v_lshl_add_u64 v[218:219], s[62:63], 0, v[136:137]
	s_add_i32 m0, s64, 0x2000
	s_nop 0
	global_load_lds_dwordx4 v[218:219], off
	v_lshl_add_u64 v[218:219], v[222:223], 0, s[18:19]
	s_mov_b32 m0, s73
	s_nop 0
	global_load_lds_dwordx4 v[218:219], off
	v_lshl_add_u64 v[218:219], v[224:225], 0, s[18:19]
	s_mov_b32 m0, s74
	s_nop 0
	global_load_lds_dwordx4 v[218:219], off
	s_waitcnt vmcnt(8)
	s_waitcnt lgkmcnt(0)
	s_barrier
	v_mfma_f32_16x16x32_bf16 v[54:57], v[142:145], v[186:189], v[54:57]
	v_mfma_f32_16x16x32_bf16 v[42:45], v[162:165], v[186:189], v[42:45]
	v_mfma_f32_16x16x32_bf16 v[30:33], v[142:145], v[194:197], v[30:33]
	v_mfma_f32_16x16x32_bf16 v[26:29], v[162:165], v[194:197], v[26:29]
	v_mfma_f32_16x16x32_bf16 v[14:17], v[142:145], v[202:205], v[14:17]
	v_mfma_f32_16x16x32_bf16 v[10:13], v[162:165], v[202:205], v[10:13]
	v_mfma_f32_16x16x32_bf16 v[6:9], v[142:145], v[210:213], v[6:9]
	v_mfma_f32_16x16x32_bf16 v[2:5], v[162:165], v[210:213], v[2:5]
	v_mfma_f32_16x16x32_bf16 v[54:57], v[158:161], v[190:193], v[54:57]
	v_mfma_f32_16x16x32_bf16 v[42:45], v[166:169], v[190:193], v[42:45]
	v_mfma_f32_16x16x32_bf16 v[30:33], v[158:161], v[198:201], v[30:33]
	v_mfma_f32_16x16x32_bf16 v[26:29], v[166:169], v[198:201], v[26:29]
	v_mfma_f32_16x16x32_bf16 v[14:17], v[158:161], v[206:209], v[14:17]
	v_mfma_f32_16x16x32_bf16 v[10:13], v[166:169], v[206:209], v[10:13]
	v_mfma_f32_16x16x32_bf16 v[6:9], v[158:161], v[214:217], v[6:9]
	v_mfma_f32_16x16x32_bf16 v[2:5], v[166:169], v[214:217], v[2:5]
	v_mfma_f32_16x16x32_bf16 v[70:73], v[170:173], v[186:189], v[70:73]
	v_mfma_f32_16x16x32_bf16 v[66:69], v[178:181], v[186:189], v[66:69]
	v_mfma_f32_16x16x32_bf16 v[50:53], v[170:173], v[194:197], v[50:53]
	v_mfma_f32_16x16x32_bf16 v[46:49], v[178:181], v[194:197], v[46:49]
	v_mfma_f32_16x16x32_bf16 v[38:41], v[170:173], v[202:205], v[38:41]
	v_mfma_f32_16x16x32_bf16 v[34:37], v[178:181], v[202:205], v[34:37]
	v_mfma_f32_16x16x32_bf16 v[22:25], v[170:173], v[210:213], v[22:25]
	v_mfma_f32_16x16x32_bf16 v[18:21], v[178:181], v[210:213], v[18:21]
	v_mfma_f32_16x16x32_bf16 v[70:73], v[174:177], v[190:193], v[70:73]
	v_mfma_f32_16x16x32_bf16 v[66:69], v[182:185], v[190:193], v[66:69]
	v_mfma_f32_16x16x32_bf16 v[50:53], v[174:177], v[198:201], v[50:53]
	v_mfma_f32_16x16x32_bf16 v[46:49], v[182:185], v[198:201], v[46:49]
	v_mfma_f32_16x16x32_bf16 v[38:41], v[174:177], v[206:209], v[38:41]
	v_mfma_f32_16x16x32_bf16 v[34:37], v[182:185], v[206:209], v[34:37]
	v_mfma_f32_16x16x32_bf16 v[22:25], v[174:177], v[214:217], v[22:25]
	v_mfma_f32_16x16x32_bf16 v[18:21], v[182:185], v[214:217], v[18:21]
	s_barrier
	s_add_i32 s92, s92, 2
	s_add_u32 s90, s90, 0x100
	s_addc_u32 s91, s91, 0
	s_add_u32 s60, s60, 0x100
	s_addc_u32 s61, s61, 0
	s_cmp_gt_u32 s92, 5
	s_cbranch_scc0 .LBB0_805
	s_and_b64 vcc, exec, s[22:23]
	s_cbranch_vccz .LBB0_808
	s_barrier

; #define PG8_STAGE(bufoff, gbase, voff) do { _Pragma("unroll") for (int _i = 0; _i < 2; ++_i) \
;         __builtin_amdgcn_global_load_lds((const unsigned*)((const char*)(gbase) + (voff)[_i]), (PG8_LAS unsigned*)(lds + (bufoff) + ldsw + _i * 8192), 16, 0, 0); } while (0)
; #define PG8_LDA(dst, b, h) do { _Pragma("unroll") for (int m = 0; m < 4; ++m) _Pragma("unroll") for (int k = 0; k < 2; ++k) dst[m][k] = *(const PG8_LAS bf16x8*)(lds + PG8_SA(b, h) + aoff + m * 2048 + k * 1024); } while (0)
; #define PG8_LDB(dst, b, h) do { _Pragma("unroll") for (int n = 0; n < 2; ++n) _Pragma("unroll") for (int k = 0; k < 2; ++k) dst[n][k] = *(const PG8_LAS bf16x8*)(lds + PG8_SB(b, h) + boff + n * 2048 + k * 1024); } while (0)
; #define PG8_MMA(ai, bj, At, Bt) do { __builtin_amdgcn_s_setprio(1); _Pragma("unroll") for (int m = 0; m < 4; ++m) _Pragma("unroll") for (int n = 0; n < 2; ++n) _Pragma("unroll") for (int k = 0; k < 2; ++k) \
;         acc[ai][bj][m][n] = __builtin_amdgcn_mfma_f32_16x16x32_bf16(Bt[n][k], At[m][k], acc[ai][bj][m][n], 0, 0, 0); __builtin_amdgcn_s_setprio(0); } while (0)
; #define PG8_WAIT_V(n) asm volatile("s_waitcnt vmcnt(" #n ")" ::: "memory")
; #define PG8_WAIT_L(n) asm volatile("s_waitcnt lgkmcnt(" #n ")" ::: "memory")
; #define PG8_BAR __builtin_amdgcn_s_barrier()
; #define PG8_SCHED __builtin_amdgcn_sched_barrier(0)
; template <class Epi, class Sched, bool ALIGN_EPI = false>
; __device__ __forceinline__ void gemm_phase(PG8_LAS unsigned char* lds, const Gemm g, const Sched& S, const Epi& E) {
;     ...
;             PG8_LDB(B0, 0, 0); PG8_LDB(B1, 0, 1); PG8_SCHED; PG8_LDA(At, 0, 0); PG8_STAGE(PG8_SA(1, 1), a1 + hstepA, vc1);
;             PG8_WAIT_V(8); PG8_WAIT_L(0); PG8_BAR; PG8_MMA(0, 0, At, B0); PG8_MMA(0, 1, At, B1); PG8_BAR; PG8_SCHED;
;             PG8_LDA(At, 0, 1); PG8_STAGE(PG8_SB(0, 0), b2, voffB); PG8_STAGE(PG8_SB(0, 1), b2 + hstep, voffB); PG8_STAGE(PG8_SA(0, 0), a2, w0);
;             PG8_WAIT_V(8); PG8_WAIT_L(0); PG8_BAR; PG8_MMA(1, 0, At, B0); PG8_MMA(1, 1, At, B1); PG8_BAR; PG8_SCHED;
.LBB0_908:
	ds_read_b128 v[144:147], v157
	ds_read_b128 v[160:163], v157 offset:1024
	ds_read_b128 v[164:167], v157 offset:2048
	ds_read_b128 v[168:171], v157 offset:3072
	ds_read_b128 v[172:175], v158
	ds_read_b128 v[176:179], v158 offset:1024
	ds_read_b128 v[180:183], v158 offset:2048
	ds_read_b128 v[184:187], v158 offset:3072
	s_add_u32 s58, s56, 0xfffe0080
	s_addc_u32 s59, s57, -1
	s_cmp_eq_u32 s92, 4
	s_cselect_b32 s61, s41, s59
	s_cselect_b32 s60, s47, s58
	s_cselect_b32 s59, s43, s91
	s_cselect_b32 s58, s89, s90
	v_lshl_add_u64 v[220:221], s[56:57], 0, v[142:143]
	s_add_i32 m0, s49, 0xc000
	ds_read_b128 v[188:191], v159
	ds_read_b128 v[192:195], v159 offset:1024
	ds_read_b128 v[196:199], v159 offset:2048
	ds_read_b128 v[200:203], v159 offset:3072
	ds_read_b128 v[204:207], v159 offset:4096
	ds_read_b128 v[208:211], v159 offset:5120
	ds_read_b128 v[212:215], v159 offset:6144
	ds_read_b128 v[216:219], v159 offset:7168
	global_load_lds_dwordx4 v[220:221], off
	v_lshl_add_u64 v[220:221], s[56:57], 0, v[140:141]
	s_add_i32 m0, s49, 0xe000
	s_nop 0
	global_load_lds_dwordx4 v[220:221], off
	s_waitcnt vmcnt(8)
	s_waitcnt lgkmcnt(0)
	s_barrier
	v_mfma_f32_16x16x32_bf16 v[126:129], v[144:147], v[188:191], v[126:129]
	v_mfma_f32_16x16x32_bf16 v[122:125], v[164:167], v[188:191], v[122:125]
	v_mfma_f32_16x16x32_bf16 v[114:117], v[144:147], v[196:199], v[114:117]
	v_mfma_f32_16x16x32_bf16 v[106:109], v[164:167], v[196:199], v[106:109]
	v_mfma_f32_16x16x32_bf16 v[98:101], v[144:147], v[204:207], v[98:101]
	v_mfma_f32_16x16x32_bf16 v[90:93], v[164:167], v[204:207], v[90:93]
	v_mfma_f32_16x16x32_bf16 v[82:85], v[144:147], v[212:215], v[82:85]
	v_mfma_f32_16x16x32_bf16 v[74:77], v[164:167], v[212:215], v[74:77]
	v_mfma_f32_16x16x32_bf16 v[126:129], v[160:163], v[192:195], v[126:129]
	v_mfma_f32_16x16x32_bf16 v[122:125], v[168:171], v[192:195], v[122:125]
	v_mfma_f32_16x16x32_bf16 v[114:117], v[160:163], v[200:203], v[114:117]
	v_mfma_f32_16x16x32_bf16 v[106:109], v[168:171], v[200:203], v[106:109]
	v_mfma_f32_16x16x32_bf16 v[98:101], v[160:163], v[208:211], v[98:101]
	v_mfma_f32_16x16x32_bf16 v[90:93], v[168:171], v[208:211], v[90:93]
	v_mfma_f32_16x16x32_bf16 v[82:85], v[160:163], v[216:219], v[82:85]
	v_mfma_f32_16x16x32_bf16 v[74:77], v[168:171], v[216:219], v[74:77]
	v_mfma_f32_16x16x32_bf16 v[118:121], v[172:175], v[188:191], v[118:121]
	v_mfma_f32_16x16x32_bf16 v[110:113], v[180:183], v[188:191], v[110:113]
	v_mfma_f32_16x16x32_bf16 v[102:105], v[172:175], v[196:199], v[102:105]
	v_mfma_f32_16x16x32_bf16 v[94:97], v[180:183], v[196:199], v[94:97]
	v_mfma_f32_16x16x32_bf16 v[86:89], v[172:175], v[204:207], v[86:89]
	v_mfma_f32_16x16x32_bf16 v[78:81], v[180:183], v[204:207], v[78:81]
	v_mfma_f32_16x16x32_bf16 v[62:65], v[172:175], v[212:215], v[62:65]
	v_mfma_f32_16x16x32_bf16 v[58:61], v[180:183], v[212:215], v[58:61]
	v_mfma_f32_16x16x32_bf16 v[118:121], v[176:179], v[192:195], v[118:121]
	v_mfma_f32_16x16x32_bf16 v[110:113], v[184:187], v[192:195], v[110:113]
	v_mfma_f32_16x16x32_bf16 v[102:105], v[176:179], v[200:203], v[102:105]
	v_mfma_f32_16x16x32_bf16 v[94:97], v[184:187], v[200:203], v[94:97]
	v_mfma_f32_16x16x32_bf16 v[86:89], v[176:179], v[208:211], v[86:89]
	v_mfma_f32_16x16x32_bf16 v[78:81], v[184:187], v[208:211], v[78:81]
	v_mfma_f32_16x16x32_bf16 v[62:65], v[176:179], v[216:219], v[62:65]
	v_mfma_f32_16x16x32_bf16 v[58:61], v[184:187], v[216:219], v[58:61]
	s_barrier
	s_add_i32 s93, s79, s66
	v_lshl_add_u64 v[220:221], s[58:59], 0, v[134:135]
	s_mov_b32 m0, s93
	ds_read_b128 v[188:191], v159 offset:16384
	ds_read_b128 v[192:195], v159 offset:17408
	ds_read_b128 v[196:199], v159 offset:18432
	ds_read_b128 v[200:203], v159 offset:19456
	ds_read_b128 v[204:207], v159 offset:20480
	ds_read_b128 v[208:211], v159 offset:21504
	ds_read_b128 v[212:215], v159 offset:22528
	ds_read_b128 v[216:219], v159 offset:23552
	global_load_lds_dwordx4 v[220:221], off
	s_add_i32 m0, s93, 0x2000
	s_add_u32 s94, s58, 0x20000
	v_lshl_add_u64 v[222:223], s[58:59], 0, v[138:139]
	s_addc_u32 s95, s59, 0
	s_add_i32 s93, s80, s66
	global_load_lds_dwordx4 v[222:223], off
	v_lshl_add_u64 v[224:225], s[94:95], 0, v[134:135]
	s_mov_b32 m0, s93
	v_lshl_add_u64 v[226:227], s[60:61], 0, v[136:137]
	global_load_lds_dwordx4 v[224:225], off
	v_lshl_add_u64 v[224:225], s[94:95], 0, v[138:139]
	s_add_i32 m0, s93, 0x2000
	s_nop 0
	global_load_lds_dwordx4 v[224:225], off
	v_lshl_add_u64 v[224:225], s[60:61], 0, v[132:133]
	s_mov_b32 m0, s49
	s_nop 0
	global_load_lds_dwordx4 v[224:225], off
	s_mov_b32 m0, s67
	s_nop 0
	global_load_lds_dwordx4 v[226:227], off
	s_waitcnt vmcnt(8)
	s_waitcnt lgkmcnt(0)
	s_barrier
; #define PG8_STAGE(bufoff, gbase, voff) do { _Pragma("unroll") for (int _i = 0; _i < 2; ++_i) \
;         __builtin_amdgcn_global_load_lds((const unsigned*)((const char*)(gbase) + (voff)[_i]), (PG8_LAS unsigned*)(lds + (bufoff) + ldsw + _i * 8192), 16, 0, 0); } while (0)
; #define PG8_LDA(dst, b, h) do { _Pragma("unroll") for (int m = 0; m < 4; ++m) _Pragma("unroll") for (int k = 0; k < 2; ++k) dst[m][k] = *(const PG8_LAS bf16x8*)(lds + PG8_SA(b, h) + aoff + m * 2048 + k * 1024); } while (0)
; #define PG8_LDB(dst, b, h) do { _Pragma("unroll") for (int n = 0; n < 2; ++n) _Pragma("unroll") for (int k = 0; k < 2; ++k) dst[n][k] = *(const PG8_LAS bf16x8*)(lds + PG8_SB(b, h) + boff + n * 2048 + k * 1024); } while (0)
; #define PG8_MMA(ai, bj, At, Bt) do { __builtin_amdgcn_s_setprio(1); _Pragma("unroll") for (int m = 0; m < 4; ++m) _Pragma("unroll") for (int n = 0; n < 2; ++n) _Pragma("unroll") for (int k = 0; k < 2; ++k) \
;         acc[ai][bj][m][n] = __builtin_amdgcn_mfma_f32_16x16x32_bf16(Bt[n][k], At[m][k], acc[ai][bj][m][n], 0, 0, 0); __builtin_amdgcn_s_setprio(0); } while (0)
; #define PG8_WAIT_V(n) asm volatile("s_waitcnt vmcnt(" #n ")" ::: "memory")
; #define PG8_WAIT_L(n) asm volatile("s_waitcnt lgkmcnt(" #n ")" ::: "memory")
; #define PG8_BAR __builtin_amdgcn_s_barrier()
; #define PG8_SCHED __builtin_amdgcn_sched_barrier(0)
; template <class Epi, class Sched, bool ALIGN_EPI = false>
; __device__ __forceinline__ void gemm_phase(PG8_LAS unsigned char* lds, const Gemm g, const Sched& S, const Epi& E) {
;     ...
;             PG8_WAIT_V(8); PG8_WAIT_L(0); PG8_BAR; PG8_MMA(1, 0, At, B0); PG8_MMA(1, 1, At, B1); PG8_BAR; PG8_SCHED;
;             PG8_LDB(B0, 1, 0); PG8_LDB(B1, 1, 1); PG8_SCHED; PG8_LDA(At, 1, 0); PG8_STAGE(PG8_SA(0, 1), a2 + hstepA, w1);
;             PG8_WAIT_V(8); PG8_WAIT_L(0); PG8_BAR; PG8_MMA(0, 0, At, B0); PG8_MMA(0, 1, At, B1); PG8_BAR; PG8_SCHED;
	v_mfma_f32_16x16x32_bf16 v[54:57], v[144:147], v[188:191], v[54:57]
	v_mfma_f32_16x16x32_bf16 v[42:45], v[164:167], v[188:191], v[42:45]
	v_mfma_f32_16x16x32_bf16 v[30:33], v[144:147], v[196:199], v[30:33]
	v_mfma_f32_16x16x32_bf16 v[26:29], v[164:167], v[196:199], v[26:29]
	v_mfma_f32_16x16x32_bf16 v[14:17], v[144:147], v[204:207], v[14:17]
	v_mfma_f32_16x16x32_bf16 v[10:13], v[164:167], v[204:207], v[10:13]
	v_mfma_f32_16x16x32_bf16 v[6:9], v[144:147], v[212:215], v[6:9]
	v_mfma_f32_16x16x32_bf16 v[2:5], v[164:167], v[212:215], v[2:5]
	v_mfma_f32_16x16x32_bf16 v[54:57], v[160:163], v[192:195], v[54:57]
	v_mfma_f32_16x16x32_bf16 v[42:45], v[168:171], v[192:195], v[42:45]
	v_mfma_f32_16x16x32_bf16 v[30:33], v[160:163], v[200:203], v[30:33]
	v_mfma_f32_16x16x32_bf16 v[26:29], v[168:171], v[200:203], v[26:29]
	v_mfma_f32_16x16x32_bf16 v[14:17], v[160:163], v[208:211], v[14:17]
	v_mfma_f32_16x16x32_bf16 v[10:13], v[168:171], v[208:211], v[10:13]
	v_mfma_f32_16x16x32_bf16 v[6:9], v[160:163], v[216:219], v[6:9]
	v_mfma_f32_16x16x32_bf16 v[2:5], v[168:171], v[216:219], v[2:5]
	v_mfma_f32_16x16x32_bf16 v[70:73], v[172:175], v[188:191], v[70:73]
	v_mfma_f32_16x16x32_bf16 v[66:69], v[180:183], v[188:191], v[66:69]
	v_mfma_f32_16x16x32_bf16 v[50:53], v[172:175], v[196:199], v[50:53]
	v_mfma_f32_16x16x32_bf16 v[46:49], v[180:183], v[196:199], v[46:49]
	v_mfma_f32_16x16x32_bf16 v[38:41], v[172:175], v[204:207], v[38:41]
	v_mfma_f32_16x16x32_bf16 v[34:37], v[180:183], v[204:207], v[34:37]
	v_mfma_f32_16x16x32_bf16 v[22:25], v[172:175], v[212:215], v[22:25]
	v_mfma_f32_16x16x32_bf16 v[18:21], v[180:183], v[212:215], v[18:21]
	v_mfma_f32_16x16x32_bf16 v[70:73], v[176:179], v[192:195], v[70:73]
	v_mfma_f32_16x16x32_bf16 v[66:69], v[184:187], v[192:195], v[66:69]
	v_mfma_f32_16x16x32_bf16 v[50:53], v[176:179], v[200:203], v[50:53]
	v_mfma_f32_16x16x32_bf16 v[46:49], v[184:187], v[200:203], v[46:49]
	v_mfma_f32_16x16x32_bf16 v[38:41], v[176:179], v[208:211], v[38:41]
	v_mfma_f32_16x16x32_bf16 v[34:37], v[184:187], v[208:211], v[34:37]
	v_mfma_f32_16x16x32_bf16 v[22:25], v[176:179], v[216:219], v[22:25]
	v_mfma_f32_16x16x32_bf16 v[18:21], v[184:187], v[216:219], v[18:21]
	s_barrier
	s_add_i32 s93, 0, 0x18000
	s_add_i32 s94, 0, 0x1c000
	v_add_u32_e32 v168, s93, v148
	v_add_u32_e32 v184, s94, v148
	ds_read_b128 v[144:147], v168
	ds_read_b128 v[160:163], v168 offset:1024
	ds_read_b128 v[164:167], v168 offset:2048
	ds_read_b128 v[168:171], v168 offset:3072
	ds_read_b128 v[172:175], v184
	ds_read_b128 v[176:179], v184 offset:1024
	ds_read_b128 v[180:183], v184 offset:2048
	ds_read_b128 v[184:187], v184 offset:3072
	s_add_u32 s60, s60, 0x20000
	s_addc_u32 s61, s61, 0
	s_mov_b32 m0, s68
	v_lshl_add_u64 v[228:229], s[60:61], 0, v[132:133]
	ds_read_b128 v[188:191], v159 offset:32768
	ds_read_b128 v[192:195], v159 offset:33792
	ds_read_b128 v[196:199], v159 offset:34816
	ds_read_b128 v[200:203], v159 offset:35840
	ds_read_b128 v[204:207], v159 offset:36864
	ds_read_b128 v[208:211], v159 offset:37888
	ds_read_b128 v[212:215], v159 offset:38912
	ds_read_b128 v[216:219], v159 offset:39936
	global_load_lds_dwordx4 v[228:229], off
	v_lshl_add_u64 v[228:229], s[60:61], 0, v[136:137]
	s_mov_b32 m0, s69
	s_nop 0
	global_load_lds_dwordx4 v[228:229], off
	s_waitcnt vmcnt(8)
	s_waitcnt lgkmcnt(0)
	s_barrier
	v_mfma_f32_16x16x32_bf16 v[126:129], v[144:147], v[188:191], v[126:129]
	v_mfma_f32_16x16x32_bf16 v[122:125], v[164:167], v[188:191], v[122:125]
	v_mfma_f32_16x16x32_bf16 v[114:117], v[144:147], v[196:199], v[114:117]
	v_mfma_f32_16x16x32_bf16 v[106:109], v[164:167], v[196:199], v[106:109]
	v_mfma_f32_16x16x32_bf16 v[98:101], v[144:147], v[204:207], v[98:101]
	v_mfma_f32_16x16x32_bf16 v[90:93], v[164:167], v[204:207], v[90:93]
	v_mfma_f32_16x16x32_bf16 v[82:85], v[144:147], v[212:215], v[82:85]
	v_mfma_f32_16x16x32_bf16 v[74:77], v[164:167], v[212:215], v[74:77]
	v_mfma_f32_16x16x32_bf16 v[126:129], v[160:163], v[192:195], v[126:129]
	v_mfma_f32_16x16x32_bf16 v[122:125], v[168:171], v[192:195], v[122:125]
	v_mfma_f32_16x16x32_bf16 v[114:117], v[160:163], v[200:203], v[114:117]
	v_mfma_f32_16x16x32_bf16 v[106:109], v[168:171], v[200:203], v[106:109]
	v_mfma_f32_16x16x32_bf16 v[98:101], v[160:163], v[208:211], v[98:101]
	v_mfma_f32_16x16x32_bf16 v[90:93], v[168:171], v[208:211], v[90:93]
	v_mfma_f32_16x16x32_bf16 v[82:85], v[160:163], v[216:219], v[82:85]
	v_mfma_f32_16x16x32_bf16 v[74:77], v[168:171], v[216:219], v[74:77]
	v_mfma_f32_16x16x32_bf16 v[118:121], v[172:175], v[188:191], v[118:121]
	v_mfma_f32_16x16x32_bf16 v[110:113], v[180:183], v[188:191], v[110:113]
	v_mfma_f32_16x16x32_bf16 v[102:105], v[172:175], v[196:199], v[102:105]
	v_mfma_f32_16x16x32_bf16 v[94:97], v[180:183], v[196:199], v[94:97]
	v_mfma_f32_16x16x32_bf16 v[86:89], v[172:175], v[204:207], v[86:89]
	v_mfma_f32_16x16x32_bf16 v[78:81], v[180:183], v[204:207], v[78:81]
	v_mfma_f32_16x16x32_bf16 v[62:65], v[172:175], v[212:215], v[62:65]
	v_mfma_f32_16x16x32_bf16 v[58:61], v[180:183], v[212:215], v[58:61]
	v_mfma_f32_16x16x32_bf16 v[118:121], v[176:179], v[192:195], v[118:121]
	v_mfma_f32_16x16x32_bf16 v[110:113], v[184:187], v[192:195], v[110:113]
	v_mfma_f32_16x16x32_bf16 v[102:105], v[176:179], v[200:203], v[102:105]
	v_mfma_f32_16x16x32_bf16 v[94:97], v[184:187], v[200:203], v[94:97]
	v_mfma_f32_16x16x32_bf16 v[86:89], v[176:179], v[208:211], v[86:89]
	v_mfma_f32_16x16x32_bf16 v[78:81], v[184:187], v[208:211], v[78:81]
	v_mfma_f32_16x16x32_bf16 v[62:65], v[176:179], v[216:219], v[62:65]
	v_mfma_f32_16x16x32_bf16 v[58:61], v[184:187], v[216:219], v[58:61]
	s_barrier
; #define PG8_STAGE(bufoff, gbase, voff) do { _Pragma("unroll") for (int _i = 0; _i < 2; ++_i) \
;         __builtin_amdgcn_global_load_lds((const unsigned*)((const char*)(gbase) + (voff)[_i]), (PG8_LAS unsigned*)(lds + (bufoff) + ldsw + _i * 8192), 16, 0, 0); } while (0)
; #define PG8_LDA(dst, b, h) do { _Pragma("unroll") for (int m = 0; m < 4; ++m) _Pragma("unroll") for (int k = 0; k < 2; ++k) dst[m][k] = *(const PG8_LAS bf16x8*)(lds + PG8_SA(b, h) + aoff + m * 2048 + k * 1024); } while (0)
; #define PG8_MMA(ai, bj, At, Bt) do { __builtin_amdgcn_s_setprio(1); _Pragma("unroll") for (int m = 0; m < 4; ++m) _Pragma("unroll") for (int n = 0; n < 2; ++n) _Pragma("unroll") for (int k = 0; k < 2; ++k) \
;         acc[ai][bj][m][n] = __builtin_amdgcn_mfma_f32_16x16x32_bf16(Bt[n][k], At[m][k], acc[ai][bj][m][n], 0, 0, 0); __builtin_amdgcn_s_setprio(0); } while (0)
; #define PG8_WAIT_V(n) asm volatile("s_waitcnt vmcnt(" #n ")" ::: "memory")
; #define PG8_WAIT_L(n) asm volatile("s_waitcnt lgkmcnt(" #n ")" ::: "memory")
; #define PG8_BAR __builtin_amdgcn_s_barrier()
; #define PG8_SCHED __builtin_amdgcn_sched_barrier(0)
; template <class Epi, class Sched, bool ALIGN_EPI = false>
; __device__ __forceinline__ void gemm_phase(PG8_LAS unsigned char* lds, const Gemm g, const Sched& S, const Epi& E) {
;     ...
;             PG8_LDA(At, 1, 1); PG8_STAGE(PG8_SB(1, 0), b3, voffB); PG8_STAGE(PG8_SB(1, 1), b3 + hstep, voffB); PG8_STAGE(PG8_SA(1, 0), a3, w0);
;             PG8_WAIT_V(8); PG8_WAIT_L(0); PG8_BAR; PG8_MMA(1, 0, At, B0); PG8_MMA(1, 1, At, B1); PG8_BAR; PG8_SCHED;
;             if constexpr (Epi::KSCALE) { if (((t + 2) & 7) == 0 && t + 2 < nt) { E.kscale(acc, pf, ((t + 2) >> 3) - 1, wr, fr); PG8_SCHED; } }
;         }
;         if constexpr (ALIGN_EPI) { if (wr == 0) PG8_BAR; }
	s_add_i32 s60, s93, s66
	v_lshl_add_u64 v[220:221], v[220:221], 0, s[14:15]
	s_mov_b32 m0, s60
	ds_read_b128 v[188:191], v159 offset:49152
	ds_read_b128 v[192:195], v159 offset:50176
	ds_read_b128 v[196:199], v159 offset:51200
	ds_read_b128 v[200:203], v159 offset:52224
	ds_read_b128 v[204:207], v159 offset:53248
	ds_read_b128 v[208:211], v159 offset:54272
	ds_read_b128 v[212:215], v159 offset:55296
	ds_read_b128 v[216:219], v159 offset:56320
	global_load_lds_dwordx4 v[220:221], off
	s_add_i32 m0, s60, 0x2000
	s_add_u32 s58, s58, 0x20080
	v_lshl_add_u64 v[220:221], v[222:223], 0, s[14:15]
	s_addc_u32 s59, s59, 0
	s_add_i32 s60, s94, s66
	global_load_lds_dwordx4 v[220:221], off
	v_lshl_add_u64 v[220:221], s[58:59], 0, v[134:135]
	s_mov_b32 m0, s60
	s_nop 0
	global_load_lds_dwordx4 v[220:221], off
	v_lshl_add_u64 v[220:221], s[58:59], 0, v[138:139]
	s_add_i32 m0, s60, 0x2000
	s_nop 0
	global_load_lds_dwordx4 v[220:221], off
	v_lshl_add_u64 v[220:221], v[224:225], 0, s[14:15]
	s_mov_b32 m0, s74
	s_nop 0
	global_load_lds_dwordx4 v[220:221], off
	v_lshl_add_u64 v[220:221], v[226:227], 0, s[14:15]
	s_mov_b32 m0, s75
	s_nop 0
	global_load_lds_dwordx4 v[220:221], off
	s_waitcnt vmcnt(8)
	s_waitcnt lgkmcnt(0)
	s_barrier
	v_mfma_f32_16x16x32_bf16 v[54:57], v[144:147], v[188:191], v[54:57]
	v_mfma_f32_16x16x32_bf16 v[42:45], v[164:167], v[188:191], v[42:45]
	v_mfma_f32_16x16x32_bf16 v[30:33], v[144:147], v[196:199], v[30:33]
	v_mfma_f32_16x16x32_bf16 v[26:29], v[164:167], v[196:199], v[26:29]
	v_mfma_f32_16x16x32_bf16 v[14:17], v[144:147], v[204:207], v[14:17]
	v_mfma_f32_16x16x32_bf16 v[10:13], v[164:167], v[204:207], v[10:13]
	v_mfma_f32_16x16x32_bf16 v[6:9], v[144:147], v[212:215], v[6:9]
	v_mfma_f32_16x16x32_bf16 v[2:5], v[164:167], v[212:215], v[2:5]
	v_mfma_f32_16x16x32_bf16 v[54:57], v[160:163], v[192:195], v[54:57]
	v_mfma_f32_16x16x32_bf16 v[42:45], v[168:171], v[192:195], v[42:45]
	v_mfma_f32_16x16x32_bf16 v[30:33], v[160:163], v[200:203], v[30:33]
	v_mfma_f32_16x16x32_bf16 v[26:29], v[168:171], v[200:203], v[26:29]
	v_mfma_f32_16x16x32_bf16 v[14:17], v[160:163], v[208:211], v[14:17]
	v_mfma_f32_16x16x32_bf16 v[10:13], v[168:171], v[208:211], v[10:13]
	v_mfma_f32_16x16x32_bf16 v[6:9], v[160:163], v[216:219], v[6:9]
	v_mfma_f32_16x16x32_bf16 v[2:5], v[168:171], v[216:219], v[2:5]
	v_mfma_f32_16x16x32_bf16 v[70:73], v[172:175], v[188:191], v[70:73]
	v_mfma_f32_16x16x32_bf16 v[66:69], v[180:183], v[188:191], v[66:69]
	v_mfma_f32_16x16x32_bf16 v[50:53], v[172:175], v[196:199], v[50:53]
	v_mfma_f32_16x16x32_bf16 v[46:49], v[180:183], v[196:199], v[46:49]
	v_mfma_f32_16x16x32_bf16 v[38:41], v[172:175], v[204:207], v[38:41]
	v_mfma_f32_16x16x32_bf16 v[34:37], v[180:183], v[204:207], v[34:37]
	v_mfma_f32_16x16x32_bf16 v[22:25], v[172:175], v[212:215], v[22:25]
	v_mfma_f32_16x16x32_bf16 v[18:21], v[180:183], v[212:215], v[18:21]
	v_mfma_f32_16x16x32_bf16 v[70:73], v[176:179], v[192:195], v[70:73]
	v_mfma_f32_16x16x32_bf16 v[66:69], v[184:187], v[192:195], v[66:69]
	v_mfma_f32_16x16x32_bf16 v[50:53], v[176:179], v[200:203], v[50:53]
	v_mfma_f32_16x16x32_bf16 v[46:49], v[184:187], v[200:203], v[46:49]
	v_mfma_f32_16x16x32_bf16 v[38:41], v[176:179], v[208:211], v[38:41]
	v_mfma_f32_16x16x32_bf16 v[34:37], v[184:187], v[208:211], v[34:37]
	v_mfma_f32_16x16x32_bf16 v[22:25], v[176:179], v[216:219], v[22:25]
	v_mfma_f32_16x16x32_bf16 v[18:21], v[184:187], v[216:219], v[18:21]
	s_barrier
	s_add_i32 s92, s92, 2
	s_add_u32 s90, s90, 0x100
	s_addc_u32 s91, s91, 0
	s_add_u32 s56, s56, 0x100
	s_addc_u32 s57, s57, 0
	s_cmp_gt_u32 s92, 5
	s_cbranch_scc0 .LBB0_908
	s_and_b64 vcc, exec, s[16:17]
	s_cbranch_vccz .LBB0_911
	s_barrier

; #define PG8_STAGE(bufoff, gbase, voff) do { _Pragma("unroll") for (int _i = 0; _i < 2; ++_i) \
;         __builtin_amdgcn_global_load_lds((const unsigned*)((const char*)(gbase) + (voff)[_i]), (PG8_LAS unsigned*)(lds + (bufoff) + ldsw + _i * 8192), 16, 0, 0); } while (0)
; #define PG8_LDA(dst, b, h) do { _Pragma("unroll") for (int m = 0; m < 4; ++m) _Pragma("unroll") for (int k = 0; k < 2; ++k) dst[m][k] = *(const PG8_LAS bf16x8*)(lds + PG8_SA(b, h) + aoff + m * 2048 + k * 1024); } while (0)
; #define PG8_LDB(dst, b, h) do { _Pragma("unroll") for (int n = 0; n < 2; ++n) _Pragma("unroll") for (int k = 0; k < 2; ++k) dst[n][k] = *(const PG8_LAS bf16x8*)(lds + PG8_SB(b, h) + boff + n * 2048 + k * 1024); } while (0)
; #define PG8_MMA(ai, bj, At, Bt) do { __builtin_amdgcn_s_setprio(1); _Pragma("unroll") for (int m = 0; m < 4; ++m) _Pragma("unroll") for (int n = 0; n < 2; ++n) _Pragma("unroll") for (int k = 0; k < 2; ++k) \
;         acc[ai][bj][m][n] = __builtin_amdgcn_mfma_f32_16x16x32_bf16(Bt[n][k], At[m][k], acc[ai][bj][m][n], 0, 0, 0); __builtin_amdgcn_s_setprio(0); } while (0)
; #define PG8_WAIT_V(n) asm volatile("s_waitcnt vmcnt(" #n ")" ::: "memory")
; #define PG8_WAIT_L(n) asm volatile("s_waitcnt lgkmcnt(" #n ")" ::: "memory")
; #define PG8_BAR __builtin_amdgcn_s_barrier()
; #define PG8_SCHED __builtin_amdgcn_sched_barrier(0)
; template <class Epi, class Sched, bool ALIGN_EPI = false>
; __device__ __forceinline__ void gemm_phase(PG8_LAS unsigned char* lds, const Gemm g, const Sched& S, const Epi& E) {
;     ...
;             PG8_LDB(B0, 0, 0); PG8_LDB(B1, 0, 1); PG8_SCHED; PG8_LDA(At, 0, 0); PG8_STAGE(PG8_SA(1, 1), a1 + hstepA, vc1);
;             PG8_WAIT_V(8); PG8_WAIT_L(0); PG8_BAR; PG8_MMA(0, 0, At, B0); PG8_MMA(0, 1, At, B1); PG8_BAR; PG8_SCHED;
;             PG8_LDA(At, 0, 1); PG8_STAGE(PG8_SB(0, 0), b2, voffB); PG8_STAGE(PG8_SB(0, 1), b2 + hstep, voffB); PG8_STAGE(PG8_SA(0, 0), a2, w0);
;             PG8_WAIT_V(8); PG8_WAIT_L(0); PG8_BAR; PG8_MMA(1, 0, At, B0); PG8_MMA(1, 1, At, B1); PG8_BAR; PG8_SCHED;
.LBB0_1055:
	ds_read_b128 v[166:169], v155
	ds_read_b128 v[170:173], v155 offset:1024
	ds_read_b128 v[174:177], v155 offset:2048
	ds_read_b128 v[178:181], v155 offset:3072
	ds_read_b128 v[182:185], v157
	ds_read_b128 v[186:189], v157 offset:1024
	ds_read_b128 v[190:193], v157 offset:2048
	ds_read_b128 v[194:197], v157 offset:3072
	s_add_u32 s56, s54, 0xfff80080
	s_addc_u32 s57, s55, -1
	s_cmp_eq_u32 s83, 28
	s_cselect_b32 s59, s15, s57
	s_cselect_b32 s58, s79, s56
	s_cselect_b32 s57, s49, s82
	s_cselect_b32 s56, s80, s81
	v_lshl_add_u64 v[230:231], s[54:55], 0, v[140:141]
	s_add_i32 m0, s63, 0xc000
	ds_read_b128 v[198:201], v159
	ds_read_b128 v[202:205], v159 offset:1024
	ds_read_b128 v[206:209], v159 offset:2048
	ds_read_b128 v[210:213], v159 offset:3072
	ds_read_b128 v[214:217], v159 offset:4096
	ds_read_b128 v[218:221], v159 offset:5120
	ds_read_b128 v[222:225], v159 offset:6144
	ds_read_b128 v[226:229], v159 offset:7168
	global_load_lds_dwordx4 v[230:231], off
	v_lshl_add_u64 v[230:231], s[54:55], 0, v[142:143]
	s_add_i32 m0, s63, 0xe000
	s_nop 0
	global_load_lds_dwordx4 v[230:231], off
	s_waitcnt vmcnt(8)
	s_waitcnt lgkmcnt(0)
	s_barrier
	v_mfma_f32_16x16x32_bf16 v[126:129], v[166:169], v[198:201], v[126:129]
	v_mfma_f32_16x16x32_bf16 v[122:125], v[174:177], v[198:201], v[122:125]
	v_mfma_f32_16x16x32_bf16 v[114:117], v[166:169], v[206:209], v[114:117]
	v_mfma_f32_16x16x32_bf16 v[106:109], v[174:177], v[206:209], v[106:109]
	v_mfma_f32_16x16x32_bf16 v[98:101], v[166:169], v[214:217], v[98:101]
	v_mfma_f32_16x16x32_bf16 v[90:93], v[174:177], v[214:217], v[90:93]
	v_mfma_f32_16x16x32_bf16 v[82:85], v[166:169], v[222:225], v[82:85]
	v_mfma_f32_16x16x32_bf16 v[74:77], v[174:177], v[222:225], v[74:77]
	v_mfma_f32_16x16x32_bf16 v[126:129], v[170:173], v[202:205], v[126:129]
	v_mfma_f32_16x16x32_bf16 v[122:125], v[178:181], v[202:205], v[122:125]
	v_mfma_f32_16x16x32_bf16 v[114:117], v[170:173], v[210:213], v[114:117]
	v_mfma_f32_16x16x32_bf16 v[106:109], v[178:181], v[210:213], v[106:109]
	v_mfma_f32_16x16x32_bf16 v[98:101], v[170:173], v[218:221], v[98:101]
	v_mfma_f32_16x16x32_bf16 v[90:93], v[178:181], v[218:221], v[90:93]
	v_mfma_f32_16x16x32_bf16 v[82:85], v[170:173], v[226:229], v[82:85]
	v_mfma_f32_16x16x32_bf16 v[74:77], v[178:181], v[226:229], v[74:77]
	v_mfma_f32_16x16x32_bf16 v[118:121], v[182:185], v[198:201], v[118:121]
	v_mfma_f32_16x16x32_bf16 v[110:113], v[190:193], v[198:201], v[110:113]
	v_mfma_f32_16x16x32_bf16 v[102:105], v[182:185], v[206:209], v[102:105]
	v_mfma_f32_16x16x32_bf16 v[94:97], v[190:193], v[206:209], v[94:97]
	v_mfma_f32_16x16x32_bf16 v[86:89], v[182:185], v[214:217], v[86:89]
	v_mfma_f32_16x16x32_bf16 v[78:81], v[190:193], v[214:217], v[78:81]
	v_mfma_f32_16x16x32_bf16 v[62:65], v[182:185], v[222:225], v[62:65]
	v_mfma_f32_16x16x32_bf16 v[58:61], v[190:193], v[222:225], v[58:61]
	v_mfma_f32_16x16x32_bf16 v[118:121], v[186:189], v[202:205], v[118:121]
	v_mfma_f32_16x16x32_bf16 v[110:113], v[194:197], v[202:205], v[110:113]
	v_mfma_f32_16x16x32_bf16 v[102:105], v[186:189], v[210:213], v[102:105]
	v_mfma_f32_16x16x32_bf16 v[94:97], v[194:197], v[210:213], v[94:97]
	v_mfma_f32_16x16x32_bf16 v[86:89], v[186:189], v[218:221], v[86:89]
	v_mfma_f32_16x16x32_bf16 v[78:81], v[194:197], v[218:221], v[78:81]
	v_mfma_f32_16x16x32_bf16 v[62:65], v[186:189], v[226:229], v[62:65]
	v_mfma_f32_16x16x32_bf16 v[58:61], v[194:197], v[226:229], v[58:61]
	s_barrier
	s_add_i32 s84, s73, s61
	v_lshl_add_u64 v[230:231], s[56:57], 0, v[132:133]
	s_mov_b32 m0, s84
	ds_read_b128 v[198:201], v159 offset:16384
	ds_read_b128 v[202:205], v159 offset:17408
	ds_read_b128 v[206:209], v159 offset:18432
	ds_read_b128 v[210:213], v159 offset:19456
	ds_read_b128 v[214:217], v159 offset:20480
	ds_read_b128 v[218:221], v159 offset:21504
	ds_read_b128 v[222:225], v159 offset:22528
	ds_read_b128 v[226:229], v159 offset:23552
	global_load_lds_dwordx4 v[230:231], off
	s_add_i32 m0, s84, 0x2000
	s_add_u32 s84, s56, 0x80000
	v_lshl_add_u64 v[232:233], s[56:57], 0, v[136:137]
	s_addc_u32 s85, s57, 0
	s_add_i32 s86, s74, s61
	global_load_lds_dwordx4 v[232:233], off
	v_lshl_add_u64 v[234:235], s[84:85], 0, v[132:133]
	s_mov_b32 m0, s86
	v_lshl_add_u64 v[236:237], s[58:59], 0, v[134:135]
	global_load_lds_dwordx4 v[234:235], off
	v_lshl_add_u64 v[234:235], s[84:85], 0, v[136:137]
	s_add_i32 m0, s86, 0x2000
	s_nop 0
	global_load_lds_dwordx4 v[234:235], off
	v_lshl_add_u64 v[234:235], s[58:59], 0, v[130:131]
	s_mov_b32 m0, s63
	s_nop 0
	global_load_lds_dwordx4 v[234:235], off
	s_mov_b32 m0, s64
	s_nop 0
	global_load_lds_dwordx4 v[236:237], off
	s_waitcnt vmcnt(8)
	s_waitcnt lgkmcnt(0)
	s_barrier
; #define PG8_STAGE(bufoff, gbase, voff) do { _Pragma("unroll") for (int _i = 0; _i < 2; ++_i) \
;         __builtin_amdgcn_global_load_lds((const unsigned*)((const char*)(gbase) + (voff)[_i]), (PG8_LAS unsigned*)(lds + (bufoff) + ldsw + _i * 8192), 16, 0, 0); } while (0)
; #define PG8_LDA(dst, b, h) do { _Pragma("unroll") for (int m = 0; m < 4; ++m) _Pragma("unroll") for (int k = 0; k < 2; ++k) dst[m][k] = *(const PG8_LAS bf16x8*)(lds + PG8_SA(b, h) + aoff + m * 2048 + k * 1024); } while (0)
; #define PG8_LDB(dst, b, h) do { _Pragma("unroll") for (int n = 0; n < 2; ++n) _Pragma("unroll") for (int k = 0; k < 2; ++k) dst[n][k] = *(const PG8_LAS bf16x8*)(lds + PG8_SB(b, h) + boff + n * 2048 + k * 1024); } while (0)
; #define PG8_MMA(ai, bj, At, Bt) do { __builtin_amdgcn_s_setprio(1); _Pragma("unroll") for (int m = 0; m < 4; ++m) _Pragma("unroll") for (int n = 0; n < 2; ++n) _Pragma("unroll") for (int k = 0; k < 2; ++k) \
;         acc[ai][bj][m][n] = __builtin_amdgcn_mfma_f32_16x16x32_bf16(Bt[n][k], At[m][k], acc[ai][bj][m][n], 0, 0, 0); __builtin_amdgcn_s_setprio(0); } while (0)
; #define PG8_WAIT_V(n) asm volatile("s_waitcnt vmcnt(" #n ")" ::: "memory")
; #define PG8_WAIT_L(n) asm volatile("s_waitcnt lgkmcnt(" #n ")" ::: "memory")
; #define PG8_BAR __builtin_amdgcn_s_barrier()
; #define PG8_SCHED __builtin_amdgcn_sched_barrier(0)
; template <class Epi, class Sched, bool ALIGN_EPI = false>
; __device__ __forceinline__ void gemm_phase(PG8_LAS unsigned char* lds, const Gemm g, const Sched& S, const Epi& E) {
;     ...
;             PG8_WAIT_V(8); PG8_WAIT_L(0); PG8_BAR; PG8_MMA(1, 0, At, B0); PG8_MMA(1, 1, At, B1); PG8_BAR; PG8_SCHED;
;             PG8_LDB(B0, 1, 0); PG8_LDB(B1, 1, 1); PG8_SCHED; PG8_LDA(At, 1, 0); PG8_STAGE(PG8_SA(0, 1), a2 + hstepA, w1);
;             PG8_WAIT_V(8); PG8_WAIT_L(0); PG8_BAR; PG8_MMA(0, 0, At, B0); PG8_MMA(0, 1, At, B1); PG8_BAR; PG8_SCHED;
	v_mfma_f32_16x16x32_bf16 v[54:57], v[166:169], v[198:201], v[54:57]
	v_mfma_f32_16x16x32_bf16 v[42:45], v[174:177], v[198:201], v[42:45]
	v_mfma_f32_16x16x32_bf16 v[30:33], v[166:169], v[206:209], v[30:33]
	v_mfma_f32_16x16x32_bf16 v[26:29], v[174:177], v[206:209], v[26:29]
	v_mfma_f32_16x16x32_bf16 v[14:17], v[166:169], v[214:217], v[14:17]
	v_mfma_f32_16x16x32_bf16 v[10:13], v[174:177], v[214:217], v[10:13]
	v_mfma_f32_16x16x32_bf16 v[6:9], v[166:169], v[222:225], v[6:9]
	v_mfma_f32_16x16x32_bf16 v[2:5], v[174:177], v[222:225], v[2:5]
	v_mfma_f32_16x16x32_bf16 v[54:57], v[170:173], v[202:205], v[54:57]
	v_mfma_f32_16x16x32_bf16 v[42:45], v[178:181], v[202:205], v[42:45]
	v_mfma_f32_16x16x32_bf16 v[30:33], v[170:173], v[210:213], v[30:33]
	v_mfma_f32_16x16x32_bf16 v[26:29], v[178:181], v[210:213], v[26:29]
	v_mfma_f32_16x16x32_bf16 v[14:17], v[170:173], v[218:221], v[14:17]
	v_mfma_f32_16x16x32_bf16 v[10:13], v[178:181], v[218:221], v[10:13]
	v_mfma_f32_16x16x32_bf16 v[6:9], v[170:173], v[226:229], v[6:9]
	v_mfma_f32_16x16x32_bf16 v[2:5], v[178:181], v[226:229], v[2:5]
	v_mfma_f32_16x16x32_bf16 v[66:69], v[182:185], v[198:201], v[66:69]
	v_mfma_f32_16x16x32_bf16 v[70:73], v[190:193], v[198:201], v[70:73]
	v_mfma_f32_16x16x32_bf16 v[46:49], v[182:185], v[206:209], v[46:49]
	v_mfma_f32_16x16x32_bf16 v[50:53], v[190:193], v[206:209], v[50:53]
	v_mfma_f32_16x16x32_bf16 v[34:37], v[182:185], v[214:217], v[34:37]
	v_mfma_f32_16x16x32_bf16 v[38:41], v[190:193], v[214:217], v[38:41]
	v_mfma_f32_16x16x32_bf16 v[18:21], v[182:185], v[222:225], v[18:21]
	v_mfma_f32_16x16x32_bf16 v[22:25], v[190:193], v[222:225], v[22:25]
	v_mfma_f32_16x16x32_bf16 v[66:69], v[186:189], v[202:205], v[66:69]
	v_mfma_f32_16x16x32_bf16 v[70:73], v[194:197], v[202:205], v[70:73]
	v_mfma_f32_16x16x32_bf16 v[46:49], v[186:189], v[210:213], v[46:49]
	v_mfma_f32_16x16x32_bf16 v[50:53], v[194:197], v[210:213], v[50:53]
	v_mfma_f32_16x16x32_bf16 v[34:37], v[186:189], v[218:221], v[34:37]
	v_mfma_f32_16x16x32_bf16 v[38:41], v[194:197], v[218:221], v[38:41]
	v_mfma_f32_16x16x32_bf16 v[18:21], v[186:189], v[226:229], v[18:21]
	v_mfma_f32_16x16x32_bf16 v[22:25], v[194:197], v[226:229], v[22:25]
	s_barrier
	s_add_i32 s84, 0, 0x18000
	v_add_u32_e32 v138, s84, v149
	s_add_i32 s85, 0, 0x1c000
	ds_read_b128 v[166:169], v138
	ds_read_b128 v[170:173], v138 offset:1024
	ds_read_b128 v[174:177], v138 offset:2048
	ds_read_b128 v[178:181], v138 offset:3072
	v_add_u32_e32 v138, s85, v149
	ds_read_b128 v[182:185], v138
	ds_read_b128 v[186:189], v138 offset:1024
	ds_read_b128 v[190:193], v138 offset:2048
	ds_read_b128 v[194:197], v138 offset:3072
	s_add_u32 s58, s58, 0x80000
	s_addc_u32 s59, s59, 0
	s_mov_b32 m0, s65
	v_lshl_add_u64 v[238:239], s[58:59], 0, v[130:131]
	ds_read_b128 v[198:201], v159 offset:32768
	ds_read_b128 v[202:205], v159 offset:33792
	ds_read_b128 v[206:209], v159 offset:34816
	ds_read_b128 v[210:213], v159 offset:35840
	ds_read_b128 v[214:217], v159 offset:36864
	ds_read_b128 v[218:221], v159 offset:37888
	ds_read_b128 v[222:225], v159 offset:38912
	ds_read_b128 v[226:229], v159 offset:39936
	global_load_lds_dwordx4 v[238:239], off
	v_lshl_add_u64 v[238:239], s[58:59], 0, v[134:135]
	s_mov_b32 m0, s66
	s_nop 0
	global_load_lds_dwordx4 v[238:239], off
	s_waitcnt vmcnt(8)
	s_waitcnt lgkmcnt(0)
	s_barrier
	v_mfma_f32_16x16x32_bf16 v[126:129], v[166:169], v[198:201], v[126:129]
	v_mfma_f32_16x16x32_bf16 v[122:125], v[174:177], v[198:201], v[122:125]
	v_mfma_f32_16x16x32_bf16 v[114:117], v[166:169], v[206:209], v[114:117]
	v_mfma_f32_16x16x32_bf16 v[106:109], v[174:177], v[206:209], v[106:109]
	v_mfma_f32_16x16x32_bf16 v[98:101], v[166:169], v[214:217], v[98:101]
	v_mfma_f32_16x16x32_bf16 v[90:93], v[174:177], v[214:217], v[90:93]
	v_mfma_f32_16x16x32_bf16 v[82:85], v[166:169], v[222:225], v[82:85]
	v_mfma_f32_16x16x32_bf16 v[74:77], v[174:177], v[222:225], v[74:77]
	v_mfma_f32_16x16x32_bf16 v[126:129], v[170:173], v[202:205], v[126:129]
	v_mfma_f32_16x16x32_bf16 v[122:125], v[178:181], v[202:205], v[122:125]
	v_mfma_f32_16x16x32_bf16 v[114:117], v[170:173], v[210:213], v[114:117]
	v_mfma_f32_16x16x32_bf16 v[106:109], v[178:181], v[210:213], v[106:109]
	v_mfma_f32_16x16x32_bf16 v[98:101], v[170:173], v[218:221], v[98:101]
	v_mfma_f32_16x16x32_bf16 v[90:93], v[178:181], v[218:221], v[90:93]
	v_mfma_f32_16x16x32_bf16 v[82:85], v[170:173], v[226:229], v[82:85]
	v_mfma_f32_16x16x32_bf16 v[74:77], v[178:181], v[226:229], v[74:77]
	v_mfma_f32_16x16x32_bf16 v[118:121], v[182:185], v[198:201], v[118:121]
	v_mfma_f32_16x16x32_bf16 v[110:113], v[190:193], v[198:201], v[110:113]
	v_mfma_f32_16x16x32_bf16 v[102:105], v[182:185], v[206:209], v[102:105]
	v_mfma_f32_16x16x32_bf16 v[94:97], v[190:193], v[206:209], v[94:97]
	v_mfma_f32_16x16x32_bf16 v[86:89], v[182:185], v[214:217], v[86:89]
	v_mfma_f32_16x16x32_bf16 v[78:81], v[190:193], v[214:217], v[78:81]
	v_mfma_f32_16x16x32_bf16 v[62:65], v[182:185], v[222:225], v[62:65]
	v_mfma_f32_16x16x32_bf16 v[58:61], v[190:193], v[222:225], v[58:61]
	v_mfma_f32_16x16x32_bf16 v[118:121], v[186:189], v[202:205], v[118:121]
	v_mfma_f32_16x16x32_bf16 v[110:113], v[194:197], v[202:205], v[110:113]
	v_mfma_f32_16x16x32_bf16 v[102:105], v[186:189], v[210:213], v[102:105]
	v_mfma_f32_16x16x32_bf16 v[94:97], v[194:197], v[210:213], v[94:97]
	v_mfma_f32_16x16x32_bf16 v[86:89], v[186:189], v[218:221], v[86:89]
	v_mfma_f32_16x16x32_bf16 v[78:81], v[194:197], v[218:221], v[78:81]
	v_mfma_f32_16x16x32_bf16 v[62:65], v[186:189], v[226:229], v[62:65]
	v_mfma_f32_16x16x32_bf16 v[58:61], v[194:197], v[226:229], v[58:61]
	s_barrier
; #define PG8_STAGE(bufoff, gbase, voff) do { _Pragma("unroll") for (int _i = 0; _i < 2; ++_i) \
;         __builtin_amdgcn_global_load_lds((const unsigned*)((const char*)(gbase) + (voff)[_i]), (PG8_LAS unsigned*)(lds + (bufoff) + ldsw + _i * 8192), 16, 0, 0); } while (0)
; #define PG8_LDA(dst, b, h) do { _Pragma("unroll") for (int m = 0; m < 4; ++m) _Pragma("unroll") for (int k = 0; k < 2; ++k) dst[m][k] = *(const PG8_LAS bf16x8*)(lds + PG8_SA(b, h) + aoff + m * 2048 + k * 1024); } while (0)
; #define PG8_MMA(ai, bj, At, Bt) do { __builtin_amdgcn_s_setprio(1); _Pragma("unroll") for (int m = 0; m < 4; ++m) _Pragma("unroll") for (int n = 0; n < 2; ++n) _Pragma("unroll") for (int k = 0; k < 2; ++k) \
;         acc[ai][bj][m][n] = __builtin_amdgcn_mfma_f32_16x16x32_bf16(Bt[n][k], At[m][k], acc[ai][bj][m][n], 0, 0, 0); __builtin_amdgcn_s_setprio(0); } while (0)
; #define PG8_WAIT_V(n) asm volatile("s_waitcnt vmcnt(" #n ")" ::: "memory")
; #define PG8_WAIT_L(n) asm volatile("s_waitcnt lgkmcnt(" #n ")" ::: "memory")
; #define PG8_BAR __builtin_amdgcn_s_barrier()
; #define PG8_SCHED __builtin_amdgcn_sched_barrier(0)
; template <class Epi, class Sched, bool ALIGN_EPI = false>
; __device__ __forceinline__ void gemm_phase(PG8_LAS unsigned char* lds, const Gemm g, const Sched& S, const Epi& E) {
;     ...
;             PG8_LDA(At, 1, 1); PG8_STAGE(PG8_SB(1, 0), b3, voffB); PG8_STAGE(PG8_SB(1, 1), b3 + hstep, voffB); PG8_STAGE(PG8_SA(1, 0), a3, w0);
;             PG8_WAIT_V(8); PG8_WAIT_L(0); PG8_BAR; PG8_MMA(1, 0, At, B0); PG8_MMA(1, 1, At, B1); PG8_BAR; PG8_SCHED;
;             if constexpr (Epi::KSCALE) { if (((t + 2) & 7) == 0 && t + 2 < nt) { E.kscale(acc, pf, ((t + 2) >> 3) - 1, wr, fr); PG8_SCHED; } }
;         }
;         if constexpr (ALIGN_EPI) { if (wr == 0) PG8_BAR; }
	s_add_i32 s58, s84, s61
	v_lshl_add_u64 v[230:231], v[230:231], 0, s[26:27]
	s_mov_b32 m0, s58
	ds_read_b128 v[198:201], v159 offset:49152
	ds_read_b128 v[202:205], v159 offset:50176
	ds_read_b128 v[206:209], v159 offset:51200
	ds_read_b128 v[210:213], v159 offset:52224
	ds_read_b128 v[214:217], v159 offset:53248
	ds_read_b128 v[218:221], v159 offset:54272
	ds_read_b128 v[222:225], v159 offset:55296
	ds_read_b128 v[226:229], v159 offset:56320
	global_load_lds_dwordx4 v[230:231], off
	s_add_i32 m0, s58, 0x2000
	s_add_u32 s56, s56, 0x80080
	v_lshl_add_u64 v[230:231], v[232:233], 0, s[26:27]
	s_addc_u32 s57, s57, 0
	s_add_i32 s58, s85, s61
	global_load_lds_dwordx4 v[230:231], off
	v_lshl_add_u64 v[230:231], s[56:57], 0, v[132:133]
	s_mov_b32 m0, s58
	s_nop 0
	global_load_lds_dwordx4 v[230:231], off
	v_lshl_add_u64 v[230:231], s[56:57], 0, v[136:137]
	s_add_i32 m0, s58, 0x2000
	s_nop 0
	global_load_lds_dwordx4 v[230:231], off
	v_lshl_add_u64 v[230:231], v[234:235], 0, s[26:27]
	s_mov_b32 m0, s69
	s_nop 0
	global_load_lds_dwordx4 v[230:231], off
	v_lshl_add_u64 v[230:231], v[236:237], 0, s[26:27]
	s_mov_b32 m0, s72
	s_nop 0
	global_load_lds_dwordx4 v[230:231], off
	s_waitcnt vmcnt(8)
	s_waitcnt lgkmcnt(0)
	s_barrier
	v_mfma_f32_16x16x32_bf16 v[54:57], v[166:169], v[198:201], v[54:57]
	v_mfma_f32_16x16x32_bf16 v[42:45], v[174:177], v[198:201], v[42:45]
	v_mfma_f32_16x16x32_bf16 v[30:33], v[166:169], v[206:209], v[30:33]
	v_mfma_f32_16x16x32_bf16 v[26:29], v[174:177], v[206:209], v[26:29]
	v_mfma_f32_16x16x32_bf16 v[14:17], v[166:169], v[214:217], v[14:17]
	v_mfma_f32_16x16x32_bf16 v[10:13], v[174:177], v[214:217], v[10:13]
	v_mfma_f32_16x16x32_bf16 v[6:9], v[166:169], v[222:225], v[6:9]
	v_mfma_f32_16x16x32_bf16 v[2:5], v[174:177], v[222:225], v[2:5]
	v_mfma_f32_16x16x32_bf16 v[54:57], v[170:173], v[202:205], v[54:57]
	v_mfma_f32_16x16x32_bf16 v[42:45], v[178:181], v[202:205], v[42:45]
	v_mfma_f32_16x16x32_bf16 v[30:33], v[170:173], v[210:213], v[30:33]
	v_mfma_f32_16x16x32_bf16 v[26:29], v[178:181], v[210:213], v[26:29]
	v_mfma_f32_16x16x32_bf16 v[14:17], v[170:173], v[218:221], v[14:17]
	v_mfma_f32_16x16x32_bf16 v[10:13], v[178:181], v[218:221], v[10:13]
	v_mfma_f32_16x16x32_bf16 v[6:9], v[170:173], v[226:229], v[6:9]
	v_mfma_f32_16x16x32_bf16 v[2:5], v[178:181], v[226:229], v[2:5]
	v_mfma_f32_16x16x32_bf16 v[66:69], v[182:185], v[198:201], v[66:69]
	v_mfma_f32_16x16x32_bf16 v[70:73], v[190:193], v[198:201], v[70:73]
	v_mfma_f32_16x16x32_bf16 v[46:49], v[182:185], v[206:209], v[46:49]
	v_mfma_f32_16x16x32_bf16 v[50:53], v[190:193], v[206:209], v[50:53]
	v_mfma_f32_16x16x32_bf16 v[34:37], v[182:185], v[214:217], v[34:37]
	v_mfma_f32_16x16x32_bf16 v[38:41], v[190:193], v[214:217], v[38:41]
	v_mfma_f32_16x16x32_bf16 v[18:21], v[182:185], v[222:225], v[18:21]
	v_mfma_f32_16x16x32_bf16 v[22:25], v[190:193], v[222:225], v[22:25]
	v_mfma_f32_16x16x32_bf16 v[66:69], v[186:189], v[202:205], v[66:69]
	v_mfma_f32_16x16x32_bf16 v[70:73], v[194:197], v[202:205], v[70:73]
	v_mfma_f32_16x16x32_bf16 v[46:49], v[186:189], v[210:213], v[46:49]
	v_mfma_f32_16x16x32_bf16 v[50:53], v[194:197], v[210:213], v[50:53]
	v_mfma_f32_16x16x32_bf16 v[34:37], v[186:189], v[218:221], v[34:37]
	v_mfma_f32_16x16x32_bf16 v[38:41], v[194:197], v[218:221], v[38:41]
	v_mfma_f32_16x16x32_bf16 v[18:21], v[186:189], v[226:229], v[18:21]
	v_mfma_f32_16x16x32_bf16 v[22:25], v[194:197], v[226:229], v[22:25]
	s_barrier
	s_add_i32 s83, s83, 2
	s_add_u32 s54, s54, 0x100
	s_addc_u32 s55, s55, 0
	s_add_u32 s81, s81, 0x100
	s_addc_u32 s82, s82, 0
	s_cmp_gt_u32 s83, 29
	s_cbranch_scc0 .LBB0_1055
	s_and_b64 vcc, exec, s[40:41]
	s_cbranch_vccz .LBB0_1058
	s_barrier

; #define PG8_STAGE(bufoff, gbase, voff) do { _Pragma("unroll") for (int _i = 0; _i < 2; ++_i) \
;         __builtin_amdgcn_global_load_lds((const unsigned*)((const char*)(gbase) + (voff)[_i]), (PG8_LAS unsigned*)(lds + (bufoff) + ldsw + _i * 8192), 16, 0, 0); } while (0)
; #define PG8_LDA(dst, b, h) do { _Pragma("unroll") for (int m = 0; m < 4; ++m) _Pragma("unroll") for (int k = 0; k < 2; ++k) dst[m][k] = *(const PG8_LAS bf16x8*)(lds + PG8_SA(b, h) + aoff + m * 2048 + k * 1024); } while (0)
; #define PG8_LDB(dst, b, h) do { _Pragma("unroll") for (int n = 0; n < 2; ++n) _Pragma("unroll") for (int k = 0; k < 2; ++k) dst[n][k] = *(const PG8_LAS bf16x8*)(lds + PG8_SB(b, h) + boff + n * 2048 + k * 1024); } while (0)
; #define PG8_MMA(ai, bj, At, Bt) do { __builtin_amdgcn_s_setprio(1); _Pragma("unroll") for (int m = 0; m < 4; ++m) _Pragma("unroll") for (int n = 0; n < 2; ++n) _Pragma("unroll") for (int k = 0; k < 2; ++k) \
;         acc[ai][bj][m][n] = __builtin_amdgcn_mfma_f32_16x16x32_bf16(Bt[n][k], At[m][k], acc[ai][bj][m][n], 0, 0, 0); __builtin_amdgcn_s_setprio(0); } while (0)
; #define PG8_WAIT_V(n) asm volatile("s_waitcnt vmcnt(" #n ")" ::: "memory")
; #define PG8_WAIT_L(n) asm volatile("s_waitcnt lgkmcnt(" #n ")" ::: "memory")
; #define PG8_BAR __builtin_amdgcn_s_barrier()
; #define PG8_SCHED __builtin_amdgcn_sched_barrier(0)
; template <class Epi, class Sched, bool ALIGN_EPI = false>
; __device__ __forceinline__ void gemm_phase(PG8_LAS unsigned char* lds, const Gemm g, const Sched& S, const Epi& E) {
;     ...
;             PG8_LDB(B0, 0, 0); PG8_LDB(B1, 0, 1); PG8_SCHED; PG8_LDA(At, 0, 0); PG8_STAGE(PG8_SA(1, 1), a1 + hstepA, vc1);
;             PG8_WAIT_V(8); PG8_WAIT_L(0); PG8_BAR; PG8_MMA(0, 0, At, B0); PG8_MMA(0, 1, At, B1); PG8_BAR; PG8_SCHED;
;             PG8_LDA(At, 0, 1); PG8_STAGE(PG8_SB(0, 0), b2, voffB); PG8_STAGE(PG8_SB(0, 1), b2 + hstep, voffB); PG8_STAGE(PG8_SA(0, 0), a2, w0);
;             PG8_WAIT_V(8); PG8_WAIT_L(0); PG8_BAR; PG8_MMA(1, 0, At, B0); PG8_MMA(1, 1, At, B1); PG8_BAR; PG8_SCHED;
.LBB0_1198:
	ds_read_b128 v[130:133], v168
	ds_read_b128 v[134:137], v168 offset:1024
	ds_read_b128 v[154:157], v168 offset:2048
	ds_read_b128 v[158:161], v168 offset:3072
	ds_read_b128 v[162:165], v169
	ds_read_b128 v[172:175], v169 offset:1024
	ds_read_b128 v[176:179], v169 offset:2048
	ds_read_b128 v[180:183], v169 offset:3072
	s_add_u32 s54, s52, 0xfff80080
	s_addc_u32 s55, s53, -1
	s_cmp_eq_u32 s78, 28
	s_cselect_b32 s57, s45, s55
	s_cselect_b32 s56, s74, s54
	s_cselect_b32 s55, s43, s77
	s_cselect_b32 s54, s75, s76
	v_lshl_add_u64 v[216:217], s[52:53], 0, v[146:147]
	s_add_i32 m0, s51, 0xc000
	ds_read_b128 v[184:187], v170
	ds_read_b128 v[188:191], v170 offset:1024
	ds_read_b128 v[192:195], v170 offset:2048
	ds_read_b128 v[196:199], v170 offset:3072
	ds_read_b128 v[200:203], v170 offset:4096
	ds_read_b128 v[204:207], v170 offset:5120
	ds_read_b128 v[208:211], v170 offset:6144
	ds_read_b128 v[212:215], v170 offset:7168
	global_load_lds_dwordx4 v[216:217], off
	v_lshl_add_u64 v[216:217], s[52:53], 0, v[148:149]
	s_add_i32 m0, s51, 0xe000
	s_nop 0
	global_load_lds_dwordx4 v[216:217], off
	s_waitcnt vmcnt(8)
	s_waitcnt lgkmcnt(0)
	s_barrier
	v_mfma_f32_16x16x32_bf16 v[126:129], v[130:133], v[184:187], v[126:129]
	v_mfma_f32_16x16x32_bf16 v[122:125], v[154:157], v[184:187], v[122:125]
	v_mfma_f32_16x16x32_bf16 v[118:121], v[130:133], v[192:195], v[118:121]
	v_mfma_f32_16x16x32_bf16 v[114:117], v[154:157], v[192:195], v[114:117]
	v_mfma_f32_16x16x32_bf16 v[94:97], v[130:133], v[200:203], v[94:97]
	v_mfma_f32_16x16x32_bf16 v[90:93], v[154:157], v[200:203], v[90:93]
	v_mfma_f32_16x16x32_bf16 v[78:81], v[130:133], v[208:211], v[78:81]
	v_mfma_f32_16x16x32_bf16 v[74:77], v[154:157], v[208:211], v[74:77]
	v_mfma_f32_16x16x32_bf16 v[126:129], v[134:137], v[188:191], v[126:129]
	v_mfma_f32_16x16x32_bf16 v[122:125], v[158:161], v[188:191], v[122:125]
	v_mfma_f32_16x16x32_bf16 v[118:121], v[134:137], v[196:199], v[118:121]
	v_mfma_f32_16x16x32_bf16 v[114:117], v[158:161], v[196:199], v[114:117]
	v_mfma_f32_16x16x32_bf16 v[94:97], v[134:137], v[204:207], v[94:97]
	v_mfma_f32_16x16x32_bf16 v[90:93], v[158:161], v[204:207], v[90:93]
	v_mfma_f32_16x16x32_bf16 v[78:81], v[134:137], v[212:215], v[78:81]
	v_mfma_f32_16x16x32_bf16 v[74:77], v[158:161], v[212:215], v[74:77]
	v_mfma_f32_16x16x32_bf16 v[110:113], v[162:165], v[184:187], v[110:113]
	v_mfma_f32_16x16x32_bf16 v[106:109], v[176:179], v[184:187], v[106:109]
	v_mfma_f32_16x16x32_bf16 v[102:105], v[162:165], v[192:195], v[102:105]
	v_mfma_f32_16x16x32_bf16 v[98:101], v[176:179], v[192:195], v[98:101]
	v_mfma_f32_16x16x32_bf16 v[86:89], v[162:165], v[200:203], v[86:89]
	v_mfma_f32_16x16x32_bf16 v[82:85], v[176:179], v[200:203], v[82:85]
	v_mfma_f32_16x16x32_bf16 v[70:73], v[162:165], v[208:211], v[70:73]
	v_mfma_f32_16x16x32_bf16 v[66:69], v[176:179], v[208:211], v[66:69]
	v_mfma_f32_16x16x32_bf16 v[110:113], v[172:175], v[188:191], v[110:113]
	v_mfma_f32_16x16x32_bf16 v[106:109], v[180:183], v[188:191], v[106:109]
	v_mfma_f32_16x16x32_bf16 v[102:105], v[172:175], v[196:199], v[102:105]
	v_mfma_f32_16x16x32_bf16 v[98:101], v[180:183], v[196:199], v[98:101]
	v_mfma_f32_16x16x32_bf16 v[86:89], v[172:175], v[204:207], v[86:89]
	v_mfma_f32_16x16x32_bf16 v[82:85], v[180:183], v[204:207], v[82:85]
	v_mfma_f32_16x16x32_bf16 v[70:73], v[172:175], v[212:215], v[70:73]
	v_mfma_f32_16x16x32_bf16 v[66:69], v[180:183], v[212:215], v[66:69]
	s_barrier
	s_add_i32 s79, s69, s61
	v_lshl_add_u64 v[216:217], s[54:55], 0, v[140:141]
	s_mov_b32 m0, s79
	ds_read_b128 v[184:187], v170 offset:16384
	ds_read_b128 v[188:191], v170 offset:17408
	ds_read_b128 v[192:195], v170 offset:18432
	ds_read_b128 v[196:199], v170 offset:19456
	ds_read_b128 v[200:203], v170 offset:20480
	ds_read_b128 v[204:207], v170 offset:21504
	ds_read_b128 v[208:211], v170 offset:22528
	ds_read_b128 v[212:215], v170 offset:23552
	global_load_lds_dwordx4 v[216:217], off
	s_add_i32 m0, s79, 0x2000
	s_add_u32 s80, s54, 0x80000
	v_lshl_add_u64 v[218:219], s[54:55], 0, v[144:145]
	s_addc_u32 s81, s55, 0
	s_add_i32 s79, s72, s61
	global_load_lds_dwordx4 v[218:219], off
	v_lshl_add_u64 v[220:221], s[80:81], 0, v[140:141]
	s_mov_b32 m0, s79
	v_lshl_add_u64 v[222:223], s[56:57], 0, v[142:143]
	global_load_lds_dwordx4 v[220:221], off
	v_lshl_add_u64 v[220:221], s[80:81], 0, v[144:145]
	s_add_i32 m0, s79, 0x2000
	s_nop 0
	global_load_lds_dwordx4 v[220:221], off
	v_lshl_add_u64 v[220:221], s[56:57], 0, v[138:139]
	s_mov_b32 m0, s51
	s_nop 0
	global_load_lds_dwordx4 v[220:221], off
	s_mov_b32 m0, s62
	s_nop 0
	global_load_lds_dwordx4 v[222:223], off
	s_waitcnt vmcnt(8)
	s_waitcnt lgkmcnt(0)
	s_barrier
; #define PG8_STAGE(bufoff, gbase, voff) do { _Pragma("unroll") for (int _i = 0; _i < 2; ++_i) \
;         __builtin_amdgcn_global_load_lds((const unsigned*)((const char*)(gbase) + (voff)[_i]), (PG8_LAS unsigned*)(lds + (bufoff) + ldsw + _i * 8192), 16, 0, 0); } while (0)
; #define PG8_LDA(dst, b, h) do { _Pragma("unroll") for (int m = 0; m < 4; ++m) _Pragma("unroll") for (int k = 0; k < 2; ++k) dst[m][k] = *(const PG8_LAS bf16x8*)(lds + PG8_SA(b, h) + aoff + m * 2048 + k * 1024); } while (0)
; #define PG8_LDB(dst, b, h) do { _Pragma("unroll") for (int n = 0; n < 2; ++n) _Pragma("unroll") for (int k = 0; k < 2; ++k) dst[n][k] = *(const PG8_LAS bf16x8*)(lds + PG8_SB(b, h) + boff + n * 2048 + k * 1024); } while (0)
; #define PG8_MMA(ai, bj, At, Bt) do { __builtin_amdgcn_s_setprio(1); _Pragma("unroll") for (int m = 0; m < 4; ++m) _Pragma("unroll") for (int n = 0; n < 2; ++n) _Pragma("unroll") for (int k = 0; k < 2; ++k) \
;         acc[ai][bj][m][n] = __builtin_amdgcn_mfma_f32_16x16x32_bf16(Bt[n][k], At[m][k], acc[ai][bj][m][n], 0, 0, 0); __builtin_amdgcn_s_setprio(0); } while (0)
; #define PG8_WAIT_V(n) asm volatile("s_waitcnt vmcnt(" #n ")" ::: "memory")
; #define PG8_WAIT_L(n) asm volatile("s_waitcnt lgkmcnt(" #n ")" ::: "memory")
; #define PG8_BAR __builtin_amdgcn_s_barrier()
; #define PG8_SCHED __builtin_amdgcn_sched_barrier(0)
; template <class Epi, class Sched, bool ALIGN_EPI = false>
; __device__ __forceinline__ void gemm_phase(PG8_LAS unsigned char* lds, const Gemm g, const Sched& S, const Epi& E) {
;     ...
;             PG8_WAIT_V(8); PG8_WAIT_L(0); PG8_BAR; PG8_MMA(1, 0, At, B0); PG8_MMA(1, 1, At, B1); PG8_BAR; PG8_SCHED;
;             PG8_LDB(B0, 1, 0); PG8_LDB(B1, 1, 1); PG8_SCHED; PG8_LDA(At, 1, 0); PG8_STAGE(PG8_SA(0, 1), a2 + hstepA, w1);
;             PG8_WAIT_V(8); PG8_WAIT_L(0); PG8_BAR; PG8_MMA(0, 0, At, B0); PG8_MMA(0, 1, At, B1); PG8_BAR; PG8_SCHED;
	v_mfma_f32_16x16x32_bf16 v[54:57], v[130:133], v[184:187], v[54:57]
	v_mfma_f32_16x16x32_bf16 v[50:53], v[154:157], v[184:187], v[50:53]
	v_mfma_f32_16x16x32_bf16 v[38:41], v[130:133], v[192:195], v[38:41]
	v_mfma_f32_16x16x32_bf16 v[34:37], v[154:157], v[192:195], v[34:37]
	v_mfma_f32_16x16x32_bf16 v[22:25], v[130:133], v[200:203], v[22:25]
	v_mfma_f32_16x16x32_bf16 v[18:21], v[154:157], v[200:203], v[18:21]
	v_mfma_f32_16x16x32_bf16 v[6:9], v[130:133], v[208:211], v[6:9]
	v_mfma_f32_16x16x32_bf16 v[2:5], v[154:157], v[208:211], v[2:5]
	v_mfma_f32_16x16x32_bf16 v[54:57], v[134:137], v[188:191], v[54:57]
	v_mfma_f32_16x16x32_bf16 v[50:53], v[158:161], v[188:191], v[50:53]
	v_mfma_f32_16x16x32_bf16 v[38:41], v[134:137], v[196:199], v[38:41]
	v_mfma_f32_16x16x32_bf16 v[34:37], v[158:161], v[196:199], v[34:37]
	v_mfma_f32_16x16x32_bf16 v[22:25], v[134:137], v[204:207], v[22:25]
	v_mfma_f32_16x16x32_bf16 v[18:21], v[158:161], v[204:207], v[18:21]
	v_mfma_f32_16x16x32_bf16 v[6:9], v[134:137], v[212:215], v[6:9]
	v_mfma_f32_16x16x32_bf16 v[2:5], v[158:161], v[212:215], v[2:5]
	v_mfma_f32_16x16x32_bf16 v[62:65], v[162:165], v[184:187], v[62:65]
	v_mfma_f32_16x16x32_bf16 v[58:61], v[176:179], v[184:187], v[58:61]
	v_mfma_f32_16x16x32_bf16 v[46:49], v[162:165], v[192:195], v[46:49]
	v_mfma_f32_16x16x32_bf16 v[42:45], v[176:179], v[192:195], v[42:45]
	v_mfma_f32_16x16x32_bf16 v[30:33], v[162:165], v[200:203], v[30:33]
	v_mfma_f32_16x16x32_bf16 v[26:29], v[176:179], v[200:203], v[26:29]
	v_mfma_f32_16x16x32_bf16 v[14:17], v[162:165], v[208:211], v[14:17]
	v_mfma_f32_16x16x32_bf16 v[10:13], v[176:179], v[208:211], v[10:13]
	v_mfma_f32_16x16x32_bf16 v[62:65], v[172:175], v[188:191], v[62:65]
	v_mfma_f32_16x16x32_bf16 v[58:61], v[180:183], v[188:191], v[58:61]
	v_mfma_f32_16x16x32_bf16 v[46:49], v[172:175], v[196:199], v[46:49]
	v_mfma_f32_16x16x32_bf16 v[42:45], v[180:183], v[196:199], v[42:45]
	v_mfma_f32_16x16x32_bf16 v[30:33], v[172:175], v[204:207], v[30:33]
	v_mfma_f32_16x16x32_bf16 v[26:29], v[180:183], v[204:207], v[26:29]
	v_mfma_f32_16x16x32_bf16 v[14:17], v[172:175], v[212:215], v[14:17]
	v_mfma_f32_16x16x32_bf16 v[10:13], v[180:183], v[212:215], v[10:13]
	s_barrier
	s_add_i32 s79, 0, 0x18000
	s_add_i32 s80, 0, 0x1c000
	v_add_u32_e32 v158, s79, v166
	v_add_u32_e32 v171, s80, v166
	ds_read_b128 v[130:133], v158
	ds_read_b128 v[134:137], v158 offset:1024
	ds_read_b128 v[154:157], v158 offset:2048
	ds_read_b128 v[158:161], v158 offset:3072
	ds_read_b128 v[162:165], v171
	ds_read_b128 v[172:175], v171 offset:1024
	ds_read_b128 v[176:179], v171 offset:2048
	ds_read_b128 v[180:183], v171 offset:3072
	s_add_u32 s56, s56, 0x80000
	s_addc_u32 s57, s57, 0
	s_mov_b32 m0, s63
	v_lshl_add_u64 v[224:225], s[56:57], 0, v[138:139]
	ds_read_b128 v[184:187], v170 offset:32768
	ds_read_b128 v[188:191], v170 offset:33792
	ds_read_b128 v[192:195], v170 offset:34816
	ds_read_b128 v[196:199], v170 offset:35840
	ds_read_b128 v[200:203], v170 offset:36864
	ds_read_b128 v[204:207], v170 offset:37888
	ds_read_b128 v[208:211], v170 offset:38912
	ds_read_b128 v[212:215], v170 offset:39936
	global_load_lds_dwordx4 v[224:225], off
	v_lshl_add_u64 v[224:225], s[56:57], 0, v[142:143]
	s_mov_b32 m0, s64
	s_nop 0
	global_load_lds_dwordx4 v[224:225], off
	s_waitcnt vmcnt(8)
	s_waitcnt lgkmcnt(0)
	s_barrier
	v_mfma_f32_16x16x32_bf16 v[126:129], v[130:133], v[184:187], v[126:129]
	v_mfma_f32_16x16x32_bf16 v[122:125], v[154:157], v[184:187], v[122:125]
	v_mfma_f32_16x16x32_bf16 v[118:121], v[130:133], v[192:195], v[118:121]
	v_mfma_f32_16x16x32_bf16 v[114:117], v[154:157], v[192:195], v[114:117]
	v_mfma_f32_16x16x32_bf16 v[94:97], v[130:133], v[200:203], v[94:97]
	v_mfma_f32_16x16x32_bf16 v[90:93], v[154:157], v[200:203], v[90:93]
	v_mfma_f32_16x16x32_bf16 v[78:81], v[130:133], v[208:211], v[78:81]
	v_mfma_f32_16x16x32_bf16 v[74:77], v[154:157], v[208:211], v[74:77]
	v_mfma_f32_16x16x32_bf16 v[126:129], v[134:137], v[188:191], v[126:129]
	v_mfma_f32_16x16x32_bf16 v[122:125], v[158:161], v[188:191], v[122:125]
	v_mfma_f32_16x16x32_bf16 v[118:121], v[134:137], v[196:199], v[118:121]
	v_mfma_f32_16x16x32_bf16 v[114:117], v[158:161], v[196:199], v[114:117]
	v_mfma_f32_16x16x32_bf16 v[94:97], v[134:137], v[204:207], v[94:97]
	v_mfma_f32_16x16x32_bf16 v[90:93], v[158:161], v[204:207], v[90:93]
	v_mfma_f32_16x16x32_bf16 v[78:81], v[134:137], v[212:215], v[78:81]
	v_mfma_f32_16x16x32_bf16 v[74:77], v[158:161], v[212:215], v[74:77]
	v_mfma_f32_16x16x32_bf16 v[110:113], v[162:165], v[184:187], v[110:113]
	v_mfma_f32_16x16x32_bf16 v[106:109], v[176:179], v[184:187], v[106:109]
	v_mfma_f32_16x16x32_bf16 v[102:105], v[162:165], v[192:195], v[102:105]
	v_mfma_f32_16x16x32_bf16 v[98:101], v[176:179], v[192:195], v[98:101]
	v_mfma_f32_16x16x32_bf16 v[86:89], v[162:165], v[200:203], v[86:89]
	v_mfma_f32_16x16x32_bf16 v[82:85], v[176:179], v[200:203], v[82:85]
	v_mfma_f32_16x16x32_bf16 v[70:73], v[162:165], v[208:211], v[70:73]
	v_mfma_f32_16x16x32_bf16 v[66:69], v[176:179], v[208:211], v[66:69]
	v_mfma_f32_16x16x32_bf16 v[110:113], v[172:175], v[188:191], v[110:113]
	v_mfma_f32_16x16x32_bf16 v[106:109], v[180:183], v[188:191], v[106:109]
	v_mfma_f32_16x16x32_bf16 v[102:105], v[172:175], v[196:199], v[102:105]
	v_mfma_f32_16x16x32_bf16 v[98:101], v[180:183], v[196:199], v[98:101]
	v_mfma_f32_16x16x32_bf16 v[86:89], v[172:175], v[204:207], v[86:89]
	v_mfma_f32_16x16x32_bf16 v[82:85], v[180:183], v[204:207], v[82:85]
	v_mfma_f32_16x16x32_bf16 v[70:73], v[172:175], v[212:215], v[70:73]
	v_mfma_f32_16x16x32_bf16 v[66:69], v[180:183], v[212:215], v[66:69]
	s_barrier
; #define PG8_STAGE(bufoff, gbase, voff) do { _Pragma("unroll") for (int _i = 0; _i < 2; ++_i) \
;         __builtin_amdgcn_global_load_lds((const unsigned*)((const char*)(gbase) + (voff)[_i]), (PG8_LAS unsigned*)(lds + (bufoff) + ldsw + _i * 8192), 16, 0, 0); } while (0)
; #define PG8_LDA(dst, b, h) do { _Pragma("unroll") for (int m = 0; m < 4; ++m) _Pragma("unroll") for (int k = 0; k < 2; ++k) dst[m][k] = *(const PG8_LAS bf16x8*)(lds + PG8_SA(b, h) + aoff + m * 2048 + k * 1024); } while (0)
; #define PG8_MMA(ai, bj, At, Bt) do { __builtin_amdgcn_s_setprio(1); _Pragma("unroll") for (int m = 0; m < 4; ++m) _Pragma("unroll") for (int n = 0; n < 2; ++n) _Pragma("unroll") for (int k = 0; k < 2; ++k) \
;         acc[ai][bj][m][n] = __builtin_amdgcn_mfma_f32_16x16x32_bf16(Bt[n][k], At[m][k], acc[ai][bj][m][n], 0, 0, 0); __builtin_amdgcn_s_setprio(0); } while (0)
; #define PG8_WAIT_V(n) asm volatile("s_waitcnt vmcnt(" #n ")" ::: "memory")
; #define PG8_WAIT_L(n) asm volatile("s_waitcnt lgkmcnt(" #n ")" ::: "memory")
; #define PG8_BAR __builtin_amdgcn_s_barrier()
; #define PG8_SCHED __builtin_amdgcn_sched_barrier(0)
; template <class Epi, class Sched, bool ALIGN_EPI = false>
; __device__ __forceinline__ void gemm_phase(PG8_LAS unsigned char* lds, const Gemm g, const Sched& S, const Epi& E) {
;     ...
;             PG8_LDA(At, 1, 1); PG8_STAGE(PG8_SB(1, 0), b3, voffB); PG8_STAGE(PG8_SB(1, 1), b3 + hstep, voffB); PG8_STAGE(PG8_SA(1, 0), a3, w0);
;             PG8_WAIT_V(8); PG8_WAIT_L(0); PG8_BAR; PG8_MMA(1, 0, At, B0); PG8_MMA(1, 1, At, B1); PG8_BAR; PG8_SCHED;
;             if constexpr (Epi::KSCALE) { if (((t + 2) & 7) == 0 && t + 2 < nt) { E.kscale(acc, pf, ((t + 2) >> 3) - 1, wr, fr); PG8_SCHED; } }
;         }
;         if constexpr (ALIGN_EPI) { if (wr == 0) PG8_BAR; }
	s_add_i32 s56, s79, s61
	v_lshl_add_u64 v[216:217], v[216:217], 0, s[18:19]
	s_mov_b32 m0, s56
	ds_read_b128 v[184:187], v170 offset:49152
	ds_read_b128 v[188:191], v170 offset:50176
	ds_read_b128 v[192:195], v170 offset:51200
	ds_read_b128 v[196:199], v170 offset:52224
	ds_read_b128 v[200:203], v170 offset:53248
	ds_read_b128 v[204:207], v170 offset:54272
	ds_read_b128 v[208:211], v170 offset:55296
	ds_read_b128 v[212:215], v170 offset:56320
	global_load_lds_dwordx4 v[216:217], off
	s_add_i32 m0, s56, 0x2000
	s_add_u32 s54, s54, 0x80080
	v_lshl_add_u64 v[216:217], v[218:219], 0, s[18:19]
	s_addc_u32 s55, s55, 0
	s_add_i32 s56, s80, s61
	global_load_lds_dwordx4 v[216:217], off
	v_lshl_add_u64 v[216:217], s[54:55], 0, v[140:141]
	s_mov_b32 m0, s56
	s_nop 0
	global_load_lds_dwordx4 v[216:217], off
	v_lshl_add_u64 v[216:217], s[54:55], 0, v[144:145]
	s_add_i32 m0, s56, 0x2000
	s_nop 0
	global_load_lds_dwordx4 v[216:217], off
	v_lshl_add_u64 v[216:217], v[220:221], 0, s[18:19]
	s_mov_b32 m0, s67
	s_nop 0
	global_load_lds_dwordx4 v[216:217], off
	v_lshl_add_u64 v[216:217], v[222:223], 0, s[18:19]
	s_mov_b32 m0, s68
	s_nop 0
	global_load_lds_dwordx4 v[216:217], off
	s_waitcnt vmcnt(8)
	s_waitcnt lgkmcnt(0)
	s_barrier
	v_mfma_f32_16x16x32_bf16 v[54:57], v[130:133], v[184:187], v[54:57]
	v_mfma_f32_16x16x32_bf16 v[50:53], v[154:157], v[184:187], v[50:53]
	v_mfma_f32_16x16x32_bf16 v[38:41], v[130:133], v[192:195], v[38:41]
	v_mfma_f32_16x16x32_bf16 v[34:37], v[154:157], v[192:195], v[34:37]
	v_mfma_f32_16x16x32_bf16 v[22:25], v[130:133], v[200:203], v[22:25]
	v_mfma_f32_16x16x32_bf16 v[18:21], v[154:157], v[200:203], v[18:21]
	v_mfma_f32_16x16x32_bf16 v[6:9], v[130:133], v[208:211], v[6:9]
	v_mfma_f32_16x16x32_bf16 v[2:5], v[154:157], v[208:211], v[2:5]
	v_mfma_f32_16x16x32_bf16 v[54:57], v[134:137], v[188:191], v[54:57]
	v_mfma_f32_16x16x32_bf16 v[50:53], v[158:161], v[188:191], v[50:53]
	v_mfma_f32_16x16x32_bf16 v[38:41], v[134:137], v[196:199], v[38:41]
	v_mfma_f32_16x16x32_bf16 v[34:37], v[158:161], v[196:199], v[34:37]
	v_mfma_f32_16x16x32_bf16 v[22:25], v[134:137], v[204:207], v[22:25]
	v_mfma_f32_16x16x32_bf16 v[18:21], v[158:161], v[204:207], v[18:21]
	v_mfma_f32_16x16x32_bf16 v[6:9], v[134:137], v[212:215], v[6:9]
	v_mfma_f32_16x16x32_bf16 v[2:5], v[158:161], v[212:215], v[2:5]
	v_mfma_f32_16x16x32_bf16 v[62:65], v[162:165], v[184:187], v[62:65]
	v_mfma_f32_16x16x32_bf16 v[58:61], v[176:179], v[184:187], v[58:61]
	v_mfma_f32_16x16x32_bf16 v[46:49], v[162:165], v[192:195], v[46:49]
	v_mfma_f32_16x16x32_bf16 v[42:45], v[176:179], v[192:195], v[42:45]
	v_mfma_f32_16x16x32_bf16 v[30:33], v[162:165], v[200:203], v[30:33]
	v_mfma_f32_16x16x32_bf16 v[26:29], v[176:179], v[200:203], v[26:29]
	v_mfma_f32_16x16x32_bf16 v[14:17], v[162:165], v[208:211], v[14:17]
	v_mfma_f32_16x16x32_bf16 v[10:13], v[176:179], v[208:211], v[10:13]
	v_mfma_f32_16x16x32_bf16 v[62:65], v[172:175], v[188:191], v[62:65]
	v_mfma_f32_16x16x32_bf16 v[58:61], v[180:183], v[188:191], v[58:61]
	v_mfma_f32_16x16x32_bf16 v[46:49], v[172:175], v[196:199], v[46:49]
	v_mfma_f32_16x16x32_bf16 v[42:45], v[180:183], v[196:199], v[42:45]
	v_mfma_f32_16x16x32_bf16 v[30:33], v[172:175], v[204:207], v[30:33]
	v_mfma_f32_16x16x32_bf16 v[26:29], v[180:183], v[204:207], v[26:29]
	v_mfma_f32_16x16x32_bf16 v[14:17], v[172:175], v[212:215], v[14:17]
	v_mfma_f32_16x16x32_bf16 v[10:13], v[180:183], v[212:215], v[10:13]
	s_barrier
	s_add_i32 s78, s78, 2
	s_add_u32 s52, s52, 0x100
	s_addc_u32 s53, s53, 0
	s_add_u32 s76, s76, 0x100
	s_addc_u32 s77, s77, 0
	s_cmp_gt_u32 s78, 29
	s_cbranch_scc0 .LBB0_1198
	s_and_b64 vcc, exec, s[22:23]
	s_cbranch_vccz .LBB0_1201
	s_barrier

; #define PG8_STAGE(bufoff, gbase, voff) do { _Pragma("unroll") for (int _i = 0; _i < 2; ++_i) \
;         __builtin_amdgcn_global_load_lds((const unsigned*)((const char*)(gbase) + (voff)[_i]), (PG8_LAS unsigned*)(lds + (bufoff) + ldsw + _i * 8192), 16, 0, 0); } while (0)
; #define PG8_LDA(dst, b, h) do { _Pragma("unroll") for (int m = 0; m < 4; ++m) _Pragma("unroll") for (int k = 0; k < 2; ++k) dst[m][k] = *(const PG8_LAS bf16x8*)(lds + PG8_SA(b, h) + aoff + m * 2048 + k * 1024); } while (0)
; #define PG8_LDB(dst, b, h) do { _Pragma("unroll") for (int n = 0; n < 2; ++n) _Pragma("unroll") for (int k = 0; k < 2; ++k) dst[n][k] = *(const PG8_LAS bf16x8*)(lds + PG8_SB(b, h) + boff + n * 2048 + k * 1024); } while (0)
; #define PG8_MMA(ai, bj, At, Bt) do { __builtin_amdgcn_s_setprio(1); _Pragma("unroll") for (int m = 0; m < 4; ++m) _Pragma("unroll") for (int n = 0; n < 2; ++n) _Pragma("unroll") for (int k = 0; k < 2; ++k) \
;         acc[ai][bj][m][n] = __builtin_amdgcn_mfma_f32_16x16x32_bf16(Bt[n][k], At[m][k], acc[ai][bj][m][n], 0, 0, 0); __builtin_amdgcn_s_setprio(0); } while (0)
; #define PG8_BAR __builtin_amdgcn_s_barrier()
; template <class Epi, class Sched, bool ALIGN_EPI = false>
; __device__ __forceinline__ void gemm_phase(PG8_LAS unsigned char* lds, const Gemm g, const Sched& S, const Epi& E) {
;     ...
;             const bool last = (t == nt - 2);
;             const char* a1 = cA + (size_t)(t + 1) * kstep;
;             const char* a2 = last ? nA : cA + (size_t)(t + 2) * kstep; const char* b2 = last ? nB : cB + (size_t)(t + 2) * kstep;
;             const char* a3 = a2 + kstep; const char* b3 = b2 + kstep;
;             unsigned w0[2], w1[2];
; #pragma unroll
;             for (int i = 0; i < 2; ++i) { w0[i] = (Sched::GATHER && last) ? vn0[i] : vc0[i]; w1[i] = (Sched::GATHER && last) ? vn1[i] : vc1[i]; }
;             if (last && has_next) S.a_ready(nxt);
;             PG8_LDB(B0, 0, 0); PG8_LDB(B1, 0, 1); PG8_SCHED; PG8_LDA(At, 0, 0); PG8_STAGE(PG8_SA(1, 1), a1 + hstepA, vc1);
;             PG8_WAIT_V(8); PG8_WAIT_L(0); PG8_BAR; PG8_MMA(0, 0, At, B0); PG8_MMA(0, 1, At, B1); PG8_BAR; PG8_SCHED;
;             PG8_LDA(At, 0, 1); PG8_STAGE(PG8_SB(0, 0), b2, voffB); PG8_STAGE(PG8_SB(0, 1), b2 + hstep, voffB); PG8_STAGE(PG8_SA(0, 0), a2, w0);
;             PG8_WAIT_V(8); PG8_WAIT_L(0); PG8_BAR; PG8_MMA(1, 0, At, B0); PG8_MMA(1, 1, At, B1); PG8_BAR; PG8_SCHED;
.LBB0_1414:
	s_add_u32 s56, s36, s54
	v_add_u32_e32 v155, s79, v143
	s_addc_u32 s57, s37, s55
	ds_read_b128 v[164:167], v155
	ds_read_b128 v[168:171], v155 offset:1024
	ds_read_b128 v[172:175], v155 offset:2048
	ds_read_b128 v[176:179], v155 offset:3072
	v_add_u32_e32 v155, s80, v143
	s_add_u32 s58, s56, 0x3c800100
	ds_read_b128 v[180:183], v155
	ds_read_b128 v[184:187], v155 offset:1024
	ds_read_b128 v[188:191], v155 offset:2048
	ds_read_b128 v[192:195], v155 offset:3072
	s_addc_u32 s59, s57, 0
	s_add_u32 s88, s47, s54
	s_addc_u32 s89, s86, s55
	s_cmpk_eq_i32 s54, 0xf00
	s_cselect_b64 vcc, -1, 0
	s_and_b64 s[56:57], vcc, exec
	v_cndmask_b32_e32 v134, v151, v149, vcc
	s_cselect_b32 s59, s21, s59
	s_cselect_b32 s58, s20, s58
	v_cndmask_b32_e32 v153, v152, v157, vcc
	v_cndmask_b32_e32 v228, v150, v162, vcc
	v_cndmask_b32_e32 v155, v154, v163, vcc
	s_cselect_b32 s57, s51, s89
	s_cselect_b32 s56, s50, s88
	v_lshl_add_u64 v[230:231], v[160:161], 0, s[54:55]
	s_add_i32 m0, s53, 0xc000
	ds_read_b128 v[196:199], v147
	ds_read_b128 v[200:203], v147 offset:1024
	ds_read_b128 v[204:207], v147 offset:2048
	ds_read_b128 v[208:211], v147 offset:3072
	ds_read_b128 v[212:215], v147 offset:4096
	ds_read_b128 v[216:219], v147 offset:5120
	ds_read_b128 v[220:223], v147 offset:6144
	ds_read_b128 v[224:227], v147 offset:7168
	global_load_lds_dwordx4 v[230:231], off
	v_lshl_add_u64 v[230:231], v[158:159], 0, s[54:55]
	s_add_i32 m0, s53, 0xe000
	s_nop 0
	global_load_lds_dwordx4 v[230:231], off
	s_waitcnt vmcnt(8)
	s_waitcnt lgkmcnt(0)
	s_barrier
	v_mfma_f32_16x16x32_bf16 v[126:129], v[164:167], v[196:199], v[126:129]
	v_mfma_f32_16x16x32_bf16 v[122:125], v[172:175], v[196:199], v[122:125]
	v_mfma_f32_16x16x32_bf16 v[110:113], v[164:167], v[204:207], v[110:113]
	v_mfma_f32_16x16x32_bf16 v[106:109], v[172:175], v[204:207], v[106:109]
	v_mfma_f32_16x16x32_bf16 v[94:97], v[164:167], v[212:215], v[94:97]
	v_mfma_f32_16x16x32_bf16 v[90:93], v[172:175], v[212:215], v[90:93]
	v_mfma_f32_16x16x32_bf16 v[78:81], v[164:167], v[220:223], v[78:81]
	v_mfma_f32_16x16x32_bf16 v[74:77], v[172:175], v[220:223], v[74:77]
	v_mfma_f32_16x16x32_bf16 v[126:129], v[168:171], v[200:203], v[126:129]
	v_mfma_f32_16x16x32_bf16 v[122:125], v[176:179], v[200:203], v[122:125]
	v_mfma_f32_16x16x32_bf16 v[110:113], v[168:171], v[208:211], v[110:113]
	v_mfma_f32_16x16x32_bf16 v[106:109], v[176:179], v[208:211], v[106:109]
	v_mfma_f32_16x16x32_bf16 v[94:97], v[168:171], v[216:219], v[94:97]
	v_mfma_f32_16x16x32_bf16 v[90:93], v[176:179], v[216:219], v[90:93]
	v_mfma_f32_16x16x32_bf16 v[78:81], v[168:171], v[224:227], v[78:81]
	v_mfma_f32_16x16x32_bf16 v[74:77], v[176:179], v[224:227], v[74:77]
	v_mfma_f32_16x16x32_bf16 v[118:121], v[180:183], v[196:199], v[118:121]
	v_mfma_f32_16x16x32_bf16 v[114:117], v[188:191], v[196:199], v[114:117]
	v_mfma_f32_16x16x32_bf16 v[102:105], v[180:183], v[204:207], v[102:105]
	v_mfma_f32_16x16x32_bf16 v[98:101], v[188:191], v[204:207], v[98:101]
	v_mfma_f32_16x16x32_bf16 v[86:89], v[180:183], v[212:215], v[86:89]
	v_mfma_f32_16x16x32_bf16 v[82:85], v[188:191], v[212:215], v[82:85]
	v_mfma_f32_16x16x32_bf16 v[70:73], v[180:183], v[220:223], v[70:73]
	v_mfma_f32_16x16x32_bf16 v[66:69], v[188:191], v[220:223], v[66:69]
	v_mfma_f32_16x16x32_bf16 v[118:121], v[184:187], v[200:203], v[118:121]
	v_mfma_f32_16x16x32_bf16 v[114:117], v[192:195], v[200:203], v[114:117]
	v_mfma_f32_16x16x32_bf16 v[102:105], v[184:187], v[208:211], v[102:105]
	v_mfma_f32_16x16x32_bf16 v[98:101], v[192:195], v[208:211], v[98:101]
	v_mfma_f32_16x16x32_bf16 v[86:89], v[184:187], v[216:219], v[86:89]
	v_mfma_f32_16x16x32_bf16 v[82:85], v[192:195], v[216:219], v[82:85]
	v_mfma_f32_16x16x32_bf16 v[70:73], v[184:187], v[224:227], v[70:73]
	v_mfma_f32_16x16x32_bf16 v[66:69], v[192:195], v[224:227], v[66:69]
	s_barrier
	s_add_i32 s88, s79, s71
	v_lshl_add_u64 v[230:231], s[56:57], 0, v[130:131]
	s_mov_b32 m0, s88
	ds_read_b128 v[196:199], v147 offset:16384
	ds_read_b128 v[200:203], v147 offset:17408
	ds_read_b128 v[204:207], v147 offset:18432
	ds_read_b128 v[208:211], v147 offset:19456
	ds_read_b128 v[212:215], v147 offset:20480
	ds_read_b128 v[216:219], v147 offset:21504
	ds_read_b128 v[220:223], v147 offset:22528
	ds_read_b128 v[224:227], v147 offset:23552
	global_load_lds_dwordx4 v[230:231], off
	s_add_i32 m0, s88, 0x2000
	s_add_u32 s88, s56, 0x80000
	v_lshl_add_u64 v[232:233], s[56:57], 0, v[132:133]
	s_addc_u32 s89, s57, 0
	s_add_i32 s90, s80, s71
	global_load_lds_dwordx4 v[232:233], off
	v_lshl_add_u64 v[234:235], s[88:89], 0, v[130:131]
	s_mov_b32 m0, s90
	v_mov_b32_e32 v229, v135
	global_load_lds_dwordx4 v[234:235], off
	v_lshl_add_u64 v[234:235], s[88:89], 0, v[132:133]
	s_add_i32 m0, s90, 0x2000
	s_nop 0
	global_load_lds_dwordx4 v[234:235], off
	s_mov_b32 m0, s53
	v_lshl_add_u64 v[234:235], s[58:59], 0, v[134:135]
	global_load_lds_dwordx4 v134, s[58:59]
	s_mov_b32 m0, s72
	s_nop 0
	global_load_lds_dwordx4 v228, s[58:59]
	s_waitcnt vmcnt(8)
	s_waitcnt lgkmcnt(0)
	v_lshl_add_u64 v[228:229], s[58:59], 0, v[228:229]
	s_barrier
; #define PG8_STAGE(bufoff, gbase, voff) do { _Pragma("unroll") for (int _i = 0; _i < 2; ++_i) \
;         __builtin_amdgcn_global_load_lds((const unsigned*)((const char*)(gbase) + (voff)[_i]), (PG8_LAS unsigned*)(lds + (bufoff) + ldsw + _i * 8192), 16, 0, 0); } while (0)
; #define PG8_LDA(dst, b, h) do { _Pragma("unroll") for (int m = 0; m < 4; ++m) _Pragma("unroll") for (int k = 0; k < 2; ++k) dst[m][k] = *(const PG8_LAS bf16x8*)(lds + PG8_SA(b, h) + aoff + m * 2048 + k * 1024); } while (0)
; #define PG8_LDB(dst, b, h) do { _Pragma("unroll") for (int n = 0; n < 2; ++n) _Pragma("unroll") for (int k = 0; k < 2; ++k) dst[n][k] = *(const PG8_LAS bf16x8*)(lds + PG8_SB(b, h) + boff + n * 2048 + k * 1024); } while (0)
; #define PG8_MMA(ai, bj, At, Bt) do { __builtin_amdgcn_s_setprio(1); _Pragma("unroll") for (int m = 0; m < 4; ++m) _Pragma("unroll") for (int n = 0; n < 2; ++n) _Pragma("unroll") for (int k = 0; k < 2; ++k) \
;         acc[ai][bj][m][n] = __builtin_amdgcn_mfma_f32_16x16x32_bf16(Bt[n][k], At[m][k], acc[ai][bj][m][n], 0, 0, 0); __builtin_amdgcn_s_setprio(0); } while (0)
; #define PG8_WAIT_V(n) asm volatile("s_waitcnt vmcnt(" #n ")" ::: "memory")
; #define PG8_WAIT_L(n) asm volatile("s_waitcnt lgkmcnt(" #n ")" ::: "memory")
; #define PG8_BAR __builtin_amdgcn_s_barrier()
; #define PG8_SCHED __builtin_amdgcn_sched_barrier(0)
; template <class Epi, class Sched, bool ALIGN_EPI = false>
; __device__ __forceinline__ void gemm_phase(PG8_LAS unsigned char* lds, const Gemm g, const Sched& S, const Epi& E) {
;     ...
;             PG8_WAIT_V(8); PG8_WAIT_L(0); PG8_BAR; PG8_MMA(1, 0, At, B0); PG8_MMA(1, 1, At, B1); PG8_BAR; PG8_SCHED;
;             PG8_LDB(B0, 1, 0); PG8_LDB(B1, 1, 1); PG8_SCHED; PG8_LDA(At, 1, 0); PG8_STAGE(PG8_SA(0, 1), a2 + hstepA, w1);
;             PG8_WAIT_V(8); PG8_WAIT_L(0); PG8_BAR; PG8_MMA(0, 0, At, B0); PG8_MMA(0, 1, At, B1); PG8_BAR; PG8_SCHED;
	v_mfma_f32_16x16x32_bf16 v[62:65], v[164:167], v[196:199], v[62:65]
	v_mfma_f32_16x16x32_bf16 v[58:61], v[172:175], v[196:199], v[58:61]
	v_mfma_f32_16x16x32_bf16 v[50:53], v[164:167], v[204:207], v[50:53]
	v_mfma_f32_16x16x32_bf16 v[42:45], v[172:175], v[204:207], v[42:45]
	v_mfma_f32_16x16x32_bf16 v[34:37], v[164:167], v[212:215], v[34:37]
	v_mfma_f32_16x16x32_bf16 v[30:33], v[172:175], v[212:215], v[30:33]
	v_mfma_f32_16x16x32_bf16 v[14:17], v[164:167], v[220:223], v[14:17]
	v_mfma_f32_16x16x32_bf16 v[2:5], v[172:175], v[220:223], v[2:5]
	v_mfma_f32_16x16x32_bf16 v[62:65], v[168:171], v[200:203], v[62:65]
	v_mfma_f32_16x16x32_bf16 v[58:61], v[176:179], v[200:203], v[58:61]
	v_mfma_f32_16x16x32_bf16 v[50:53], v[168:171], v[208:211], v[50:53]
	v_mfma_f32_16x16x32_bf16 v[42:45], v[176:179], v[208:211], v[42:45]
	v_mfma_f32_16x16x32_bf16 v[34:37], v[168:171], v[216:219], v[34:37]
	v_mfma_f32_16x16x32_bf16 v[30:33], v[176:179], v[216:219], v[30:33]
	v_mfma_f32_16x16x32_bf16 v[14:17], v[168:171], v[224:227], v[14:17]
	v_mfma_f32_16x16x32_bf16 v[2:5], v[176:179], v[224:227], v[2:5]
	v_mfma_f32_16x16x32_bf16 v[54:57], v[180:183], v[196:199], v[54:57]
	v_mfma_f32_16x16x32_bf16 v[46:49], v[188:191], v[196:199], v[46:49]
	v_mfma_f32_16x16x32_bf16 v[38:41], v[180:183], v[204:207], v[38:41]
	v_mfma_f32_16x16x32_bf16 v[26:29], v[188:191], v[204:207], v[26:29]
	v_mfma_f32_16x16x32_bf16 v[22:25], v[180:183], v[212:215], v[22:25]
	v_mfma_f32_16x16x32_bf16 v[18:21], v[188:191], v[212:215], v[18:21]
	v_mfma_f32_16x16x32_bf16 v[10:13], v[180:183], v[220:223], v[10:13]
	v_mfma_f32_16x16x32_bf16 v[6:9], v[188:191], v[220:223], v[6:9]
	v_mfma_f32_16x16x32_bf16 v[54:57], v[184:187], v[200:203], v[54:57]
	v_mfma_f32_16x16x32_bf16 v[46:49], v[192:195], v[200:203], v[46:49]
	v_mfma_f32_16x16x32_bf16 v[38:41], v[184:187], v[208:211], v[38:41]
	v_mfma_f32_16x16x32_bf16 v[26:29], v[192:195], v[208:211], v[26:29]
	v_mfma_f32_16x16x32_bf16 v[22:25], v[184:187], v[216:219], v[22:25]
	v_mfma_f32_16x16x32_bf16 v[18:21], v[192:195], v[216:219], v[18:21]
	v_mfma_f32_16x16x32_bf16 v[10:13], v[184:187], v[224:227], v[10:13]
	v_mfma_f32_16x16x32_bf16 v[6:9], v[192:195], v[224:227], v[6:9]
	s_barrier
	s_add_i32 s88, 0, 0x18000
	v_add_u32_e32 v134, s88, v143
	s_add_i32 s89, 0, 0x1c000
	ds_read_b128 v[164:167], v134
	ds_read_b128 v[168:171], v134 offset:1024
	ds_read_b128 v[172:175], v134 offset:2048
	ds_read_b128 v[176:179], v134 offset:3072
	v_add_u32_e32 v134, s89, v143
	ds_read_b128 v[180:183], v134
	ds_read_b128 v[184:187], v134 offset:1024
	ds_read_b128 v[188:191], v134 offset:2048
	ds_read_b128 v[192:195], v134 offset:3072
	s_mov_b32 m0, s73
	ds_read_b128 v[196:199], v147 offset:32768
	ds_read_b128 v[200:203], v147 offset:33792
	ds_read_b128 v[204:207], v147 offset:34816
	ds_read_b128 v[208:211], v147 offset:35840
	ds_read_b128 v[212:215], v147 offset:36864
	ds_read_b128 v[216:219], v147 offset:37888
	ds_read_b128 v[220:223], v147 offset:38912
	ds_read_b128 v[224:227], v147 offset:39936
	global_load_lds_dwordx4 v153, s[58:59]
	s_mov_b32 m0, s74
	s_nop 0
	global_load_lds_dwordx4 v155, s[58:59]
	s_waitcnt vmcnt(8)
	s_waitcnt lgkmcnt(0)
	s_barrier
	v_mfma_f32_16x16x32_bf16 v[126:129], v[164:167], v[196:199], v[126:129]
	v_mfma_f32_16x16x32_bf16 v[122:125], v[172:175], v[196:199], v[122:125]
	v_mfma_f32_16x16x32_bf16 v[110:113], v[164:167], v[204:207], v[110:113]
	v_mfma_f32_16x16x32_bf16 v[106:109], v[172:175], v[204:207], v[106:109]
	v_mfma_f32_16x16x32_bf16 v[94:97], v[164:167], v[212:215], v[94:97]
	v_mfma_f32_16x16x32_bf16 v[90:93], v[172:175], v[212:215], v[90:93]
	v_mfma_f32_16x16x32_bf16 v[78:81], v[164:167], v[220:223], v[78:81]
	v_mfma_f32_16x16x32_bf16 v[74:77], v[172:175], v[220:223], v[74:77]
	v_mfma_f32_16x16x32_bf16 v[126:129], v[168:171], v[200:203], v[126:129]
	v_mfma_f32_16x16x32_bf16 v[122:125], v[176:179], v[200:203], v[122:125]
	v_mfma_f32_16x16x32_bf16 v[110:113], v[168:171], v[208:211], v[110:113]
	v_mfma_f32_16x16x32_bf16 v[106:109], v[176:179], v[208:211], v[106:109]
	v_mfma_f32_16x16x32_bf16 v[94:97], v[168:171], v[216:219], v[94:97]
	v_mfma_f32_16x16x32_bf16 v[90:93], v[176:179], v[216:219], v[90:93]
	v_mfma_f32_16x16x32_bf16 v[78:81], v[168:171], v[224:227], v[78:81]
	v_mfma_f32_16x16x32_bf16 v[74:77], v[176:179], v[224:227], v[74:77]
	v_mfma_f32_16x16x32_bf16 v[118:121], v[180:183], v[196:199], v[118:121]
	v_mfma_f32_16x16x32_bf16 v[114:117], v[188:191], v[196:199], v[114:117]
	v_mfma_f32_16x16x32_bf16 v[102:105], v[180:183], v[204:207], v[102:105]
	v_mfma_f32_16x16x32_bf16 v[98:101], v[188:191], v[204:207], v[98:101]
	v_mfma_f32_16x16x32_bf16 v[86:89], v[180:183], v[212:215], v[86:89]
	v_mfma_f32_16x16x32_bf16 v[82:85], v[188:191], v[212:215], v[82:85]
	v_mfma_f32_16x16x32_bf16 v[70:73], v[180:183], v[220:223], v[70:73]
	v_mfma_f32_16x16x32_bf16 v[66:69], v[188:191], v[220:223], v[66:69]
	v_mfma_f32_16x16x32_bf16 v[118:121], v[184:187], v[200:203], v[118:121]
	v_mfma_f32_16x16x32_bf16 v[114:117], v[192:195], v[200:203], v[114:117]
	v_mfma_f32_16x16x32_bf16 v[102:105], v[184:187], v[208:211], v[102:105]
	v_mfma_f32_16x16x32_bf16 v[98:101], v[192:195], v[208:211], v[98:101]
	v_mfma_f32_16x16x32_bf16 v[86:89], v[184:187], v[216:219], v[86:89]
	v_mfma_f32_16x16x32_bf16 v[82:85], v[192:195], v[216:219], v[82:85]
	v_mfma_f32_16x16x32_bf16 v[70:73], v[184:187], v[224:227], v[70:73]
	v_mfma_f32_16x16x32_bf16 v[66:69], v[192:195], v[224:227], v[66:69]
	s_barrier
; #define PG8_STAGE(bufoff, gbase, voff) do { _Pragma("unroll") for (int _i = 0; _i < 2; ++_i) \
;         __builtin_amdgcn_global_load_lds((const unsigned*)((const char*)(gbase) + (voff)[_i]), (PG8_LAS unsigned*)(lds + (bufoff) + ldsw + _i * 8192), 16, 0, 0); } while (0)
; #define PG8_LDA(dst, b, h) do { _Pragma("unroll") for (int m = 0; m < 4; ++m) _Pragma("unroll") for (int k = 0; k < 2; ++k) dst[m][k] = *(const PG8_LAS bf16x8*)(lds + PG8_SA(b, h) + aoff + m * 2048 + k * 1024); } while (0)
; #define PG8_MMA(ai, bj, At, Bt) do { __builtin_amdgcn_s_setprio(1); _Pragma("unroll") for (int m = 0; m < 4; ++m) _Pragma("unroll") for (int n = 0; n < 2; ++n) _Pragma("unroll") for (int k = 0; k < 2; ++k) \
;         acc[ai][bj][m][n] = __builtin_amdgcn_mfma_f32_16x16x32_bf16(Bt[n][k], At[m][k], acc[ai][bj][m][n], 0, 0, 0); __builtin_amdgcn_s_setprio(0); } while (0)
; #define PG8_WAIT_V(n) asm volatile("s_waitcnt vmcnt(" #n ")" ::: "memory")
; #define PG8_WAIT_L(n) asm volatile("s_waitcnt lgkmcnt(" #n ")" ::: "memory")
; #define PG8_BAR __builtin_amdgcn_s_barrier()
; #define PG8_SCHED __builtin_amdgcn_sched_barrier(0)
; template <class Epi, class Sched, bool ALIGN_EPI = false>
; __device__ __forceinline__ void gemm_phase(PG8_LAS unsigned char* lds, const Gemm g, const Sched& S, const Epi& E) {
;     ...
;             PG8_LDA(At, 1, 1); PG8_STAGE(PG8_SB(1, 0), b3, voffB); PG8_STAGE(PG8_SB(1, 1), b3 + hstep, voffB); PG8_STAGE(PG8_SA(1, 0), a3, w0);
;             PG8_WAIT_V(8); PG8_WAIT_L(0); PG8_BAR; PG8_MMA(1, 0, At, B0); PG8_MMA(1, 1, At, B1); PG8_BAR; PG8_SCHED;
;             if constexpr (Epi::KSCALE) { if (((t + 2) & 7) == 0 && t + 2 < nt) { E.kscale(acc, pf, ((t + 2) >> 3) - 1, wr, fr); PG8_SCHED; } }
;         }
;         if constexpr (ALIGN_EPI) { if (wr == 0) PG8_BAR; }
	s_add_i32 s58, s88, s71
	v_lshl_add_u64 v[230:231], v[230:231], 0, s[42:43]
	s_mov_b32 m0, s58
	ds_read_b128 v[196:199], v147 offset:49152
	ds_read_b128 v[200:203], v147 offset:50176
	ds_read_b128 v[204:207], v147 offset:51200
	ds_read_b128 v[208:211], v147 offset:52224
	ds_read_b128 v[212:215], v147 offset:53248
	ds_read_b128 v[216:219], v147 offset:54272
	ds_read_b128 v[220:223], v147 offset:55296
	ds_read_b128 v[224:227], v147 offset:56320
	global_load_lds_dwordx4 v[230:231], off
	s_add_i32 m0, s58, 0x2000
	s_add_u32 s56, s56, 0x80080
	v_lshl_add_u64 v[230:231], v[232:233], 0, s[42:43]
	s_addc_u32 s57, s57, 0
	s_add_i32 s58, s89, s71
	global_load_lds_dwordx4 v[230:231], off
	v_lshl_add_u64 v[230:231], s[56:57], 0, v[130:131]
	s_mov_b32 m0, s58
	v_lshl_add_u64 v[228:229], v[228:229], 0, s[42:43]
	global_load_lds_dwordx4 v[230:231], off
	v_lshl_add_u64 v[230:231], s[56:57], 0, v[132:133]
	s_add_i32 m0, s58, 0x2000
	s_nop 0
	global_load_lds_dwordx4 v[230:231], off
	v_lshl_add_u64 v[230:231], v[234:235], 0, s[42:43]
	s_mov_b32 m0, s77
	s_nop 0
	global_load_lds_dwordx4 v[230:231], off
	s_mov_b32 m0, s78
	s_nop 0
	global_load_lds_dwordx4 v[228:229], off
	s_waitcnt vmcnt(8)
	s_waitcnt lgkmcnt(0)
	s_barrier
	v_mfma_f32_16x16x32_bf16 v[62:65], v[164:167], v[196:199], v[62:65]
	v_mfma_f32_16x16x32_bf16 v[58:61], v[172:175], v[196:199], v[58:61]
	v_mfma_f32_16x16x32_bf16 v[50:53], v[164:167], v[204:207], v[50:53]
	v_mfma_f32_16x16x32_bf16 v[42:45], v[172:175], v[204:207], v[42:45]
	v_mfma_f32_16x16x32_bf16 v[34:37], v[164:167], v[212:215], v[34:37]
	v_mfma_f32_16x16x32_bf16 v[30:33], v[172:175], v[212:215], v[30:33]
	v_mfma_f32_16x16x32_bf16 v[14:17], v[164:167], v[220:223], v[14:17]
	v_mfma_f32_16x16x32_bf16 v[2:5], v[172:175], v[220:223], v[2:5]
	v_mfma_f32_16x16x32_bf16 v[62:65], v[168:171], v[200:203], v[62:65]
	v_mfma_f32_16x16x32_bf16 v[58:61], v[176:179], v[200:203], v[58:61]
	v_mfma_f32_16x16x32_bf16 v[50:53], v[168:171], v[208:211], v[50:53]
	v_mfma_f32_16x16x32_bf16 v[42:45], v[176:179], v[208:211], v[42:45]
	v_mfma_f32_16x16x32_bf16 v[34:37], v[168:171], v[216:219], v[34:37]
	v_mfma_f32_16x16x32_bf16 v[30:33], v[176:179], v[216:219], v[30:33]
	v_mfma_f32_16x16x32_bf16 v[14:17], v[168:171], v[224:227], v[14:17]
	v_mfma_f32_16x16x32_bf16 v[2:5], v[176:179], v[224:227], v[2:5]
	v_mfma_f32_16x16x32_bf16 v[54:57], v[180:183], v[196:199], v[54:57]
	v_mfma_f32_16x16x32_bf16 v[46:49], v[188:191], v[196:199], v[46:49]
	v_mfma_f32_16x16x32_bf16 v[38:41], v[180:183], v[204:207], v[38:41]
	v_mfma_f32_16x16x32_bf16 v[26:29], v[188:191], v[204:207], v[26:29]
	v_mfma_f32_16x16x32_bf16 v[22:25], v[180:183], v[212:215], v[22:25]
	v_mfma_f32_16x16x32_bf16 v[18:21], v[188:191], v[212:215], v[18:21]
	v_mfma_f32_16x16x32_bf16 v[10:13], v[180:183], v[220:223], v[10:13]
	v_mfma_f32_16x16x32_bf16 v[6:9], v[188:191], v[220:223], v[6:9]
	v_mfma_f32_16x16x32_bf16 v[54:57], v[184:187], v[200:203], v[54:57]
	v_mfma_f32_16x16x32_bf16 v[46:49], v[192:195], v[200:203], v[46:49]
	v_mfma_f32_16x16x32_bf16 v[38:41], v[184:187], v[208:211], v[38:41]
	v_mfma_f32_16x16x32_bf16 v[26:29], v[192:195], v[208:211], v[26:29]
	v_mfma_f32_16x16x32_bf16 v[22:25], v[184:187], v[216:219], v[22:25]
	v_mfma_f32_16x16x32_bf16 v[18:21], v[192:195], v[216:219], v[18:21]
	v_mfma_f32_16x16x32_bf16 v[10:13], v[184:187], v[224:227], v[10:13]
	v_mfma_f32_16x16x32_bf16 v[6:9], v[192:195], v[224:227], v[6:9]
	s_barrier
	s_add_i32 s87, s87, 2
	s_add_u32 s54, s54, 0x100
	s_addc_u32 s55, s55, 0
	s_cmp_gt_u32 s87, 29
	s_cbranch_scc0 .LBB0_1414
	s_and_b64 vcc, exec, s[44:45]
	s_cbranch_vccz .LBB0_1417
	s_barrier

; #define PG8_STAGE(bufoff, gbase, voff) do { _Pragma("unroll") for (int _i = 0; _i < 2; ++_i) \
;         __builtin_amdgcn_global_load_lds((const unsigned*)((const char*)(gbase) + (voff)[_i]), (PG8_LAS unsigned*)(lds + (bufoff) + ldsw + _i * 8192), 16, 0, 0); } while (0)
; #define PG8_LDA(dst, b, h) do { _Pragma("unroll") for (int m = 0; m < 4; ++m) _Pragma("unroll") for (int k = 0; k < 2; ++k) dst[m][k] = *(const PG8_LAS bf16x8*)(lds + PG8_SA(b, h) + aoff + m * 2048 + k * 1024); } while (0)
; #define PG8_LDB(dst, b, h) do { _Pragma("unroll") for (int n = 0; n < 2; ++n) _Pragma("unroll") for (int k = 0; k < 2; ++k) dst[n][k] = *(const PG8_LAS bf16x8*)(lds + PG8_SB(b, h) + boff + n * 2048 + k * 1024); } while (0)
; #define PG8_MMA(ai, bj, At, Bt) do { __builtin_amdgcn_s_setprio(1); _Pragma("unroll") for (int m = 0; m < 4; ++m) _Pragma("unroll") for (int n = 0; n < 2; ++n) _Pragma("unroll") for (int k = 0; k < 2; ++k) \
;         acc[ai][bj][m][n] = __builtin_amdgcn_mfma_f32_16x16x32_bf16(Bt[n][k], At[m][k], acc[ai][bj][m][n], 0, 0, 0); __builtin_amdgcn_s_setprio(0); } while (0)
; #define PG8_BAR __builtin_amdgcn_s_barrier()
; template <class Epi, class Sched, bool ALIGN_EPI = false>
; __device__ __forceinline__ void gemm_phase(PG8_LAS unsigned char* lds, const Gemm g, const Sched& S, const Epi& E) {
;     ...
;             const bool last = (t == nt - 2);
;             const char* a1 = cA + (size_t)(t + 1) * kstep;
;             const char* a2 = last ? nA : cA + (size_t)(t + 2) * kstep; const char* b2 = last ? nB : cB + (size_t)(t + 2) * kstep;
;             const char* a3 = a2 + kstep; const char* b3 = b2 + kstep;
;             unsigned w0[2], w1[2];
; #pragma unroll
;             for (int i = 0; i < 2; ++i) { w0[i] = (Sched::GATHER && last) ? vn0[i] : vc0[i]; w1[i] = (Sched::GATHER && last) ? vn1[i] : vc1[i]; }
;             if (last && has_next) S.a_ready(nxt);
;             PG8_LDB(B0, 0, 0); PG8_LDB(B1, 0, 1); PG8_SCHED; PG8_LDA(At, 0, 0); PG8_STAGE(PG8_SA(1, 1), a1 + hstepA, vc1);
;             PG8_WAIT_V(8); PG8_WAIT_L(0); PG8_BAR; PG8_MMA(0, 0, At, B0); PG8_MMA(0, 1, At, B1); PG8_BAR; PG8_SCHED;
;             PG8_LDA(At, 0, 1); PG8_STAGE(PG8_SB(0, 0), b2, voffB); PG8_STAGE(PG8_SB(0, 1), b2 + hstep, voffB); PG8_STAGE(PG8_SA(0, 0), a2, w0);
;             PG8_WAIT_V(8); PG8_WAIT_L(0); PG8_BAR; PG8_MMA(1, 0, At, B0); PG8_MMA(1, 1, At, B1); PG8_BAR; PG8_SCHED;
.LBB0_1480:
	ds_read_b128 v[172:175], v167
	ds_read_b128 v[176:179], v167 offset:1024
	ds_read_b128 v[180:183], v167 offset:2048
	ds_read_b128 v[184:187], v167 offset:3072
	ds_read_b128 v[188:191], v168
	ds_read_b128 v[192:195], v168 offset:1024
	ds_read_b128 v[196:199], v168 offset:2048
	ds_read_b128 v[200:203], v168 offset:3072
	s_add_u32 s16, s14, 0x3c800100
	s_addc_u32 s17, s15, 0
	s_add_u32 s56, s14, s43
	s_addc_u32 s57, s15, s44
	s_cmp_eq_u32 s45, 28
	s_cselect_b32 s19, s21, s17
	s_cselect_b32 s18, s20, s16
	s_cselect_b32 s17, s11, s57
	s_cselect_b32 s16, s10, s56
	s_mov_b32 m0, s46
	v_lshl_add_u64 v[236:237], s[14:15], 0, v[160:161]
	ds_read_b128 v[204:207], v169
	ds_read_b128 v[208:211], v169 offset:1024
	ds_read_b128 v[212:215], v169 offset:2048
	ds_read_b128 v[216:219], v169 offset:3072
	ds_read_b128 v[220:223], v169 offset:4096
	ds_read_b128 v[224:227], v169 offset:5120
	ds_read_b128 v[228:231], v169 offset:6144
	ds_read_b128 v[232:235], v169 offset:7168
	global_load_lds_dwordx4 v[236:237], off
	v_lshl_add_u64 v[236:237], s[14:15], 0, v[158:159]
	s_mov_b32 m0, s47
	s_nop 0
	global_load_lds_dwordx4 v[236:237], off
	s_waitcnt vmcnt(8)
	s_waitcnt lgkmcnt(0)
	s_barrier
	v_mfma_f32_16x16x32_bf16 v[126:129], v[172:175], v[204:207], v[126:129]
	v_mfma_f32_16x16x32_bf16 v[122:125], v[180:183], v[204:207], v[122:125]
	v_mfma_f32_16x16x32_bf16 v[110:113], v[172:175], v[212:215], v[110:113]
	v_mfma_f32_16x16x32_bf16 v[106:109], v[180:183], v[212:215], v[106:109]
	v_mfma_f32_16x16x32_bf16 v[94:97], v[172:175], v[220:223], v[94:97]
	v_mfma_f32_16x16x32_bf16 v[90:93], v[180:183], v[220:223], v[90:93]
	v_mfma_f32_16x16x32_bf16 v[78:81], v[172:175], v[228:231], v[78:81]
	v_mfma_f32_16x16x32_bf16 v[74:77], v[180:183], v[228:231], v[74:77]
	v_mfma_f32_16x16x32_bf16 v[126:129], v[176:179], v[208:211], v[126:129]
	v_mfma_f32_16x16x32_bf16 v[122:125], v[184:187], v[208:211], v[122:125]
	v_mfma_f32_16x16x32_bf16 v[110:113], v[176:179], v[216:219], v[110:113]
	v_mfma_f32_16x16x32_bf16 v[106:109], v[184:187], v[216:219], v[106:109]
	v_mfma_f32_16x16x32_bf16 v[94:97], v[176:179], v[224:227], v[94:97]
	v_mfma_f32_16x16x32_bf16 v[90:93], v[184:187], v[224:227], v[90:93]
	v_mfma_f32_16x16x32_bf16 v[78:81], v[176:179], v[232:235], v[78:81]
	v_mfma_f32_16x16x32_bf16 v[74:77], v[184:187], v[232:235], v[74:77]
	v_mfma_f32_16x16x32_bf16 v[118:121], v[188:191], v[204:207], v[118:121]
	v_mfma_f32_16x16x32_bf16 v[114:117], v[196:199], v[204:207], v[114:117]
	v_mfma_f32_16x16x32_bf16 v[102:105], v[188:191], v[212:215], v[102:105]
	v_mfma_f32_16x16x32_bf16 v[98:101], v[196:199], v[212:215], v[98:101]
	v_mfma_f32_16x16x32_bf16 v[86:89], v[188:191], v[220:223], v[86:89]
	v_mfma_f32_16x16x32_bf16 v[82:85], v[196:199], v[220:223], v[82:85]
	v_mfma_f32_16x16x32_bf16 v[70:73], v[188:191], v[228:231], v[70:73]
	v_mfma_f32_16x16x32_bf16 v[66:69], v[196:199], v[228:231], v[66:69]
	v_mfma_f32_16x16x32_bf16 v[118:121], v[192:195], v[208:211], v[118:121]
	v_mfma_f32_16x16x32_bf16 v[114:117], v[200:203], v[208:211], v[114:117]
	v_mfma_f32_16x16x32_bf16 v[102:105], v[192:195], v[216:219], v[102:105]
	v_mfma_f32_16x16x32_bf16 v[98:101], v[200:203], v[216:219], v[98:101]
	v_mfma_f32_16x16x32_bf16 v[86:89], v[192:195], v[224:227], v[86:89]
	v_mfma_f32_16x16x32_bf16 v[82:85], v[200:203], v[224:227], v[82:85]
	v_mfma_f32_16x16x32_bf16 v[70:73], v[192:195], v[232:235], v[70:73]
	v_mfma_f32_16x16x32_bf16 v[66:69], v[200:203], v[232:235], v[66:69]
	s_barrier
	s_mov_b32 m0, s48
	v_lshl_add_u64 v[236:237], s[16:17], 0, v[146:147]
	s_add_u32 s56, s16, 0x80000
	ds_read_b128 v[204:207], v169 offset:16384
	ds_read_b128 v[208:211], v169 offset:17408
	ds_read_b128 v[212:215], v169 offset:18432
	ds_read_b128 v[216:219], v169 offset:19456
	ds_read_b128 v[220:223], v169 offset:20480
	ds_read_b128 v[224:227], v169 offset:21504
	ds_read_b128 v[228:231], v169 offset:22528
	ds_read_b128 v[232:235], v169 offset:23552
	global_load_lds_dwordx4 v[236:237], off
	v_lshl_add_u64 v[238:239], s[16:17], 0, v[144:145]
	s_mov_b32 m0, s49
	s_addc_u32 s57, s17, 0
	global_load_lds_dwordx4 v[238:239], off
	v_lshl_add_u64 v[240:241], s[56:57], 0, v[146:147]
	s_mov_b32 m0, s50
	v_lshl_add_u64 v[242:243], s[18:19], 0, v[150:151]
	global_load_lds_dwordx4 v[240:241], off
	v_lshl_add_u64 v[240:241], s[56:57], 0, v[144:145]
	s_mov_b32 m0, s51
	s_nop 0
	global_load_lds_dwordx4 v[240:241], off
	v_lshl_add_u64 v[240:241], s[18:19], 0, v[148:149]
	s_mov_b32 m0, s25
	s_nop 0
	global_load_lds_dwordx4 v[240:241], off
	s_mov_b32 m0, s26
	s_nop 0
	global_load_lds_dwordx4 v[242:243], off
	s_waitcnt vmcnt(8)
	s_waitcnt lgkmcnt(0)
	s_barrier
; #define PG8_STAGE(bufoff, gbase, voff) do { _Pragma("unroll") for (int _i = 0; _i < 2; ++_i) \
;         __builtin_amdgcn_global_load_lds((const unsigned*)((const char*)(gbase) + (voff)[_i]), (PG8_LAS unsigned*)(lds + (bufoff) + ldsw + _i * 8192), 16, 0, 0); } while (0)
; #define PG8_LDA(dst, b, h) do { _Pragma("unroll") for (int m = 0; m < 4; ++m) _Pragma("unroll") for (int k = 0; k < 2; ++k) dst[m][k] = *(const PG8_LAS bf16x8*)(lds + PG8_SA(b, h) + aoff + m * 2048 + k * 1024); } while (0)
; #define PG8_LDB(dst, b, h) do { _Pragma("unroll") for (int n = 0; n < 2; ++n) _Pragma("unroll") for (int k = 0; k < 2; ++k) dst[n][k] = *(const PG8_LAS bf16x8*)(lds + PG8_SB(b, h) + boff + n * 2048 + k * 1024); } while (0)
; #define PG8_MMA(ai, bj, At, Bt) do { __builtin_amdgcn_s_setprio(1); _Pragma("unroll") for (int m = 0; m < 4; ++m) _Pragma("unroll") for (int n = 0; n < 2; ++n) _Pragma("unroll") for (int k = 0; k < 2; ++k) \
;         acc[ai][bj][m][n] = __builtin_amdgcn_mfma_f32_16x16x32_bf16(Bt[n][k], At[m][k], acc[ai][bj][m][n], 0, 0, 0); __builtin_amdgcn_s_setprio(0); } while (0)
; #define PG8_WAIT_V(n) asm volatile("s_waitcnt vmcnt(" #n ")" ::: "memory")
; #define PG8_WAIT_L(n) asm volatile("s_waitcnt lgkmcnt(" #n ")" ::: "memory")
; #define PG8_BAR __builtin_amdgcn_s_barrier()
; #define PG8_SCHED __builtin_amdgcn_sched_barrier(0)
; template <class Epi, class Sched, bool ALIGN_EPI = false>
; __device__ __forceinline__ void gemm_phase(PG8_LAS unsigned char* lds, const Gemm g, const Sched& S, const Epi& E) {
;     ...
;             PG8_WAIT_V(8); PG8_WAIT_L(0); PG8_BAR; PG8_MMA(1, 0, At, B0); PG8_MMA(1, 1, At, B1); PG8_BAR; PG8_SCHED;
;             PG8_LDB(B0, 1, 0); PG8_LDB(B1, 1, 1); PG8_SCHED; PG8_LDA(At, 1, 0); PG8_STAGE(PG8_SA(0, 1), a2 + hstepA, w1);
;             PG8_WAIT_V(8); PG8_WAIT_L(0); PG8_BAR; PG8_MMA(0, 0, At, B0); PG8_MMA(0, 1, At, B1); PG8_BAR; PG8_SCHED;
	v_mfma_f32_16x16x32_bf16 v[62:65], v[172:175], v[204:207], v[62:65]
	v_mfma_f32_16x16x32_bf16 v[58:61], v[180:183], v[204:207], v[58:61]
	v_mfma_f32_16x16x32_bf16 v[50:53], v[172:175], v[212:215], v[50:53]
	v_mfma_f32_16x16x32_bf16 v[42:45], v[180:183], v[212:215], v[42:45]
	v_mfma_f32_16x16x32_bf16 v[34:37], v[172:175], v[220:223], v[34:37]
	v_mfma_f32_16x16x32_bf16 v[26:29], v[180:183], v[220:223], v[26:29]
	v_mfma_f32_16x16x32_bf16 v[14:17], v[172:175], v[228:231], v[14:17]
	v_mfma_f32_16x16x32_bf16 v[2:5], v[180:183], v[228:231], v[2:5]
	v_mfma_f32_16x16x32_bf16 v[62:65], v[176:179], v[208:211], v[62:65]
	v_mfma_f32_16x16x32_bf16 v[58:61], v[184:187], v[208:211], v[58:61]
	v_mfma_f32_16x16x32_bf16 v[50:53], v[176:179], v[216:219], v[50:53]
	v_mfma_f32_16x16x32_bf16 v[42:45], v[184:187], v[216:219], v[42:45]
	v_mfma_f32_16x16x32_bf16 v[34:37], v[176:179], v[224:227], v[34:37]
	v_mfma_f32_16x16x32_bf16 v[26:29], v[184:187], v[224:227], v[26:29]
	v_mfma_f32_16x16x32_bf16 v[14:17], v[176:179], v[232:235], v[14:17]
	v_mfma_f32_16x16x32_bf16 v[2:5], v[184:187], v[232:235], v[2:5]
	v_mfma_f32_16x16x32_bf16 v[54:57], v[188:191], v[204:207], v[54:57]
	v_mfma_f32_16x16x32_bf16 v[46:49], v[196:199], v[204:207], v[46:49]
	v_mfma_f32_16x16x32_bf16 v[38:41], v[188:191], v[212:215], v[38:41]
	v_mfma_f32_16x16x32_bf16 v[30:33], v[196:199], v[212:215], v[30:33]
	v_mfma_f32_16x16x32_bf16 v[22:25], v[188:191], v[220:223], v[22:25]
	v_mfma_f32_16x16x32_bf16 v[18:21], v[196:199], v[220:223], v[18:21]
	v_mfma_f32_16x16x32_bf16 v[10:13], v[188:191], v[228:231], v[10:13]
	v_mfma_f32_16x16x32_bf16 v[6:9], v[196:199], v[228:231], v[6:9]
	v_mfma_f32_16x16x32_bf16 v[54:57], v[192:195], v[208:211], v[54:57]
	v_mfma_f32_16x16x32_bf16 v[46:49], v[200:203], v[208:211], v[46:49]
	v_mfma_f32_16x16x32_bf16 v[38:41], v[192:195], v[216:219], v[38:41]
	v_mfma_f32_16x16x32_bf16 v[30:33], v[200:203], v[216:219], v[30:33]
	v_mfma_f32_16x16x32_bf16 v[22:25], v[192:195], v[224:227], v[22:25]
	v_mfma_f32_16x16x32_bf16 v[18:21], v[200:203], v[224:227], v[18:21]
	v_mfma_f32_16x16x32_bf16 v[10:13], v[192:195], v[232:235], v[10:13]
	v_mfma_f32_16x16x32_bf16 v[6:9], v[200:203], v[232:235], v[6:9]
	s_barrier
	ds_read_b128 v[172:175], v170
	ds_read_b128 v[176:179], v170 offset:1024
	ds_read_b128 v[180:183], v170 offset:2048
	ds_read_b128 v[184:187], v170 offset:3072
	ds_read_b128 v[188:191], v171
	ds_read_b128 v[192:195], v171 offset:1024
	ds_read_b128 v[196:199], v171 offset:2048
	ds_read_b128 v[200:203], v171 offset:3072
	s_mov_b32 m0, s27
	v_lshl_add_u64 v[244:245], s[18:19], 0, v[152:153]
	ds_read_b128 v[204:207], v169 offset:32768
	ds_read_b128 v[208:211], v169 offset:33792
	ds_read_b128 v[212:215], v169 offset:34816
	ds_read_b128 v[216:219], v169 offset:35840
	ds_read_b128 v[220:223], v169 offset:36864
	ds_read_b128 v[224:227], v169 offset:37888
	ds_read_b128 v[228:231], v169 offset:38912
	ds_read_b128 v[232:235], v169 offset:39936
	global_load_lds_dwordx4 v[244:245], off
	v_lshl_add_u64 v[244:245], s[18:19], 0, v[154:155]
	s_mov_b32 m0, s35
	s_nop 0
	global_load_lds_dwordx4 v[244:245], off
	s_waitcnt vmcnt(8)
	s_waitcnt lgkmcnt(0)
	s_barrier
	v_mfma_f32_16x16x32_bf16 v[126:129], v[172:175], v[204:207], v[126:129]
	v_mfma_f32_16x16x32_bf16 v[122:125], v[180:183], v[204:207], v[122:125]
	v_mfma_f32_16x16x32_bf16 v[110:113], v[172:175], v[212:215], v[110:113]
	v_mfma_f32_16x16x32_bf16 v[106:109], v[180:183], v[212:215], v[106:109]
	v_mfma_f32_16x16x32_bf16 v[94:97], v[172:175], v[220:223], v[94:97]
	v_mfma_f32_16x16x32_bf16 v[90:93], v[180:183], v[220:223], v[90:93]
	v_mfma_f32_16x16x32_bf16 v[78:81], v[172:175], v[228:231], v[78:81]
	v_mfma_f32_16x16x32_bf16 v[74:77], v[180:183], v[228:231], v[74:77]
	v_mfma_f32_16x16x32_bf16 v[126:129], v[176:179], v[208:211], v[126:129]
	v_mfma_f32_16x16x32_bf16 v[122:125], v[184:187], v[208:211], v[122:125]
	v_mfma_f32_16x16x32_bf16 v[110:113], v[176:179], v[216:219], v[110:113]
	v_mfma_f32_16x16x32_bf16 v[106:109], v[184:187], v[216:219], v[106:109]
	v_mfma_f32_16x16x32_bf16 v[94:97], v[176:179], v[224:227], v[94:97]
	v_mfma_f32_16x16x32_bf16 v[90:93], v[184:187], v[224:227], v[90:93]
	v_mfma_f32_16x16x32_bf16 v[78:81], v[176:179], v[232:235], v[78:81]
	v_mfma_f32_16x16x32_bf16 v[74:77], v[184:187], v[232:235], v[74:77]
	v_mfma_f32_16x16x32_bf16 v[118:121], v[188:191], v[204:207], v[118:121]
	v_mfma_f32_16x16x32_bf16 v[114:117], v[196:199], v[204:207], v[114:117]
	v_mfma_f32_16x16x32_bf16 v[102:105], v[188:191], v[212:215], v[102:105]
	v_mfma_f32_16x16x32_bf16 v[98:101], v[196:199], v[212:215], v[98:101]
	v_mfma_f32_16x16x32_bf16 v[86:89], v[188:191], v[220:223], v[86:89]
	v_mfma_f32_16x16x32_bf16 v[82:85], v[196:199], v[220:223], v[82:85]
	v_mfma_f32_16x16x32_bf16 v[70:73], v[188:191], v[228:231], v[70:73]
	v_mfma_f32_16x16x32_bf16 v[66:69], v[196:199], v[228:231], v[66:69]
	v_mfma_f32_16x16x32_bf16 v[118:121], v[192:195], v[208:211], v[118:121]
	v_mfma_f32_16x16x32_bf16 v[114:117], v[200:203], v[208:211], v[114:117]
	v_mfma_f32_16x16x32_bf16 v[102:105], v[192:195], v[216:219], v[102:105]
	v_mfma_f32_16x16x32_bf16 v[98:101], v[200:203], v[216:219], v[98:101]
	v_mfma_f32_16x16x32_bf16 v[86:89], v[192:195], v[224:227], v[86:89]
	v_mfma_f32_16x16x32_bf16 v[82:85], v[200:203], v[224:227], v[82:85]
	v_mfma_f32_16x16x32_bf16 v[70:73], v[192:195], v[232:235], v[70:73]
	v_mfma_f32_16x16x32_bf16 v[66:69], v[200:203], v[232:235], v[66:69]
	s_barrier
; #define PG8_STAGE(bufoff, gbase, voff) do { _Pragma("unroll") for (int _i = 0; _i < 2; ++_i) \
;         __builtin_amdgcn_global_load_lds((const unsigned*)((const char*)(gbase) + (voff)[_i]), (PG8_LAS unsigned*)(lds + (bufoff) + ldsw + _i * 8192), 16, 0, 0); } while (0)
; #define PG8_LDA(dst, b, h) do { _Pragma("unroll") for (int m = 0; m < 4; ++m) _Pragma("unroll") for (int k = 0; k < 2; ++k) dst[m][k] = *(const PG8_LAS bf16x8*)(lds + PG8_SA(b, h) + aoff + m * 2048 + k * 1024); } while (0)
; #define PG8_MMA(ai, bj, At, Bt) do { __builtin_amdgcn_s_setprio(1); _Pragma("unroll") for (int m = 0; m < 4; ++m) _Pragma("unroll") for (int n = 0; n < 2; ++n) _Pragma("unroll") for (int k = 0; k < 2; ++k) \
;         acc[ai][bj][m][n] = __builtin_amdgcn_mfma_f32_16x16x32_bf16(Bt[n][k], At[m][k], acc[ai][bj][m][n], 0, 0, 0); __builtin_amdgcn_s_setprio(0); } while (0)
; #define PG8_WAIT_V(n) asm volatile("s_waitcnt vmcnt(" #n ")" ::: "memory")
; #define PG8_WAIT_L(n) asm volatile("s_waitcnt lgkmcnt(" #n ")" ::: "memory")
; #define PG8_BAR __builtin_amdgcn_s_barrier()
; #define PG8_SCHED __builtin_amdgcn_sched_barrier(0)
; template <class Epi, class Sched, bool ALIGN_EPI = false>
; __device__ __forceinline__ void gemm_phase(PG8_LAS unsigned char* lds, const Gemm g, const Sched& S, const Epi& E) {
;     ...
;             PG8_LDA(At, 1, 1); PG8_STAGE(PG8_SB(1, 0), b3, voffB); PG8_STAGE(PG8_SB(1, 1), b3 + hstep, voffB); PG8_STAGE(PG8_SA(1, 0), a3, w0);
;             PG8_WAIT_V(8); PG8_WAIT_L(0); PG8_BAR; PG8_MMA(1, 0, At, B0); PG8_MMA(1, 1, At, B1); PG8_BAR; PG8_SCHED;
;             if constexpr (Epi::KSCALE) { if (((t + 2) & 7) == 0 && t + 2 < nt) { E.kscale(acc, pf, ((t + 2) >> 3) - 1, wr, fr); PG8_SCHED; } }
;         }
;         if constexpr (ALIGN_EPI) { if (wr == 0) PG8_BAR; }
	s_mov_b32 m0, s52
	v_lshl_add_u64 v[236:237], v[236:237], 0, s[12:13]
	s_add_u32 s16, s16, 0x80080
	ds_read_b128 v[204:207], v169 offset:49152
	ds_read_b128 v[208:211], v169 offset:50176
	ds_read_b128 v[212:215], v169 offset:51200
	ds_read_b128 v[216:219], v169 offset:52224
	ds_read_b128 v[220:223], v169 offset:53248
	ds_read_b128 v[224:227], v169 offset:54272
	ds_read_b128 v[228:231], v169 offset:55296
	ds_read_b128 v[232:235], v169 offset:56320
	global_load_lds_dwordx4 v[236:237], off
	v_lshl_add_u64 v[236:237], v[238:239], 0, s[12:13]
	s_mov_b32 m0, s53
	s_addc_u32 s17, s17, 0
	global_load_lds_dwordx4 v[236:237], off
	v_lshl_add_u64 v[236:237], s[16:17], 0, v[146:147]
	s_mov_b32 m0, s54
	s_nop 0
	global_load_lds_dwordx4 v[236:237], off
	v_lshl_add_u64 v[236:237], s[16:17], 0, v[144:145]
	s_mov_b32 m0, s55
	s_nop 0
	global_load_lds_dwordx4 v[236:237], off
	v_lshl_add_u64 v[236:237], v[240:241], 0, s[12:13]
	s_mov_b32 m0, s41
	s_nop 0
	global_load_lds_dwordx4 v[236:237], off
	v_lshl_add_u64 v[236:237], v[242:243], 0, s[12:13]
	s_mov_b32 m0, s42
	s_nop 0
	global_load_lds_dwordx4 v[236:237], off
	s_waitcnt vmcnt(8)
	s_waitcnt lgkmcnt(0)
	s_barrier
	v_mfma_f32_16x16x32_bf16 v[62:65], v[172:175], v[204:207], v[62:65]
	v_mfma_f32_16x16x32_bf16 v[58:61], v[180:183], v[204:207], v[58:61]
	v_mfma_f32_16x16x32_bf16 v[50:53], v[172:175], v[212:215], v[50:53]
	v_mfma_f32_16x16x32_bf16 v[42:45], v[180:183], v[212:215], v[42:45]
	v_mfma_f32_16x16x32_bf16 v[34:37], v[172:175], v[220:223], v[34:37]
	v_mfma_f32_16x16x32_bf16 v[26:29], v[180:183], v[220:223], v[26:29]
	v_mfma_f32_16x16x32_bf16 v[14:17], v[172:175], v[228:231], v[14:17]
	v_mfma_f32_16x16x32_bf16 v[2:5], v[180:183], v[228:231], v[2:5]
	v_mfma_f32_16x16x32_bf16 v[62:65], v[176:179], v[208:211], v[62:65]
	v_mfma_f32_16x16x32_bf16 v[58:61], v[184:187], v[208:211], v[58:61]
	v_mfma_f32_16x16x32_bf16 v[50:53], v[176:179], v[216:219], v[50:53]
	v_mfma_f32_16x16x32_bf16 v[42:45], v[184:187], v[216:219], v[42:45]
	v_mfma_f32_16x16x32_bf16 v[34:37], v[176:179], v[224:227], v[34:37]
	v_mfma_f32_16x16x32_bf16 v[26:29], v[184:187], v[224:227], v[26:29]
	v_mfma_f32_16x16x32_bf16 v[14:17], v[176:179], v[232:235], v[14:17]
	v_mfma_f32_16x16x32_bf16 v[2:5], v[184:187], v[232:235], v[2:5]
	v_mfma_f32_16x16x32_bf16 v[54:57], v[188:191], v[204:207], v[54:57]
	v_mfma_f32_16x16x32_bf16 v[46:49], v[196:199], v[204:207], v[46:49]
	v_mfma_f32_16x16x32_bf16 v[38:41], v[188:191], v[212:215], v[38:41]
	v_mfma_f32_16x16x32_bf16 v[30:33], v[196:199], v[212:215], v[30:33]
	v_mfma_f32_16x16x32_bf16 v[22:25], v[188:191], v[220:223], v[22:25]
	v_mfma_f32_16x16x32_bf16 v[18:21], v[196:199], v[220:223], v[18:21]
	v_mfma_f32_16x16x32_bf16 v[10:13], v[188:191], v[228:231], v[10:13]
	v_mfma_f32_16x16x32_bf16 v[6:9], v[196:199], v[228:231], v[6:9]
	v_mfma_f32_16x16x32_bf16 v[54:57], v[192:195], v[208:211], v[54:57]
	v_mfma_f32_16x16x32_bf16 v[46:49], v[200:203], v[208:211], v[46:49]
	v_mfma_f32_16x16x32_bf16 v[38:41], v[192:195], v[216:219], v[38:41]
	v_mfma_f32_16x16x32_bf16 v[30:33], v[200:203], v[216:219], v[30:33]
	v_mfma_f32_16x16x32_bf16 v[22:25], v[192:195], v[224:227], v[22:25]
	v_mfma_f32_16x16x32_bf16 v[18:21], v[200:203], v[224:227], v[18:21]
	v_mfma_f32_16x16x32_bf16 v[10:13], v[192:195], v[232:235], v[10:13]
	v_mfma_f32_16x16x32_bf16 v[6:9], v[200:203], v[232:235], v[6:9]
	s_barrier
	s_add_i32 s45, s45, 2
	s_add_u32 s14, s14, 0x100
	s_addc_u32 s15, s15, 0
	s_cmp_gt_u32 s45, 29
	s_cbranch_scc0 .LBB0_1480
	s_cmpk_lt_u32 s22, 0x100
	s_cbranch_scc0 .LBB0_1483
	s_barrier

; #define PG8_STAGE(bufoff, gbase, voff) do { _Pragma("unroll") for (int _i = 0; _i < 2; ++_i) \
;         __builtin_amdgcn_global_load_lds((const unsigned*)((const char*)(gbase) + (voff)[_i]), (PG8_LAS unsigned*)(lds + (bufoff) + ldsw + _i * 8192), 16, 0, 0); } while (0)
; #define PG8_LDA(dst, b, h) do { _Pragma("unroll") for (int m = 0; m < 4; ++m) _Pragma("unroll") for (int k = 0; k < 2; ++k) dst[m][k] = *(const PG8_LAS bf16x8*)(lds + PG8_SA(b, h) + aoff + m * 2048 + k * 1024); } while (0)
; #define PG8_LDB(dst, b, h) do { _Pragma("unroll") for (int n = 0; n < 2; ++n) _Pragma("unroll") for (int k = 0; k < 2; ++k) dst[n][k] = *(const PG8_LAS bf16x8*)(lds + PG8_SB(b, h) + boff + n * 2048 + k * 1024); } while (0)
; #define PG8_MMA(ai, bj, At, Bt) do { __builtin_amdgcn_s_setprio(1); _Pragma("unroll") for (int m = 0; m < 4; ++m) _Pragma("unroll") for (int n = 0; n < 2; ++n) _Pragma("unroll") for (int k = 0; k < 2; ++k) \
;         acc[ai][bj][m][n] = __builtin_amdgcn_mfma_f32_16x16x32_bf16(Bt[n][k], At[m][k], acc[ai][bj][m][n], 0, 0, 0); __builtin_amdgcn_s_setprio(0); } while (0)
; #define PG8_WAIT_V(n) asm volatile("s_waitcnt vmcnt(" #n ")" ::: "memory")
; #define PG8_WAIT_L(n) asm volatile("s_waitcnt lgkmcnt(" #n ")" ::: "memory")
; #define PG8_BAR __builtin_amdgcn_s_barrier()
; #define PG8_SCHED __builtin_amdgcn_sched_barrier(0)
; template <class Epi, class Sched, bool ALIGN_EPI = false>
; __device__ __forceinline__ void gemm_phase(PG8_LAS unsigned char* lds, const Gemm g, const Sched& S, const Epi& E) {
;     ...
;             PG8_LDB(B0, 0, 0); PG8_LDB(B1, 0, 1); PG8_SCHED; PG8_LDA(At, 0, 0); PG8_STAGE(PG8_SA(1, 1), a1 + hstepA, vc1);
;             PG8_WAIT_V(8); PG8_WAIT_L(0); PG8_BAR; PG8_MMA(0, 0, At, B0); PG8_MMA(0, 1, At, B1); PG8_BAR; PG8_SCHED;
;             PG8_LDA(At, 0, 1); PG8_STAGE(PG8_SB(0, 0), b2, voffB); PG8_STAGE(PG8_SB(0, 1), b2 + hstep, voffB); PG8_STAGE(PG8_SA(0, 0), a2, w0);
;             PG8_WAIT_V(8); PG8_WAIT_L(0); PG8_BAR; PG8_MMA(1, 0, At, B0); PG8_MMA(1, 1, At, B1); PG8_BAR; PG8_SCHED;
.LBB0_1498:
	ds_read_b128 v[142:145], v1
	ds_read_b128 v[158:161], v1 offset:1024
	ds_read_b128 v[162:165], v1 offset:2048
	ds_read_b128 v[166:169], v1 offset:3072
	ds_read_b128 v[170:173], v156
	ds_read_b128 v[174:177], v156 offset:1024
	ds_read_b128 v[178:181], v156 offset:2048
	ds_read_b128 v[182:185], v156 offset:3072
	s_add_u32 s58, s56, 0xfffe0080
	s_addc_u32 s59, s57, -1
	s_cmp_eq_u32 s87, 4
	s_cselect_b32 s61, s41, s59
	s_cselect_b32 s60, s53, s58
	s_cselect_b32 s59, s43, s86
	s_cselect_b32 s58, s84, s85
	v_lshl_add_u64 v[218:219], s[56:57], 0, v[140:141]
	s_add_i32 m0, s55, 0xc000
	ds_read_b128 v[186:189], v157
	ds_read_b128 v[190:193], v157 offset:1024
	ds_read_b128 v[194:197], v157 offset:2048
	ds_read_b128 v[198:201], v157 offset:3072
	ds_read_b128 v[202:205], v157 offset:4096
	ds_read_b128 v[206:209], v157 offset:5120
	ds_read_b128 v[210:213], v157 offset:6144
	ds_read_b128 v[214:217], v157 offset:7168
	global_load_lds_dwordx4 v[218:219], off
	v_lshl_add_u64 v[218:219], s[56:57], 0, v[138:139]
	s_add_i32 m0, s55, 0xe000
	s_nop 0
	global_load_lds_dwordx4 v[218:219], off
	s_waitcnt vmcnt(8)
	s_waitcnt lgkmcnt(0)
	s_barrier
	v_mfma_f32_16x16x32_bf16 v[126:129], v[142:145], v[186:189], v[126:129]
	v_mfma_f32_16x16x32_bf16 v[122:125], v[162:165], v[186:189], v[122:125]
	v_mfma_f32_16x16x32_bf16 v[114:117], v[142:145], v[194:197], v[114:117]
	v_mfma_f32_16x16x32_bf16 v[106:109], v[162:165], v[194:197], v[106:109]
	v_mfma_f32_16x16x32_bf16 v[98:101], v[142:145], v[202:205], v[98:101]
	v_mfma_f32_16x16x32_bf16 v[90:93], v[162:165], v[202:205], v[90:93]
	v_mfma_f32_16x16x32_bf16 v[82:85], v[142:145], v[210:213], v[82:85]
	v_mfma_f32_16x16x32_bf16 v[74:77], v[162:165], v[210:213], v[74:77]
	v_mfma_f32_16x16x32_bf16 v[126:129], v[158:161], v[190:193], v[126:129]
	v_mfma_f32_16x16x32_bf16 v[122:125], v[166:169], v[190:193], v[122:125]
	v_mfma_f32_16x16x32_bf16 v[114:117], v[158:161], v[198:201], v[114:117]
	v_mfma_f32_16x16x32_bf16 v[106:109], v[166:169], v[198:201], v[106:109]
	v_mfma_f32_16x16x32_bf16 v[98:101], v[158:161], v[206:209], v[98:101]
	v_mfma_f32_16x16x32_bf16 v[90:93], v[166:169], v[206:209], v[90:93]
	v_mfma_f32_16x16x32_bf16 v[82:85], v[158:161], v[214:217], v[82:85]
	v_mfma_f32_16x16x32_bf16 v[74:77], v[166:169], v[214:217], v[74:77]
	v_mfma_f32_16x16x32_bf16 v[118:121], v[170:173], v[186:189], v[118:121]
	v_mfma_f32_16x16x32_bf16 v[110:113], v[178:181], v[186:189], v[110:113]
	v_mfma_f32_16x16x32_bf16 v[102:105], v[170:173], v[194:197], v[102:105]
	v_mfma_f32_16x16x32_bf16 v[94:97], v[178:181], v[194:197], v[94:97]
	v_mfma_f32_16x16x32_bf16 v[86:89], v[170:173], v[202:205], v[86:89]
	v_mfma_f32_16x16x32_bf16 v[78:81], v[178:181], v[202:205], v[78:81]
	v_mfma_f32_16x16x32_bf16 v[62:65], v[170:173], v[210:213], v[62:65]
	v_mfma_f32_16x16x32_bf16 v[58:61], v[178:181], v[210:213], v[58:61]
	v_mfma_f32_16x16x32_bf16 v[118:121], v[174:177], v[190:193], v[118:121]
	v_mfma_f32_16x16x32_bf16 v[110:113], v[182:185], v[190:193], v[110:113]
	v_mfma_f32_16x16x32_bf16 v[102:105], v[174:177], v[198:201], v[102:105]
	v_mfma_f32_16x16x32_bf16 v[94:97], v[182:185], v[198:201], v[94:97]
	v_mfma_f32_16x16x32_bf16 v[86:89], v[174:177], v[206:209], v[86:89]
	v_mfma_f32_16x16x32_bf16 v[78:81], v[182:185], v[206:209], v[78:81]
	v_mfma_f32_16x16x32_bf16 v[62:65], v[174:177], v[214:217], v[62:65]
	v_mfma_f32_16x16x32_bf16 v[58:61], v[182:185], v[214:217], v[58:61]
	s_barrier
	s_add_i32 s88, s74, s62
	v_lshl_add_u64 v[218:219], s[58:59], 0, v[132:133]
	s_mov_b32 m0, s88
	ds_read_b128 v[186:189], v157 offset:16384
	ds_read_b128 v[190:193], v157 offset:17408
	ds_read_b128 v[194:197], v157 offset:18432
	ds_read_b128 v[198:201], v157 offset:19456
	ds_read_b128 v[202:205], v157 offset:20480
	ds_read_b128 v[206:209], v157 offset:21504
	ds_read_b128 v[210:213], v157 offset:22528
	ds_read_b128 v[214:217], v157 offset:23552
	global_load_lds_dwordx4 v[218:219], off
	s_add_i32 m0, s88, 0x2000
	s_add_u32 s88, s58, 0x20000
	v_lshl_add_u64 v[220:221], s[58:59], 0, v[136:137]
	s_addc_u32 s89, s59, 0
	s_add_i32 s90, s75, s62
	global_load_lds_dwordx4 v[220:221], off
	v_lshl_add_u64 v[222:223], s[88:89], 0, v[132:133]
	s_mov_b32 m0, s90
	v_lshl_add_u64 v[224:225], s[60:61], 0, v[134:135]
	global_load_lds_dwordx4 v[222:223], off
	v_lshl_add_u64 v[222:223], s[88:89], 0, v[136:137]
	s_add_i32 m0, s90, 0x2000
	s_nop 0
	global_load_lds_dwordx4 v[222:223], off
	v_lshl_add_u64 v[222:223], s[60:61], 0, v[130:131]
	s_mov_b32 m0, s55
	s_nop 0
	global_load_lds_dwordx4 v[222:223], off
	s_mov_b32 m0, s63
	s_nop 0
	global_load_lds_dwordx4 v[224:225], off
	s_waitcnt vmcnt(8)
	s_waitcnt lgkmcnt(0)
	s_barrier
; #define PG8_STAGE(bufoff, gbase, voff) do { _Pragma("unroll") for (int _i = 0; _i < 2; ++_i) \
;         __builtin_amdgcn_global_load_lds((const unsigned*)((const char*)(gbase) + (voff)[_i]), (PG8_LAS unsigned*)(lds + (bufoff) + ldsw + _i * 8192), 16, 0, 0); } while (0)
; #define PG8_LDA(dst, b, h) do { _Pragma("unroll") for (int m = 0; m < 4; ++m) _Pragma("unroll") for (int k = 0; k < 2; ++k) dst[m][k] = *(const PG8_LAS bf16x8*)(lds + PG8_SA(b, h) + aoff + m * 2048 + k * 1024); } while (0)
; #define PG8_LDB(dst, b, h) do { _Pragma("unroll") for (int n = 0; n < 2; ++n) _Pragma("unroll") for (int k = 0; k < 2; ++k) dst[n][k] = *(const PG8_LAS bf16x8*)(lds + PG8_SB(b, h) + boff + n * 2048 + k * 1024); } while (0)
; #define PG8_MMA(ai, bj, At, Bt) do { __builtin_amdgcn_s_setprio(1); _Pragma("unroll") for (int m = 0; m < 4; ++m) _Pragma("unroll") for (int n = 0; n < 2; ++n) _Pragma("unroll") for (int k = 0; k < 2; ++k) \
;         acc[ai][bj][m][n] = __builtin_amdgcn_mfma_f32_16x16x32_bf16(Bt[n][k], At[m][k], acc[ai][bj][m][n], 0, 0, 0); __builtin_amdgcn_s_setprio(0); } while (0)
; #define PG8_WAIT_V(n) asm volatile("s_waitcnt vmcnt(" #n ")" ::: "memory")
; #define PG8_WAIT_L(n) asm volatile("s_waitcnt lgkmcnt(" #n ")" ::: "memory")
; #define PG8_BAR __builtin_amdgcn_s_barrier()
; #define PG8_SCHED __builtin_amdgcn_sched_barrier(0)
; template <class Epi, class Sched, bool ALIGN_EPI = false>
; __device__ __forceinline__ void gemm_phase(PG8_LAS unsigned char* lds, const Gemm g, const Sched& S, const Epi& E) {
;     ...
;             PG8_WAIT_V(8); PG8_WAIT_L(0); PG8_BAR; PG8_MMA(1, 0, At, B0); PG8_MMA(1, 1, At, B1); PG8_BAR; PG8_SCHED;
;             PG8_LDB(B0, 1, 0); PG8_LDB(B1, 1, 1); PG8_SCHED; PG8_LDA(At, 1, 0); PG8_STAGE(PG8_SA(0, 1), a2 + hstepA, w1);
;             PG8_WAIT_V(8); PG8_WAIT_L(0); PG8_BAR; PG8_MMA(0, 0, At, B0); PG8_MMA(0, 1, At, B1); PG8_BAR; PG8_SCHED;
	v_mfma_f32_16x16x32_bf16 v[54:57], v[142:145], v[186:189], v[54:57]
	v_mfma_f32_16x16x32_bf16 v[42:45], v[162:165], v[186:189], v[42:45]
	v_mfma_f32_16x16x32_bf16 v[30:33], v[142:145], v[194:197], v[30:33]
	v_mfma_f32_16x16x32_bf16 v[26:29], v[162:165], v[194:197], v[26:29]
	v_mfma_f32_16x16x32_bf16 v[14:17], v[142:145], v[202:205], v[14:17]
	v_mfma_f32_16x16x32_bf16 v[10:13], v[162:165], v[202:205], v[10:13]
	v_mfma_f32_16x16x32_bf16 v[6:9], v[142:145], v[210:213], v[6:9]
	v_mfma_f32_16x16x32_bf16 v[2:5], v[162:165], v[210:213], v[2:5]
	v_mfma_f32_16x16x32_bf16 v[54:57], v[158:161], v[190:193], v[54:57]
	v_mfma_f32_16x16x32_bf16 v[42:45], v[166:169], v[190:193], v[42:45]
	v_mfma_f32_16x16x32_bf16 v[30:33], v[158:161], v[198:201], v[30:33]
	v_mfma_f32_16x16x32_bf16 v[26:29], v[166:169], v[198:201], v[26:29]
	v_mfma_f32_16x16x32_bf16 v[14:17], v[158:161], v[206:209], v[14:17]
	v_mfma_f32_16x16x32_bf16 v[10:13], v[166:169], v[206:209], v[10:13]
	v_mfma_f32_16x16x32_bf16 v[6:9], v[158:161], v[214:217], v[6:9]
	v_mfma_f32_16x16x32_bf16 v[2:5], v[166:169], v[214:217], v[2:5]
	v_mfma_f32_16x16x32_bf16 v[70:73], v[170:173], v[186:189], v[70:73]
	v_mfma_f32_16x16x32_bf16 v[66:69], v[178:181], v[186:189], v[66:69]
	v_mfma_f32_16x16x32_bf16 v[50:53], v[170:173], v[194:197], v[50:53]
	v_mfma_f32_16x16x32_bf16 v[46:49], v[178:181], v[194:197], v[46:49]
	v_mfma_f32_16x16x32_bf16 v[38:41], v[170:173], v[202:205], v[38:41]
	v_mfma_f32_16x16x32_bf16 v[34:37], v[178:181], v[202:205], v[34:37]
	v_mfma_f32_16x16x32_bf16 v[22:25], v[170:173], v[210:213], v[22:25]
	v_mfma_f32_16x16x32_bf16 v[18:21], v[178:181], v[210:213], v[18:21]
	v_mfma_f32_16x16x32_bf16 v[70:73], v[174:177], v[190:193], v[70:73]
	v_mfma_f32_16x16x32_bf16 v[66:69], v[182:185], v[190:193], v[66:69]
	v_mfma_f32_16x16x32_bf16 v[50:53], v[174:177], v[198:201], v[50:53]
	v_mfma_f32_16x16x32_bf16 v[46:49], v[182:185], v[198:201], v[46:49]
	v_mfma_f32_16x16x32_bf16 v[38:41], v[174:177], v[206:209], v[38:41]
	v_mfma_f32_16x16x32_bf16 v[34:37], v[182:185], v[206:209], v[34:37]
	v_mfma_f32_16x16x32_bf16 v[22:25], v[174:177], v[214:217], v[22:25]
	v_mfma_f32_16x16x32_bf16 v[18:21], v[182:185], v[214:217], v[18:21]
	s_barrier
	s_add_i32 s88, 0, 0x18000
	s_add_i32 s89, 0, 0x1c000
	v_add_u32_e32 v166, s88, v147
	v_add_u32_e32 v182, s89, v147
	ds_read_b128 v[142:145], v166
	ds_read_b128 v[158:161], v166 offset:1024
	ds_read_b128 v[162:165], v166 offset:2048
	ds_read_b128 v[166:169], v166 offset:3072
	ds_read_b128 v[170:173], v182
	ds_read_b128 v[174:177], v182 offset:1024
	ds_read_b128 v[178:181], v182 offset:2048
	ds_read_b128 v[182:185], v182 offset:3072
	s_add_u32 s60, s60, 0x20000
	s_addc_u32 s61, s61, 0
	s_mov_b32 m0, s64
	v_lshl_add_u64 v[226:227], s[60:61], 0, v[130:131]
	ds_read_b128 v[186:189], v157 offset:32768
	ds_read_b128 v[190:193], v157 offset:33792
	ds_read_b128 v[194:197], v157 offset:34816
	ds_read_b128 v[198:201], v157 offset:35840
	ds_read_b128 v[202:205], v157 offset:36864
	ds_read_b128 v[206:209], v157 offset:37888
	ds_read_b128 v[210:213], v157 offset:38912
	ds_read_b128 v[214:217], v157 offset:39936
	global_load_lds_dwordx4 v[226:227], off
	v_lshl_add_u64 v[226:227], s[60:61], 0, v[134:135]
	s_mov_b32 m0, s65
	s_nop 0
	global_load_lds_dwordx4 v[226:227], off
	s_waitcnt vmcnt(8)
	s_waitcnt lgkmcnt(0)
	s_barrier
	v_mfma_f32_16x16x32_bf16 v[126:129], v[142:145], v[186:189], v[126:129]
	v_mfma_f32_16x16x32_bf16 v[122:125], v[162:165], v[186:189], v[122:125]
	v_mfma_f32_16x16x32_bf16 v[114:117], v[142:145], v[194:197], v[114:117]
	v_mfma_f32_16x16x32_bf16 v[106:109], v[162:165], v[194:197], v[106:109]
	v_mfma_f32_16x16x32_bf16 v[98:101], v[142:145], v[202:205], v[98:101]
	v_mfma_f32_16x16x32_bf16 v[90:93], v[162:165], v[202:205], v[90:93]
	v_mfma_f32_16x16x32_bf16 v[82:85], v[142:145], v[210:213], v[82:85]
	v_mfma_f32_16x16x32_bf16 v[74:77], v[162:165], v[210:213], v[74:77]
	v_mfma_f32_16x16x32_bf16 v[126:129], v[158:161], v[190:193], v[126:129]
	v_mfma_f32_16x16x32_bf16 v[122:125], v[166:169], v[190:193], v[122:125]
	v_mfma_f32_16x16x32_bf16 v[114:117], v[158:161], v[198:201], v[114:117]
	v_mfma_f32_16x16x32_bf16 v[106:109], v[166:169], v[198:201], v[106:109]
	v_mfma_f32_16x16x32_bf16 v[98:101], v[158:161], v[206:209], v[98:101]
	v_mfma_f32_16x16x32_bf16 v[90:93], v[166:169], v[206:209], v[90:93]
	v_mfma_f32_16x16x32_bf16 v[82:85], v[158:161], v[214:217], v[82:85]
	v_mfma_f32_16x16x32_bf16 v[74:77], v[166:169], v[214:217], v[74:77]
	v_mfma_f32_16x16x32_bf16 v[118:121], v[170:173], v[186:189], v[118:121]
	v_mfma_f32_16x16x32_bf16 v[110:113], v[178:181], v[186:189], v[110:113]
	v_mfma_f32_16x16x32_bf16 v[102:105], v[170:173], v[194:197], v[102:105]
	v_mfma_f32_16x16x32_bf16 v[94:97], v[178:181], v[194:197], v[94:97]
	v_mfma_f32_16x16x32_bf16 v[86:89], v[170:173], v[202:205], v[86:89]
	v_mfma_f32_16x16x32_bf16 v[78:81], v[178:181], v[202:205], v[78:81]
	v_mfma_f32_16x16x32_bf16 v[62:65], v[170:173], v[210:213], v[62:65]
	v_mfma_f32_16x16x32_bf16 v[58:61], v[178:181], v[210:213], v[58:61]
	v_mfma_f32_16x16x32_bf16 v[118:121], v[174:177], v[190:193], v[118:121]
	v_mfma_f32_16x16x32_bf16 v[110:113], v[182:185], v[190:193], v[110:113]
	v_mfma_f32_16x16x32_bf16 v[102:105], v[174:177], v[198:201], v[102:105]
	v_mfma_f32_16x16x32_bf16 v[94:97], v[182:185], v[198:201], v[94:97]
	v_mfma_f32_16x16x32_bf16 v[86:89], v[174:177], v[206:209], v[86:89]
	v_mfma_f32_16x16x32_bf16 v[78:81], v[182:185], v[206:209], v[78:81]
	v_mfma_f32_16x16x32_bf16 v[62:65], v[174:177], v[214:217], v[62:65]
	v_mfma_f32_16x16x32_bf16 v[58:61], v[182:185], v[214:217], v[58:61]
	s_barrier
; #define PG8_STAGE(bufoff, gbase, voff) do { _Pragma("unroll") for (int _i = 0; _i < 2; ++_i) \
;         __builtin_amdgcn_global_load_lds((const unsigned*)((const char*)(gbase) + (voff)[_i]), (PG8_LAS unsigned*)(lds + (bufoff) + ldsw + _i * 8192), 16, 0, 0); } while (0)
; #define PG8_LDA(dst, b, h) do { _Pragma("unroll") for (int m = 0; m < 4; ++m) _Pragma("unroll") for (int k = 0; k < 2; ++k) dst[m][k] = *(const PG8_LAS bf16x8*)(lds + PG8_SA(b, h) + aoff + m * 2048 + k * 1024); } while (0)
; #define PG8_MMA(ai, bj, At, Bt) do { __builtin_amdgcn_s_setprio(1); _Pragma("unroll") for (int m = 0; m < 4; ++m) _Pragma("unroll") for (int n = 0; n < 2; ++n) _Pragma("unroll") for (int k = 0; k < 2; ++k) \
;         acc[ai][bj][m][n] = __builtin_amdgcn_mfma_f32_16x16x32_bf16(Bt[n][k], At[m][k], acc[ai][bj][m][n], 0, 0, 0); __builtin_amdgcn_s_setprio(0); } while (0)
; #define PG8_WAIT_V(n) asm volatile("s_waitcnt vmcnt(" #n ")" ::: "memory")
; #define PG8_WAIT_L(n) asm volatile("s_waitcnt lgkmcnt(" #n ")" ::: "memory")
; #define PG8_BAR __builtin_amdgcn_s_barrier()
; #define PG8_SCHED __builtin_amdgcn_sched_barrier(0)
; template <class Epi, class Sched, bool ALIGN_EPI = false>
; __device__ __forceinline__ void gemm_phase(PG8_LAS unsigned char* lds, const Gemm g, const Sched& S, const Epi& E) {
;     ...
;             PG8_LDA(At, 1, 1); PG8_STAGE(PG8_SB(1, 0), b3, voffB); PG8_STAGE(PG8_SB(1, 1), b3 + hstep, voffB); PG8_STAGE(PG8_SA(1, 0), a3, w0);
;             PG8_WAIT_V(8); PG8_WAIT_L(0); PG8_BAR; PG8_MMA(1, 0, At, B0); PG8_MMA(1, 1, At, B1); PG8_BAR; PG8_SCHED;
;             if constexpr (Epi::KSCALE) { if (((t + 2) & 7) == 0 && t + 2 < nt) { E.kscale(acc, pf, ((t + 2) >> 3) - 1, wr, fr); PG8_SCHED; } }
;         }
;         if constexpr (ALIGN_EPI) { if (wr == 0) PG8_BAR; }
	s_add_i32 s60, s88, s62
	v_lshl_add_u64 v[218:219], v[218:219], 0, s[16:17]
	s_mov_b32 m0, s60
	ds_read_b128 v[186:189], v157 offset:49152
	ds_read_b128 v[190:193], v157 offset:50176
	ds_read_b128 v[194:197], v157 offset:51200
	ds_read_b128 v[198:201], v157 offset:52224
	ds_read_b128 v[202:205], v157 offset:53248
	ds_read_b128 v[206:209], v157 offset:54272
	ds_read_b128 v[210:213], v157 offset:55296
	ds_read_b128 v[214:217], v157 offset:56320
	global_load_lds_dwordx4 v[218:219], off
	s_add_i32 m0, s60, 0x2000
	s_add_u32 s58, s58, 0x20080
	v_lshl_add_u64 v[218:219], v[220:221], 0, s[16:17]
	s_addc_u32 s59, s59, 0
	s_add_i32 s60, s89, s62
	global_load_lds_dwordx4 v[218:219], off
	v_lshl_add_u64 v[218:219], s[58:59], 0, v[132:133]
	s_mov_b32 m0, s60
	s_nop 0
	global_load_lds_dwordx4 v[218:219], off
	v_lshl_add_u64 v[218:219], s[58:59], 0, v[136:137]
	s_add_i32 m0, s60, 0x2000
	s_nop 0
	global_load_lds_dwordx4 v[218:219], off
	v_lshl_add_u64 v[218:219], v[222:223], 0, s[16:17]
	s_mov_b32 m0, s67
	s_nop 0
	global_load_lds_dwordx4 v[218:219], off
	v_lshl_add_u64 v[218:219], v[224:225], 0, s[16:17]
	s_mov_b32 m0, s68
	s_nop 0
	global_load_lds_dwordx4 v[218:219], off
	s_waitcnt vmcnt(8)
	s_waitcnt lgkmcnt(0)
	s_barrier
	v_mfma_f32_16x16x32_bf16 v[54:57], v[142:145], v[186:189], v[54:57]
	v_mfma_f32_16x16x32_bf16 v[42:45], v[162:165], v[186:189], v[42:45]
	v_mfma_f32_16x16x32_bf16 v[30:33], v[142:145], v[194:197], v[30:33]
	v_mfma_f32_16x16x32_bf16 v[26:29], v[162:165], v[194:197], v[26:29]
	v_mfma_f32_16x16x32_bf16 v[14:17], v[142:145], v[202:205], v[14:17]
	v_mfma_f32_16x16x32_bf16 v[10:13], v[162:165], v[202:205], v[10:13]
	v_mfma_f32_16x16x32_bf16 v[6:9], v[142:145], v[210:213], v[6:9]
	v_mfma_f32_16x16x32_bf16 v[2:5], v[162:165], v[210:213], v[2:5]
	v_mfma_f32_16x16x32_bf16 v[54:57], v[158:161], v[190:193], v[54:57]
	v_mfma_f32_16x16x32_bf16 v[42:45], v[166:169], v[190:193], v[42:45]
	v_mfma_f32_16x16x32_bf16 v[30:33], v[158:161], v[198:201], v[30:33]
	v_mfma_f32_16x16x32_bf16 v[26:29], v[166:169], v[198:201], v[26:29]
	v_mfma_f32_16x16x32_bf16 v[14:17], v[158:161], v[206:209], v[14:17]
	v_mfma_f32_16x16x32_bf16 v[10:13], v[166:169], v[206:209], v[10:13]
	v_mfma_f32_16x16x32_bf16 v[6:9], v[158:161], v[214:217], v[6:9]
	v_mfma_f32_16x16x32_bf16 v[2:5], v[166:169], v[214:217], v[2:5]
	v_mfma_f32_16x16x32_bf16 v[70:73], v[170:173], v[186:189], v[70:73]
	v_mfma_f32_16x16x32_bf16 v[66:69], v[178:181], v[186:189], v[66:69]
	v_mfma_f32_16x16x32_bf16 v[50:53], v[170:173], v[194:197], v[50:53]
	v_mfma_f32_16x16x32_bf16 v[46:49], v[178:181], v[194:197], v[46:49]
	v_mfma_f32_16x16x32_bf16 v[38:41], v[170:173], v[202:205], v[38:41]
	v_mfma_f32_16x16x32_bf16 v[34:37], v[178:181], v[202:205], v[34:37]
	v_mfma_f32_16x16x32_bf16 v[22:25], v[170:173], v[210:213], v[22:25]
	v_mfma_f32_16x16x32_bf16 v[18:21], v[178:181], v[210:213], v[18:21]
	v_mfma_f32_16x16x32_bf16 v[70:73], v[174:177], v[190:193], v[70:73]
	v_mfma_f32_16x16x32_bf16 v[66:69], v[182:185], v[190:193], v[66:69]
	v_mfma_f32_16x16x32_bf16 v[50:53], v[174:177], v[198:201], v[50:53]
	v_mfma_f32_16x16x32_bf16 v[46:49], v[182:185], v[198:201], v[46:49]
	v_mfma_f32_16x16x32_bf16 v[38:41], v[174:177], v[206:209], v[38:41]
	v_mfma_f32_16x16x32_bf16 v[34:37], v[182:185], v[206:209], v[34:37]
	v_mfma_f32_16x16x32_bf16 v[22:25], v[174:177], v[214:217], v[22:25]
	v_mfma_f32_16x16x32_bf16 v[18:21], v[182:185], v[214:217], v[18:21]
	s_barrier
	s_add_i32 s87, s87, 2
	s_add_u32 s85, s85, 0x100
	s_addc_u32 s86, s86, 0
	s_add_u32 s56, s56, 0x100
	s_addc_u32 s57, s57, 0
	s_cmp_gt_u32 s87, 5
	s_cbranch_scc0 .LBB0_1498
	s_and_b64 vcc, exec, s[18:19]
	s_cbranch_vccz .LBB0_1501
	s_barrier

; #define PG8_STAGE(bufoff, gbase, voff) do { _Pragma("unroll") for (int _i = 0; _i < 2; ++_i) \
;         __builtin_amdgcn_global_load_lds((const unsigned*)((const char*)(gbase) + (voff)[_i]), (PG8_LAS unsigned*)(lds + (bufoff) + ldsw + _i * 8192), 16, 0, 0); } while (0)
; #define PG8_LDA(dst, b, h) do { _Pragma("unroll") for (int m = 0; m < 4; ++m) _Pragma("unroll") for (int k = 0; k < 2; ++k) dst[m][k] = *(const PG8_LAS bf16x8*)(lds + PG8_SA(b, h) + aoff + m * 2048 + k * 1024); } while (0)
; #define PG8_LDB(dst, b, h) do { _Pragma("unroll") for (int n = 0; n < 2; ++n) _Pragma("unroll") for (int k = 0; k < 2; ++k) dst[n][k] = *(const PG8_LAS bf16x8*)(lds + PG8_SB(b, h) + boff + n * 2048 + k * 1024); } while (0)
; #define PG8_MMA(ai, bj, At, Bt) do { __builtin_amdgcn_s_setprio(1); _Pragma("unroll") for (int m = 0; m < 4; ++m) _Pragma("unroll") for (int n = 0; n < 2; ++n) _Pragma("unroll") for (int k = 0; k < 2; ++k) \
;         acc[ai][bj][m][n] = __builtin_amdgcn_mfma_f32_16x16x32_bf16(Bt[n][k], At[m][k], acc[ai][bj][m][n], 0, 0, 0); __builtin_amdgcn_s_setprio(0); } while (0)
; #define PG8_WAIT_V(n) asm volatile("s_waitcnt vmcnt(" #n ")" ::: "memory")
; #define PG8_WAIT_L(n) asm volatile("s_waitcnt lgkmcnt(" #n ")" ::: "memory")
; #define PG8_BAR __builtin_amdgcn_s_barrier()
; #define PG8_SCHED __builtin_amdgcn_sched_barrier(0)
; template <class Epi, class Sched, bool ALIGN_EPI = false>
; __device__ __forceinline__ void gemm_phase(PG8_LAS unsigned char* lds, const Gemm g, const Sched& S, const Epi& E) {
;     ...
;             PG8_LDB(B0, 0, 0); PG8_LDB(B1, 0, 1); PG8_SCHED; PG8_LDA(At, 0, 0); PG8_STAGE(PG8_SA(1, 1), a1 + hstepA, vc1);
;             PG8_WAIT_V(8); PG8_WAIT_L(0); PG8_BAR; PG8_MMA(0, 0, At, B0); PG8_MMA(0, 1, At, B1); PG8_BAR; PG8_SCHED;
;             PG8_LDA(At, 0, 1); PG8_STAGE(PG8_SB(0, 0), b2, voffB); PG8_STAGE(PG8_SB(0, 1), b2 + hstep, voffB); PG8_STAGE(PG8_SA(0, 0), a2, w0);
;             PG8_WAIT_V(8); PG8_WAIT_L(0); PG8_BAR; PG8_MMA(1, 0, At, B0); PG8_MMA(1, 1, At, B1); PG8_BAR; PG8_SCHED;
.LBB0_1601:
	ds_read_b128 v[144:147], v157
	ds_read_b128 v[160:163], v157 offset:1024
	ds_read_b128 v[164:167], v157 offset:2048
	ds_read_b128 v[168:171], v157 offset:3072
	ds_read_b128 v[172:175], v158
	ds_read_b128 v[176:179], v158 offset:1024
	ds_read_b128 v[180:183], v158 offset:2048
	ds_read_b128 v[184:187], v158 offset:3072
	s_add_u32 s54, s52, 0xfffe0080
	s_addc_u32 s55, s53, -1
	s_cmp_eq_u32 s87, 4
	s_cselect_b32 s57, s25, s55
	s_cselect_b32 s56, s43, s54
	s_cselect_b32 s55, s27, s86
	s_cselect_b32 s54, s84, s85
	v_lshl_add_u64 v[220:221], s[52:53], 0, v[142:143]
	s_add_i32 m0, s45, 0xc000
	ds_read_b128 v[188:191], v159
	ds_read_b128 v[192:195], v159 offset:1024
	ds_read_b128 v[196:199], v159 offset:2048
	ds_read_b128 v[200:203], v159 offset:3072
	ds_read_b128 v[204:207], v159 offset:4096
	ds_read_b128 v[208:211], v159 offset:5120
	ds_read_b128 v[212:215], v159 offset:6144
	ds_read_b128 v[216:219], v159 offset:7168
	global_load_lds_dwordx4 v[220:221], off
	v_lshl_add_u64 v[220:221], s[52:53], 0, v[140:141]
	s_add_i32 m0, s45, 0xe000
	s_nop 0
	global_load_lds_dwordx4 v[220:221], off
	s_waitcnt vmcnt(8)
	s_waitcnt lgkmcnt(0)
	s_barrier
	v_mfma_f32_16x16x32_bf16 v[126:129], v[144:147], v[188:191], v[126:129]
	v_mfma_f32_16x16x32_bf16 v[122:125], v[164:167], v[188:191], v[122:125]
	v_mfma_f32_16x16x32_bf16 v[114:117], v[144:147], v[196:199], v[114:117]
	v_mfma_f32_16x16x32_bf16 v[106:109], v[164:167], v[196:199], v[106:109]
	v_mfma_f32_16x16x32_bf16 v[98:101], v[144:147], v[204:207], v[98:101]
	v_mfma_f32_16x16x32_bf16 v[90:93], v[164:167], v[204:207], v[90:93]
	v_mfma_f32_16x16x32_bf16 v[82:85], v[144:147], v[212:215], v[82:85]
	v_mfma_f32_16x16x32_bf16 v[74:77], v[164:167], v[212:215], v[74:77]
	v_mfma_f32_16x16x32_bf16 v[126:129], v[160:163], v[192:195], v[126:129]
	v_mfma_f32_16x16x32_bf16 v[122:125], v[168:171], v[192:195], v[122:125]
	v_mfma_f32_16x16x32_bf16 v[114:117], v[160:163], v[200:203], v[114:117]
	v_mfma_f32_16x16x32_bf16 v[106:109], v[168:171], v[200:203], v[106:109]
	v_mfma_f32_16x16x32_bf16 v[98:101], v[160:163], v[208:211], v[98:101]
	v_mfma_f32_16x16x32_bf16 v[90:93], v[168:171], v[208:211], v[90:93]
	v_mfma_f32_16x16x32_bf16 v[82:85], v[160:163], v[216:219], v[82:85]
	v_mfma_f32_16x16x32_bf16 v[74:77], v[168:171], v[216:219], v[74:77]
	v_mfma_f32_16x16x32_bf16 v[118:121], v[172:175], v[188:191], v[118:121]
	v_mfma_f32_16x16x32_bf16 v[110:113], v[180:183], v[188:191], v[110:113]
	v_mfma_f32_16x16x32_bf16 v[102:105], v[172:175], v[196:199], v[102:105]
	v_mfma_f32_16x16x32_bf16 v[94:97], v[180:183], v[196:199], v[94:97]
	v_mfma_f32_16x16x32_bf16 v[86:89], v[172:175], v[204:207], v[86:89]
	v_mfma_f32_16x16x32_bf16 v[78:81], v[180:183], v[204:207], v[78:81]
	v_mfma_f32_16x16x32_bf16 v[62:65], v[172:175], v[212:215], v[62:65]
	v_mfma_f32_16x16x32_bf16 v[58:61], v[180:183], v[212:215], v[58:61]
	v_mfma_f32_16x16x32_bf16 v[118:121], v[176:179], v[192:195], v[118:121]
	v_mfma_f32_16x16x32_bf16 v[110:113], v[184:187], v[192:195], v[110:113]
	v_mfma_f32_16x16x32_bf16 v[102:105], v[176:179], v[200:203], v[102:105]
	v_mfma_f32_16x16x32_bf16 v[94:97], v[184:187], v[200:203], v[94:97]
	v_mfma_f32_16x16x32_bf16 v[86:89], v[176:179], v[208:211], v[86:89]
	v_mfma_f32_16x16x32_bf16 v[78:81], v[184:187], v[208:211], v[78:81]
	v_mfma_f32_16x16x32_bf16 v[62:65], v[176:179], v[216:219], v[62:65]
	v_mfma_f32_16x16x32_bf16 v[58:61], v[184:187], v[216:219], v[58:61]
	s_barrier
	s_add_i32 s88, s74, s62
	v_lshl_add_u64 v[220:221], s[54:55], 0, v[134:135]
	s_mov_b32 m0, s88
	ds_read_b128 v[188:191], v159 offset:16384
	ds_read_b128 v[192:195], v159 offset:17408
	ds_read_b128 v[196:199], v159 offset:18432
	ds_read_b128 v[200:203], v159 offset:19456
	ds_read_b128 v[204:207], v159 offset:20480
	ds_read_b128 v[208:211], v159 offset:21504
	ds_read_b128 v[212:215], v159 offset:22528
	ds_read_b128 v[216:219], v159 offset:23552
	global_load_lds_dwordx4 v[220:221], off
	s_add_i32 m0, s88, 0x2000
	s_add_u32 s88, s54, 0x20000
	v_lshl_add_u64 v[222:223], s[54:55], 0, v[138:139]
	s_addc_u32 s89, s55, 0
	s_add_i32 s90, s75, s62
	global_load_lds_dwordx4 v[222:223], off
	v_lshl_add_u64 v[224:225], s[88:89], 0, v[134:135]
	s_mov_b32 m0, s90
	v_lshl_add_u64 v[226:227], s[56:57], 0, v[136:137]
	global_load_lds_dwordx4 v[224:225], off
	v_lshl_add_u64 v[224:225], s[88:89], 0, v[138:139]
	s_add_i32 m0, s90, 0x2000
	s_nop 0
	global_load_lds_dwordx4 v[224:225], off
	v_lshl_add_u64 v[224:225], s[56:57], 0, v[132:133]
	s_mov_b32 m0, s45
	s_nop 0
	global_load_lds_dwordx4 v[224:225], off
	s_mov_b32 m0, s63
	s_nop 0
	global_load_lds_dwordx4 v[226:227], off
	s_waitcnt vmcnt(8)
	s_waitcnt lgkmcnt(0)
	s_barrier
; #define PG8_STAGE(bufoff, gbase, voff) do { _Pragma("unroll") for (int _i = 0; _i < 2; ++_i) \
;         __builtin_amdgcn_global_load_lds((const unsigned*)((const char*)(gbase) + (voff)[_i]), (PG8_LAS unsigned*)(lds + (bufoff) + ldsw + _i * 8192), 16, 0, 0); } while (0)
; #define PG8_LDA(dst, b, h) do { _Pragma("unroll") for (int m = 0; m < 4; ++m) _Pragma("unroll") for (int k = 0; k < 2; ++k) dst[m][k] = *(const PG8_LAS bf16x8*)(lds + PG8_SA(b, h) + aoff + m * 2048 + k * 1024); } while (0)
; #define PG8_LDB(dst, b, h) do { _Pragma("unroll") for (int n = 0; n < 2; ++n) _Pragma("unroll") for (int k = 0; k < 2; ++k) dst[n][k] = *(const PG8_LAS bf16x8*)(lds + PG8_SB(b, h) + boff + n * 2048 + k * 1024); } while (0)
; #define PG8_MMA(ai, bj, At, Bt) do { __builtin_amdgcn_s_setprio(1); _Pragma("unroll") for (int m = 0; m < 4; ++m) _Pragma("unroll") for (int n = 0; n < 2; ++n) _Pragma("unroll") for (int k = 0; k < 2; ++k) \
;         acc[ai][bj][m][n] = __builtin_amdgcn_mfma_f32_16x16x32_bf16(Bt[n][k], At[m][k], acc[ai][bj][m][n], 0, 0, 0); __builtin_amdgcn_s_setprio(0); } while (0)
; #define PG8_WAIT_V(n) asm volatile("s_waitcnt vmcnt(" #n ")" ::: "memory")
; #define PG8_WAIT_L(n) asm volatile("s_waitcnt lgkmcnt(" #n ")" ::: "memory")
; #define PG8_BAR __builtin_amdgcn_s_barrier()
; #define PG8_SCHED __builtin_amdgcn_sched_barrier(0)
; template <class Epi, class Sched, bool ALIGN_EPI = false>
; __device__ __forceinline__ void gemm_phase(PG8_LAS unsigned char* lds, const Gemm g, const Sched& S, const Epi& E) {
;     ...
;             PG8_WAIT_V(8); PG8_WAIT_L(0); PG8_BAR; PG8_MMA(1, 0, At, B0); PG8_MMA(1, 1, At, B1); PG8_BAR; PG8_SCHED;
;             PG8_LDB(B0, 1, 0); PG8_LDB(B1, 1, 1); PG8_SCHED; PG8_LDA(At, 1, 0); PG8_STAGE(PG8_SA(0, 1), a2 + hstepA, w1);
;             PG8_WAIT_V(8); PG8_WAIT_L(0); PG8_BAR; PG8_MMA(0, 0, At, B0); PG8_MMA(0, 1, At, B1); PG8_BAR; PG8_SCHED;
	v_mfma_f32_16x16x32_bf16 v[54:57], v[144:147], v[188:191], v[54:57]
	v_mfma_f32_16x16x32_bf16 v[42:45], v[164:167], v[188:191], v[42:45]
	v_mfma_f32_16x16x32_bf16 v[30:33], v[144:147], v[196:199], v[30:33]
	v_mfma_f32_16x16x32_bf16 v[26:29], v[164:167], v[196:199], v[26:29]
	v_mfma_f32_16x16x32_bf16 v[14:17], v[144:147], v[204:207], v[14:17]
	v_mfma_f32_16x16x32_bf16 v[10:13], v[164:167], v[204:207], v[10:13]
	v_mfma_f32_16x16x32_bf16 v[6:9], v[144:147], v[212:215], v[6:9]
	v_mfma_f32_16x16x32_bf16 v[2:5], v[164:167], v[212:215], v[2:5]
	v_mfma_f32_16x16x32_bf16 v[54:57], v[160:163], v[192:195], v[54:57]
	v_mfma_f32_16x16x32_bf16 v[42:45], v[168:171], v[192:195], v[42:45]
	v_mfma_f32_16x16x32_bf16 v[30:33], v[160:163], v[200:203], v[30:33]
	v_mfma_f32_16x16x32_bf16 v[26:29], v[168:171], v[200:203], v[26:29]
	v_mfma_f32_16x16x32_bf16 v[14:17], v[160:163], v[208:211], v[14:17]
	v_mfma_f32_16x16x32_bf16 v[10:13], v[168:171], v[208:211], v[10:13]
	v_mfma_f32_16x16x32_bf16 v[6:9], v[160:163], v[216:219], v[6:9]
	v_mfma_f32_16x16x32_bf16 v[2:5], v[168:171], v[216:219], v[2:5]
	v_mfma_f32_16x16x32_bf16 v[70:73], v[172:175], v[188:191], v[70:73]
	v_mfma_f32_16x16x32_bf16 v[66:69], v[180:183], v[188:191], v[66:69]
	v_mfma_f32_16x16x32_bf16 v[50:53], v[172:175], v[196:199], v[50:53]
	v_mfma_f32_16x16x32_bf16 v[46:49], v[180:183], v[196:199], v[46:49]
	v_mfma_f32_16x16x32_bf16 v[38:41], v[172:175], v[204:207], v[38:41]
	v_mfma_f32_16x16x32_bf16 v[34:37], v[180:183], v[204:207], v[34:37]
	v_mfma_f32_16x16x32_bf16 v[22:25], v[172:175], v[212:215], v[22:25]
	v_mfma_f32_16x16x32_bf16 v[18:21], v[180:183], v[212:215], v[18:21]
	v_mfma_f32_16x16x32_bf16 v[70:73], v[176:179], v[192:195], v[70:73]
	v_mfma_f32_16x16x32_bf16 v[66:69], v[184:187], v[192:195], v[66:69]
	v_mfma_f32_16x16x32_bf16 v[50:53], v[176:179], v[200:203], v[50:53]
	v_mfma_f32_16x16x32_bf16 v[46:49], v[184:187], v[200:203], v[46:49]
	v_mfma_f32_16x16x32_bf16 v[38:41], v[176:179], v[208:211], v[38:41]
	v_mfma_f32_16x16x32_bf16 v[34:37], v[184:187], v[208:211], v[34:37]
	v_mfma_f32_16x16x32_bf16 v[22:25], v[176:179], v[216:219], v[22:25]
	v_mfma_f32_16x16x32_bf16 v[18:21], v[184:187], v[216:219], v[18:21]
	s_barrier
	s_add_i32 s88, 0, 0x18000
	s_add_i32 s89, 0, 0x1c000
	v_add_u32_e32 v168, s88, v148
	v_add_u32_e32 v184, s89, v148
	ds_read_b128 v[144:147], v168
	ds_read_b128 v[160:163], v168 offset:1024
	ds_read_b128 v[164:167], v168 offset:2048
	ds_read_b128 v[168:171], v168 offset:3072
	ds_read_b128 v[172:175], v184
	ds_read_b128 v[176:179], v184 offset:1024
	ds_read_b128 v[180:183], v184 offset:2048
	ds_read_b128 v[184:187], v184 offset:3072
	s_add_u32 s56, s56, 0x20000
	s_addc_u32 s57, s57, 0
	s_mov_b32 m0, s64
	v_lshl_add_u64 v[228:229], s[56:57], 0, v[132:133]
	ds_read_b128 v[188:191], v159 offset:32768
	ds_read_b128 v[192:195], v159 offset:33792
	ds_read_b128 v[196:199], v159 offset:34816
	ds_read_b128 v[200:203], v159 offset:35840
	ds_read_b128 v[204:207], v159 offset:36864
	ds_read_b128 v[208:211], v159 offset:37888
	ds_read_b128 v[212:215], v159 offset:38912
	ds_read_b128 v[216:219], v159 offset:39936
	global_load_lds_dwordx4 v[228:229], off
	v_lshl_add_u64 v[228:229], s[56:57], 0, v[136:137]
	s_mov_b32 m0, s65
	s_nop 0
	global_load_lds_dwordx4 v[228:229], off
	s_waitcnt vmcnt(8)
	s_waitcnt lgkmcnt(0)
	s_barrier
	v_mfma_f32_16x16x32_bf16 v[126:129], v[144:147], v[188:191], v[126:129]
	v_mfma_f32_16x16x32_bf16 v[122:125], v[164:167], v[188:191], v[122:125]
	v_mfma_f32_16x16x32_bf16 v[114:117], v[144:147], v[196:199], v[114:117]
	v_mfma_f32_16x16x32_bf16 v[106:109], v[164:167], v[196:199], v[106:109]
	v_mfma_f32_16x16x32_bf16 v[98:101], v[144:147], v[204:207], v[98:101]
	v_mfma_f32_16x16x32_bf16 v[90:93], v[164:167], v[204:207], v[90:93]
	v_mfma_f32_16x16x32_bf16 v[82:85], v[144:147], v[212:215], v[82:85]
	v_mfma_f32_16x16x32_bf16 v[74:77], v[164:167], v[212:215], v[74:77]
	v_mfma_f32_16x16x32_bf16 v[126:129], v[160:163], v[192:195], v[126:129]
	v_mfma_f32_16x16x32_bf16 v[122:125], v[168:171], v[192:195], v[122:125]
	v_mfma_f32_16x16x32_bf16 v[114:117], v[160:163], v[200:203], v[114:117]
	v_mfma_f32_16x16x32_bf16 v[106:109], v[168:171], v[200:203], v[106:109]
	v_mfma_f32_16x16x32_bf16 v[98:101], v[160:163], v[208:211], v[98:101]
	v_mfma_f32_16x16x32_bf16 v[90:93], v[168:171], v[208:211], v[90:93]
	v_mfma_f32_16x16x32_bf16 v[82:85], v[160:163], v[216:219], v[82:85]
	v_mfma_f32_16x16x32_bf16 v[74:77], v[168:171], v[216:219], v[74:77]
	v_mfma_f32_16x16x32_bf16 v[118:121], v[172:175], v[188:191], v[118:121]
	v_mfma_f32_16x16x32_bf16 v[110:113], v[180:183], v[188:191], v[110:113]
	v_mfma_f32_16x16x32_bf16 v[102:105], v[172:175], v[196:199], v[102:105]
	v_mfma_f32_16x16x32_bf16 v[94:97], v[180:183], v[196:199], v[94:97]
	v_mfma_f32_16x16x32_bf16 v[86:89], v[172:175], v[204:207], v[86:89]
	v_mfma_f32_16x16x32_bf16 v[78:81], v[180:183], v[204:207], v[78:81]
	v_mfma_f32_16x16x32_bf16 v[62:65], v[172:175], v[212:215], v[62:65]
	v_mfma_f32_16x16x32_bf16 v[58:61], v[180:183], v[212:215], v[58:61]
	v_mfma_f32_16x16x32_bf16 v[118:121], v[176:179], v[192:195], v[118:121]
	v_mfma_f32_16x16x32_bf16 v[110:113], v[184:187], v[192:195], v[110:113]
	v_mfma_f32_16x16x32_bf16 v[102:105], v[176:179], v[200:203], v[102:105]
	v_mfma_f32_16x16x32_bf16 v[94:97], v[184:187], v[200:203], v[94:97]
	v_mfma_f32_16x16x32_bf16 v[86:89], v[176:179], v[208:211], v[86:89]
	v_mfma_f32_16x16x32_bf16 v[78:81], v[184:187], v[208:211], v[78:81]
	v_mfma_f32_16x16x32_bf16 v[62:65], v[176:179], v[216:219], v[62:65]
	v_mfma_f32_16x16x32_bf16 v[58:61], v[184:187], v[216:219], v[58:61]
	s_barrier
; #define PG8_STAGE(bufoff, gbase, voff) do { _Pragma("unroll") for (int _i = 0; _i < 2; ++_i) \
;         __builtin_amdgcn_global_load_lds((const unsigned*)((const char*)(gbase) + (voff)[_i]), (PG8_LAS unsigned*)(lds + (bufoff) + ldsw + _i * 8192), 16, 0, 0); } while (0)
; #define PG8_LDA(dst, b, h) do { _Pragma("unroll") for (int m = 0; m < 4; ++m) _Pragma("unroll") for (int k = 0; k < 2; ++k) dst[m][k] = *(const PG8_LAS bf16x8*)(lds + PG8_SA(b, h) + aoff + m * 2048 + k * 1024); } while (0)
; #define PG8_MMA(ai, bj, At, Bt) do { __builtin_amdgcn_s_setprio(1); _Pragma("unroll") for (int m = 0; m < 4; ++m) _Pragma("unroll") for (int n = 0; n < 2; ++n) _Pragma("unroll") for (int k = 0; k < 2; ++k) \
;         acc[ai][bj][m][n] = __builtin_amdgcn_mfma_f32_16x16x32_bf16(Bt[n][k], At[m][k], acc[ai][bj][m][n], 0, 0, 0); __builtin_amdgcn_s_setprio(0); } while (0)
; #define PG8_WAIT_V(n) asm volatile("s_waitcnt vmcnt(" #n ")" ::: "memory")
; #define PG8_WAIT_L(n) asm volatile("s_waitcnt lgkmcnt(" #n ")" ::: "memory")
; #define PG8_BAR __builtin_amdgcn_s_barrier()
; #define PG8_SCHED __builtin_amdgcn_sched_barrier(0)
; template <class Epi, class Sched, bool ALIGN_EPI = false>
; __device__ __forceinline__ void gemm_phase(PG8_LAS unsigned char* lds, const Gemm g, const Sched& S, const Epi& E) {
;     ...
;             PG8_LDA(At, 1, 1); PG8_STAGE(PG8_SB(1, 0), b3, voffB); PG8_STAGE(PG8_SB(1, 1), b3 + hstep, voffB); PG8_STAGE(PG8_SA(1, 0), a3, w0);
;             PG8_WAIT_V(8); PG8_WAIT_L(0); PG8_BAR; PG8_MMA(1, 0, At, B0); PG8_MMA(1, 1, At, B1); PG8_BAR; PG8_SCHED;
;             if constexpr (Epi::KSCALE) { if (((t + 2) & 7) == 0 && t + 2 < nt) { E.kscale(acc, pf, ((t + 2) >> 3) - 1, wr, fr); PG8_SCHED; } }
;         }
;         if constexpr (ALIGN_EPI) { if (wr == 0) PG8_BAR; }
	s_add_i32 s56, s88, s62
	v_lshl_add_u64 v[220:221], v[220:221], 0, s[12:13]
	s_mov_b32 m0, s56
	ds_read_b128 v[188:191], v159 offset:49152
	ds_read_b128 v[192:195], v159 offset:50176
	ds_read_b128 v[196:199], v159 offset:51200
	ds_read_b128 v[200:203], v159 offset:52224
	ds_read_b128 v[204:207], v159 offset:53248
	ds_read_b128 v[208:211], v159 offset:54272
	ds_read_b128 v[212:215], v159 offset:55296
	ds_read_b128 v[216:219], v159 offset:56320
	global_load_lds_dwordx4 v[220:221], off
	s_add_i32 m0, s56, 0x2000
	s_add_u32 s54, s54, 0x20080
	v_lshl_add_u64 v[220:221], v[222:223], 0, s[12:13]
	s_addc_u32 s55, s55, 0
	s_add_i32 s56, s89, s62
	global_load_lds_dwordx4 v[220:221], off
	v_lshl_add_u64 v[220:221], s[54:55], 0, v[134:135]
	s_mov_b32 m0, s56
	s_nop 0
	global_load_lds_dwordx4 v[220:221], off
	v_lshl_add_u64 v[220:221], s[54:55], 0, v[138:139]
	s_add_i32 m0, s56, 0x2000
	s_nop 0
	global_load_lds_dwordx4 v[220:221], off
	v_lshl_add_u64 v[220:221], v[224:225], 0, s[12:13]
	s_mov_b32 m0, s68
	s_nop 0
	global_load_lds_dwordx4 v[220:221], off
	v_lshl_add_u64 v[220:221], v[226:227], 0, s[12:13]
	s_mov_b32 m0, s69
	s_nop 0
	global_load_lds_dwordx4 v[220:221], off
	s_waitcnt vmcnt(8)
	s_waitcnt lgkmcnt(0)
	s_barrier
	v_mfma_f32_16x16x32_bf16 v[54:57], v[144:147], v[188:191], v[54:57]
	v_mfma_f32_16x16x32_bf16 v[42:45], v[164:167], v[188:191], v[42:45]
	v_mfma_f32_16x16x32_bf16 v[30:33], v[144:147], v[196:199], v[30:33]
	v_mfma_f32_16x16x32_bf16 v[26:29], v[164:167], v[196:199], v[26:29]
	v_mfma_f32_16x16x32_bf16 v[14:17], v[144:147], v[204:207], v[14:17]
	v_mfma_f32_16x16x32_bf16 v[10:13], v[164:167], v[204:207], v[10:13]
	v_mfma_f32_16x16x32_bf16 v[6:9], v[144:147], v[212:215], v[6:9]
	v_mfma_f32_16x16x32_bf16 v[2:5], v[164:167], v[212:215], v[2:5]
	v_mfma_f32_16x16x32_bf16 v[54:57], v[160:163], v[192:195], v[54:57]
	v_mfma_f32_16x16x32_bf16 v[42:45], v[168:171], v[192:195], v[42:45]
	v_mfma_f32_16x16x32_bf16 v[30:33], v[160:163], v[200:203], v[30:33]
	v_mfma_f32_16x16x32_bf16 v[26:29], v[168:171], v[200:203], v[26:29]
	v_mfma_f32_16x16x32_bf16 v[14:17], v[160:163], v[208:211], v[14:17]
	v_mfma_f32_16x16x32_bf16 v[10:13], v[168:171], v[208:211], v[10:13]
	v_mfma_f32_16x16x32_bf16 v[6:9], v[160:163], v[216:219], v[6:9]
	v_mfma_f32_16x16x32_bf16 v[2:5], v[168:171], v[216:219], v[2:5]
	v_mfma_f32_16x16x32_bf16 v[70:73], v[172:175], v[188:191], v[70:73]
	v_mfma_f32_16x16x32_bf16 v[66:69], v[180:183], v[188:191], v[66:69]
	v_mfma_f32_16x16x32_bf16 v[50:53], v[172:175], v[196:199], v[50:53]
	v_mfma_f32_16x16x32_bf16 v[46:49], v[180:183], v[196:199], v[46:49]
	v_mfma_f32_16x16x32_bf16 v[38:41], v[172:175], v[204:207], v[38:41]
	v_mfma_f32_16x16x32_bf16 v[34:37], v[180:183], v[204:207], v[34:37]
	v_mfma_f32_16x16x32_bf16 v[22:25], v[172:175], v[212:215], v[22:25]
	v_mfma_f32_16x16x32_bf16 v[18:21], v[180:183], v[212:215], v[18:21]
	v_mfma_f32_16x16x32_bf16 v[70:73], v[176:179], v[192:195], v[70:73]
	v_mfma_f32_16x16x32_bf16 v[66:69], v[184:187], v[192:195], v[66:69]
	v_mfma_f32_16x16x32_bf16 v[50:53], v[176:179], v[200:203], v[50:53]
	v_mfma_f32_16x16x32_bf16 v[46:49], v[184:187], v[200:203], v[46:49]
	v_mfma_f32_16x16x32_bf16 v[38:41], v[176:179], v[208:211], v[38:41]
	v_mfma_f32_16x16x32_bf16 v[34:37], v[184:187], v[208:211], v[34:37]
	v_mfma_f32_16x16x32_bf16 v[22:25], v[176:179], v[216:219], v[22:25]
	v_mfma_f32_16x16x32_bf16 v[18:21], v[184:187], v[216:219], v[18:21]
	s_barrier
	s_add_i32 s87, s87, 2
	s_add_u32 s85, s85, 0x100
	s_addc_u32 s86, s86, 0
	s_add_u32 s52, s52, 0x100
	s_addc_u32 s53, s53, 0
	s_cmp_gt_u32 s87, 5
	s_cbranch_scc0 .LBB0_1601
	s_and_b64 vcc, exec, s[14:15]
	s_cbranch_vccz .LBB0_1604
	s_barrier
